# GEMM main loops: 221 already-satisfied s_waitcnt lgkmcnt inside MFMA blocks and 72 adjacent s_setprio 0/1 pairs removed; on top of packed SwiGLU stack (without the conversion re-chunking)
# baseline (speedup 1.0000x reference)
; #define PG8_WAIT_V(n) asm volatile("s_waitcnt vmcnt(" #n ")" ::: "memory")
; #define PG8_WAIT_L(n) asm volatile("s_waitcnt lgkmcnt(" #n ")" ::: "memory")
; #define PG8_BAR __builtin_amdgcn_s_barrier()
; #define PG8_SCHED __builtin_amdgcn_sched_barrier(0)
; #define PG8_STAGE_A(b, h, p) do { if constexpr (GATHER) { if ((h) == 0) PG8_STAGE(PG8_SA(b, h), p, vA0); else PG8_STAGE(PG8_SA(b, h), p, vA1); } else PG8_STAGE(PG8_SA(b, h), (p) + ((h) ? hstepA : (size_t)0), voffA); } while (0)
; #define PG8_GOFF1(un, h, d) do { int tz_ = tid; asm volatile("" : "+v"(tz_)); _Pragma("unroll") for (int i_ = 0; i_ < 2; ++i_) { int R_, C_; stage_rc(tz_ * 16 + i_ * 8192, R_, C_); \
;         d[i_] = S.gather(un, R_ + (h) * HALF) + (unsigned)C_ * 2u; } } while (0)
; template <class Epi, class Sched, bool ALIGN_EPI = true, bool SP2 = true, bool FP8 = false, bool GATHER = false>
; __device__ __forceinline__ void gemm_phase(LAS unsigned char* lds, const Dims g, const Sched& S, const Epi& E, const int wv) {
;     ...
;             PG8_LDB(B0, 0, 0); PG8_LDB(B1, 0, 1); PG8_SCHED; PG8_LDA(At, 0, 0); PG8_STAGE_A(1, 1, a1);
;             if constexpr (GATHER) { if (last) PG8_GOFF1(un_, 1, vA1); }
;             PG8_WAIT_V(8); PG8_WAIT_L(0); PG8_BAR; PG8_MMA(0, 0, At, B0); PG8_MMA(0, 1, At, B1); PG8_BAR; PG8_SCHED;
;             PG8_LDA(At, 0, 1); PG8_STAGE(PG8_SB(0, 0), b2, voffB); PG8_STAGE(PG8_SB(0, 1), b2 + hstepB, voffB); PG8_STAGE_A(0, 0, a2);
.LBB0_233:
	ds_read_b128 v[146:149], v154
	ds_read_b128 v[158:161], v154 offset:1024
	ds_read_b128 v[162:165], v154 offset:2048
	ds_read_b128 v[166:169], v154 offset:3072
	ds_read_b128 v[170:173], v155
	ds_read_b128 v[174:177], v155 offset:1024
	ds_read_b128 v[178:181], v155 offset:2048
	ds_read_b128 v[182:185], v155 offset:3072
	s_add_u32 s36, s26, 0xfffc0080
	s_addc_u32 s37, s27, -1
	s_cmp_eq_u32 s21, 12
	s_cselect_b32 s39, s23, s37
	s_cselect_b32 s38, s22, s36
	s_cselect_b32 s37, s25, s17
	s_cselect_b32 s36, s24, s5
	v_lshl_add_u64 v[150:151], s[26:27], 0, v[140:141]
	s_add_i32 m0, s48, 0xc000
	ds_read_b128 v[186:189], v156
	ds_read_b128 v[190:193], v156 offset:1024
	ds_read_b128 v[194:197], v156 offset:2048
	ds_read_b128 v[198:201], v156 offset:3072
	ds_read_b128 v[202:205], v156 offset:4096
	ds_read_b128 v[206:209], v156 offset:5120
	ds_read_b128 v[210:213], v156 offset:6144
	ds_read_b128 v[214:217], v156 offset:7168
	global_load_lds_dwordx4 v[150:151], off
	v_lshl_add_u64 v[150:151], s[26:27], 0, v[138:139]
	s_add_i32 m0, s48, 0xe000
	s_nop 0
	global_load_lds_dwordx4 v[150:151], off
	s_waitcnt vmcnt(8)
	s_waitcnt lgkmcnt(0)
	s_barrier
	s_setprio 1
	v_mfma_f32_16x16x32_bf16 v[124:127], v[146:149], v[186:189], v[124:127]
	v_mfma_f32_16x16x32_bf16 v[120:123], v[162:165], v[186:189], v[120:123]
	v_mfma_f32_16x16x32_bf16 v[108:111], v[146:149], v[194:197], v[108:111]
	v_mfma_f32_16x16x32_bf16 v[104:107], v[162:165], v[194:197], v[104:107]
	v_mfma_f32_16x16x32_bf16 v[92:95], v[146:149], v[202:205], v[92:95]
	v_mfma_f32_16x16x32_bf16 v[88:91], v[162:165], v[202:205], v[88:91]
	v_mfma_f32_16x16x32_bf16 v[76:79], v[146:149], v[210:213], v[76:79]
	v_mfma_f32_16x16x32_bf16 v[72:75], v[162:165], v[210:213], v[72:75]
	v_mfma_f32_16x16x32_bf16 v[124:127], v[158:161], v[190:193], v[124:127]
	v_mfma_f32_16x16x32_bf16 v[120:123], v[166:169], v[190:193], v[120:123]
	v_mfma_f32_16x16x32_bf16 v[108:111], v[158:161], v[198:201], v[108:111]
	v_mfma_f32_16x16x32_bf16 v[104:107], v[166:169], v[198:201], v[104:107]
	v_mfma_f32_16x16x32_bf16 v[92:95], v[158:161], v[206:209], v[92:95]
	v_mfma_f32_16x16x32_bf16 v[88:91], v[166:169], v[206:209], v[88:91]
	v_mfma_f32_16x16x32_bf16 v[76:79], v[158:161], v[214:217], v[76:79]
	v_mfma_f32_16x16x32_bf16 v[72:75], v[166:169], v[214:217], v[72:75]
	v_mfma_f32_16x16x32_bf16 v[116:119], v[170:173], v[186:189], v[116:119]
	v_mfma_f32_16x16x32_bf16 v[112:115], v[178:181], v[186:189], v[112:115]
	v_mfma_f32_16x16x32_bf16 v[100:103], v[170:173], v[194:197], v[100:103]
	v_mfma_f32_16x16x32_bf16 v[96:99], v[178:181], v[194:197], v[96:99]
	v_mfma_f32_16x16x32_bf16 v[84:87], v[170:173], v[202:205], v[84:87]
	v_mfma_f32_16x16x32_bf16 v[80:83], v[178:181], v[202:205], v[80:83]
	v_mfma_f32_16x16x32_bf16 v[68:71], v[170:173], v[210:213], v[68:71]
	v_mfma_f32_16x16x32_bf16 v[64:67], v[178:181], v[210:213], v[64:67]
	v_mfma_f32_16x16x32_bf16 v[116:119], v[174:177], v[190:193], v[116:119]
	v_mfma_f32_16x16x32_bf16 v[112:115], v[182:185], v[190:193], v[112:115]
	v_mfma_f32_16x16x32_bf16 v[100:103], v[174:177], v[198:201], v[100:103]
	v_mfma_f32_16x16x32_bf16 v[96:99], v[182:185], v[198:201], v[96:99]
	v_mfma_f32_16x16x32_bf16 v[84:87], v[174:177], v[206:209], v[84:87]
	v_mfma_f32_16x16x32_bf16 v[80:83], v[182:185], v[206:209], v[80:83]
	v_mfma_f32_16x16x32_bf16 v[68:71], v[174:177], v[214:217], v[68:71]
	v_mfma_f32_16x16x32_bf16 v[64:67], v[182:185], v[214:217], v[64:67]
	s_setprio 0
	s_barrier
	s_add_i32 s63, s59, s47
	v_lshl_add_u64 v[150:151], s[36:37], 0, v[130:131]
	s_mov_b32 m0, s63
	ds_read_b128 v[186:189], v156 offset:16384
	ds_read_b128 v[190:193], v156 offset:17408
	ds_read_b128 v[194:197], v156 offset:18432
	ds_read_b128 v[198:201], v156 offset:19456
	ds_read_b128 v[202:205], v156 offset:20480
	ds_read_b128 v[206:209], v156 offset:21504
	ds_read_b128 v[210:213], v156 offset:22528
	ds_read_b128 v[214:217], v156 offset:23552
	global_load_lds_dwordx4 v[150:151], off
	s_add_i32 m0, s63, 0x2000
	s_add_u32 s64, s36, 0x40000
	v_lshl_add_u64 v[218:219], s[36:37], 0, v[134:135]
	s_addc_u32 s65, s37, 0
	s_add_i32 s63, s60, s47
	global_load_lds_dwordx4 v[218:219], off
	v_lshl_add_u64 v[220:221], s[64:65], 0, v[130:131]
	s_mov_b32 m0, s63
	v_lshl_add_u64 v[222:223], s[38:39], 0, v[132:133]
	global_load_lds_dwordx4 v[220:221], off
	v_lshl_add_u64 v[220:221], s[64:65], 0, v[134:135]
	s_add_i32 m0, s63, 0x2000
	s_nop 0
	global_load_lds_dwordx4 v[220:221], off
	v_lshl_add_u64 v[220:221], s[38:39], 0, v[128:129]
	s_mov_b32 m0, s48
	s_nop 0
	global_load_lds_dwordx4 v[220:221], off
	s_mov_b32 m0, s49
	s_nop 0
	global_load_lds_dwordx4 v[222:223], off
	s_waitcnt vmcnt(8)
	s_waitcnt lgkmcnt(0)
	s_barrier
; #define PG8_WAIT_V(n) asm volatile("s_waitcnt vmcnt(" #n ")" ::: "memory")
; #define PG8_WAIT_L(n) asm volatile("s_waitcnt lgkmcnt(" #n ")" ::: "memory")
; #define PG8_BAR __builtin_amdgcn_s_barrier()
; #define PG8_SCHED __builtin_amdgcn_sched_barrier(0)
; #define PG8_STAGE_A(b, h, p) do { if constexpr (GATHER) { if ((h) == 0) PG8_STAGE(PG8_SA(b, h), p, vA0); else PG8_STAGE(PG8_SA(b, h), p, vA1); } else PG8_STAGE(PG8_SA(b, h), (p) + ((h) ? hstepA : (size_t)0), voffA); } while (0)
; template <class Epi, class Sched, bool ALIGN_EPI = true, bool SP2 = true, bool FP8 = false, bool GATHER = false>
; __device__ __forceinline__ void gemm_phase(LAS unsigned char* lds, const Dims g, const Sched& S, const Epi& E, const int wv) {
;     ...
;             PG8_WAIT_V(8); PG8_WAIT_L(0); PG8_BAR; PG8_MMA(1, 0, At, B0); PG8_MMA(1, 1, At, B1); PG8_BAR; PG8_SCHED;
;             PG8_LDB(B0, 1, 0); PG8_LDB(B1, 1, 1); PG8_SCHED; PG8_LDA(At, 1, 0); PG8_STAGE_A(0, 1, a2);
;             PG8_WAIT_V(8); PG8_WAIT_L(0); PG8_BAR; PG8_MMA(0, 0, At, B0); PG8_MMA(0, 1, At, B1); PG8_BAR; PG8_SCHED;
;             PG8_LDA(At, 1, 1); PG8_STAGE(PG8_SB(1, 0), b3, voffB); PG8_STAGE(PG8_SB(1, 1), b3 + hstepB, voffB); PG8_STAGE_A(1, 0, a3);
	s_setprio 1
	v_mfma_f32_16x16x32_bf16 v[60:63], v[146:149], v[186:189], v[60:63]
	v_mfma_f32_16x16x32_bf16 v[56:59], v[162:165], v[186:189], v[56:59]
	v_mfma_f32_16x16x32_bf16 v[44:47], v[146:149], v[194:197], v[44:47]
	v_mfma_f32_16x16x32_bf16 v[40:43], v[162:165], v[194:197], v[40:43]
	v_mfma_f32_16x16x32_bf16 v[28:31], v[146:149], v[202:205], v[28:31]
	v_mfma_f32_16x16x32_bf16 v[24:27], v[162:165], v[202:205], v[24:27]
	v_mfma_f32_16x16x32_bf16 v[12:15], v[146:149], v[210:213], v[12:15]
	v_mfma_f32_16x16x32_bf16 v[8:11], v[162:165], v[210:213], v[8:11]
	v_mfma_f32_16x16x32_bf16 v[60:63], v[158:161], v[190:193], v[60:63]
	v_mfma_f32_16x16x32_bf16 v[56:59], v[166:169], v[190:193], v[56:59]
	v_mfma_f32_16x16x32_bf16 v[44:47], v[158:161], v[198:201], v[44:47]
	v_mfma_f32_16x16x32_bf16 v[40:43], v[166:169], v[198:201], v[40:43]
	v_mfma_f32_16x16x32_bf16 v[28:31], v[158:161], v[206:209], v[28:31]
	v_mfma_f32_16x16x32_bf16 v[24:27], v[166:169], v[206:209], v[24:27]
	v_mfma_f32_16x16x32_bf16 v[12:15], v[158:161], v[214:217], v[12:15]
	v_mfma_f32_16x16x32_bf16 v[8:11], v[166:169], v[214:217], v[8:11]
	v_mfma_f32_16x16x32_bf16 v[52:55], v[170:173], v[186:189], v[52:55]
	v_mfma_f32_16x16x32_bf16 v[48:51], v[178:181], v[186:189], v[48:51]
	v_mfma_f32_16x16x32_bf16 v[36:39], v[170:173], v[194:197], v[36:39]
	v_mfma_f32_16x16x32_bf16 v[32:35], v[178:181], v[194:197], v[32:35]
	v_mfma_f32_16x16x32_bf16 v[20:23], v[170:173], v[202:205], v[20:23]
	v_mfma_f32_16x16x32_bf16 v[16:19], v[178:181], v[202:205], v[16:19]
	v_mfma_f32_16x16x32_bf16 v[4:7], v[170:173], v[210:213], v[4:7]
	v_mfma_f32_16x16x32_bf16 v[0:3], v[178:181], v[210:213], v[0:3]
	v_mfma_f32_16x16x32_bf16 v[52:55], v[174:177], v[190:193], v[52:55]
	v_mfma_f32_16x16x32_bf16 v[48:51], v[182:185], v[190:193], v[48:51]
	v_mfma_f32_16x16x32_bf16 v[36:39], v[174:177], v[198:201], v[36:39]
	v_mfma_f32_16x16x32_bf16 v[32:35], v[182:185], v[198:201], v[32:35]
	v_mfma_f32_16x16x32_bf16 v[20:23], v[174:177], v[206:209], v[20:23]
	v_mfma_f32_16x16x32_bf16 v[16:19], v[182:185], v[206:209], v[16:19]
	v_mfma_f32_16x16x32_bf16 v[4:7], v[174:177], v[214:217], v[4:7]
	v_mfma_f32_16x16x32_bf16 v[0:3], v[182:185], v[214:217], v[0:3]
	s_setprio 0
	s_barrier
	s_add_i32 s63, 0, 0x18000
	v_add_u32_e32 v136, s63, v153
	s_add_i32 s64, 0, 0x1c000
	ds_read_b128 v[146:149], v136
	ds_read_b128 v[158:161], v136 offset:1024
	ds_read_b128 v[162:165], v136 offset:2048
	ds_read_b128 v[166:169], v136 offset:3072
	v_add_u32_e32 v136, s64, v153
	ds_read_b128 v[170:173], v136
	ds_read_b128 v[174:177], v136 offset:1024
	ds_read_b128 v[178:181], v136 offset:2048
	ds_read_b128 v[182:185], v136 offset:3072
	s_add_u32 s38, s38, 0x40000
	s_addc_u32 s39, s39, 0
	s_mov_b32 m0, s50
	v_lshl_add_u64 v[224:225], s[38:39], 0, v[128:129]
	ds_read_b128 v[186:189], v156 offset:32768
	ds_read_b128 v[190:193], v156 offset:33792
	ds_read_b128 v[194:197], v156 offset:34816
	ds_read_b128 v[198:201], v156 offset:35840
	ds_read_b128 v[202:205], v156 offset:36864
	ds_read_b128 v[206:209], v156 offset:37888
	ds_read_b128 v[210:213], v156 offset:38912
	ds_read_b128 v[214:217], v156 offset:39936
	global_load_lds_dwordx4 v[224:225], off
	v_lshl_add_u64 v[224:225], s[38:39], 0, v[132:133]
	s_mov_b32 m0, s51
	s_nop 0
	global_load_lds_dwordx4 v[224:225], off
	s_waitcnt vmcnt(8)
	s_waitcnt lgkmcnt(0)
	s_barrier
	s_setprio 1
	v_mfma_f32_16x16x32_bf16 v[124:127], v[146:149], v[186:189], v[124:127]
	v_mfma_f32_16x16x32_bf16 v[120:123], v[162:165], v[186:189], v[120:123]
	v_mfma_f32_16x16x32_bf16 v[108:111], v[146:149], v[194:197], v[108:111]
	v_mfma_f32_16x16x32_bf16 v[104:107], v[162:165], v[194:197], v[104:107]
	v_mfma_f32_16x16x32_bf16 v[92:95], v[146:149], v[202:205], v[92:95]
	v_mfma_f32_16x16x32_bf16 v[88:91], v[162:165], v[202:205], v[88:91]
	v_mfma_f32_16x16x32_bf16 v[76:79], v[146:149], v[210:213], v[76:79]
	v_mfma_f32_16x16x32_bf16 v[72:75], v[162:165], v[210:213], v[72:75]
	v_mfma_f32_16x16x32_bf16 v[124:127], v[158:161], v[190:193], v[124:127]
	v_mfma_f32_16x16x32_bf16 v[120:123], v[166:169], v[190:193], v[120:123]
	v_mfma_f32_16x16x32_bf16 v[108:111], v[158:161], v[198:201], v[108:111]
	v_mfma_f32_16x16x32_bf16 v[104:107], v[166:169], v[198:201], v[104:107]
	v_mfma_f32_16x16x32_bf16 v[92:95], v[158:161], v[206:209], v[92:95]
	v_mfma_f32_16x16x32_bf16 v[88:91], v[166:169], v[206:209], v[88:91]
	v_mfma_f32_16x16x32_bf16 v[76:79], v[158:161], v[214:217], v[76:79]
	v_mfma_f32_16x16x32_bf16 v[72:75], v[166:169], v[214:217], v[72:75]
	v_mfma_f32_16x16x32_bf16 v[116:119], v[170:173], v[186:189], v[116:119]
	v_mfma_f32_16x16x32_bf16 v[112:115], v[178:181], v[186:189], v[112:115]
	v_mfma_f32_16x16x32_bf16 v[100:103], v[170:173], v[194:197], v[100:103]
	v_mfma_f32_16x16x32_bf16 v[96:99], v[178:181], v[194:197], v[96:99]
	v_mfma_f32_16x16x32_bf16 v[84:87], v[170:173], v[202:205], v[84:87]
	v_mfma_f32_16x16x32_bf16 v[80:83], v[178:181], v[202:205], v[80:83]
	v_mfma_f32_16x16x32_bf16 v[68:71], v[170:173], v[210:213], v[68:71]
	v_mfma_f32_16x16x32_bf16 v[64:67], v[178:181], v[210:213], v[64:67]
	v_mfma_f32_16x16x32_bf16 v[116:119], v[174:177], v[190:193], v[116:119]
	v_mfma_f32_16x16x32_bf16 v[112:115], v[182:185], v[190:193], v[112:115]
	v_mfma_f32_16x16x32_bf16 v[100:103], v[174:177], v[198:201], v[100:103]
	v_mfma_f32_16x16x32_bf16 v[96:99], v[182:185], v[198:201], v[96:99]
	v_mfma_f32_16x16x32_bf16 v[84:87], v[174:177], v[206:209], v[84:87]
	v_mfma_f32_16x16x32_bf16 v[80:83], v[182:185], v[206:209], v[80:83]
	v_mfma_f32_16x16x32_bf16 v[68:71], v[174:177], v[214:217], v[68:71]
	v_mfma_f32_16x16x32_bf16 v[64:67], v[182:185], v[214:217], v[64:67]
	s_setprio 0
	s_barrier
; #define PG8_WAIT_V(n) asm volatile("s_waitcnt vmcnt(" #n ")" ::: "memory")
; #define PG8_WAIT_L(n) asm volatile("s_waitcnt lgkmcnt(" #n ")" ::: "memory")
; #define PG8_BAR __builtin_amdgcn_s_barrier()
; #define PG8_SCHED __builtin_amdgcn_sched_barrier(0)
; #define PG8_STAGE_A(b, h, p) do { if constexpr (GATHER) { if ((h) == 0) PG8_STAGE(PG8_SA(b, h), p, vA0); else PG8_STAGE(PG8_SA(b, h), p, vA1); } else PG8_STAGE(PG8_SA(b, h), (p) + ((h) ? hstepA : (size_t)0), voffA); } while (0)
; template <class Epi, class Sched, bool ALIGN_EPI = true, bool SP2 = true, bool FP8 = false, bool GATHER = false>
; __device__ __forceinline__ void gemm_phase(LAS unsigned char* lds, const Dims g, const Sched& S, const Epi& E, const int wv) {
;     ...
;             PG8_LDA(At, 1, 1); PG8_STAGE(PG8_SB(1, 0), b3, voffB); PG8_STAGE(PG8_SB(1, 1), b3 + hstepB, voffB); PG8_STAGE_A(1, 0, a3);
;             PG8_WAIT_V(8); PG8_WAIT_L(0); PG8_BAR; PG8_MMA(1, 0, At, B0); PG8_MMA(1, 1, At, B1); PG8_BAR; PG8_SCHED;
;     ...
;         if constexpr (ALIGN_EPI) { if (wr == 0) PG8_BAR; }
	s_add_i32 s38, s63, s47
	v_lshl_add_u64 v[150:151], v[150:151], 0, s[10:11]
	s_mov_b32 m0, s38
	ds_read_b128 v[186:189], v156 offset:49152
	ds_read_b128 v[190:193], v156 offset:50176
	ds_read_b128 v[194:197], v156 offset:51200
	ds_read_b128 v[198:201], v156 offset:52224
	ds_read_b128 v[202:205], v156 offset:53248
	ds_read_b128 v[206:209], v156 offset:54272
	ds_read_b128 v[210:213], v156 offset:55296
	ds_read_b128 v[214:217], v156 offset:56320
	global_load_lds_dwordx4 v[150:151], off
	s_add_i32 m0, s38, 0x2000
	s_add_u32 s36, s36, 0x40080
	v_lshl_add_u64 v[150:151], v[218:219], 0, s[10:11]
	s_addc_u32 s37, s37, 0
	s_add_i32 s38, s64, s47
	global_load_lds_dwordx4 v[150:151], off
	v_lshl_add_u64 v[150:151], s[36:37], 0, v[130:131]
	s_mov_b32 m0, s38
	s_nop 0
	global_load_lds_dwordx4 v[150:151], off
	v_lshl_add_u64 v[150:151], s[36:37], 0, v[134:135]
	s_add_i32 m0, s38, 0x2000
	s_nop 0
	global_load_lds_dwordx4 v[150:151], off
	v_lshl_add_u64 v[150:151], v[220:221], 0, s[10:11]
	s_mov_b32 m0, s55
	s_nop 0
	global_load_lds_dwordx4 v[150:151], off
	v_lshl_add_u64 v[150:151], v[222:223], 0, s[10:11]
	s_mov_b32 m0, s56
	s_nop 0
	global_load_lds_dwordx4 v[150:151], off
	s_waitcnt vmcnt(8)
	s_waitcnt lgkmcnt(0)
	s_barrier
	s_setprio 1
	v_mfma_f32_16x16x32_bf16 v[60:63], v[146:149], v[186:189], v[60:63]
	v_mfma_f32_16x16x32_bf16 v[56:59], v[162:165], v[186:189], v[56:59]
	v_mfma_f32_16x16x32_bf16 v[44:47], v[146:149], v[194:197], v[44:47]
	v_mfma_f32_16x16x32_bf16 v[40:43], v[162:165], v[194:197], v[40:43]
	v_mfma_f32_16x16x32_bf16 v[28:31], v[146:149], v[202:205], v[28:31]
	v_mfma_f32_16x16x32_bf16 v[24:27], v[162:165], v[202:205], v[24:27]
	v_mfma_f32_16x16x32_bf16 v[12:15], v[146:149], v[210:213], v[12:15]
	v_mfma_f32_16x16x32_bf16 v[8:11], v[162:165], v[210:213], v[8:11]
	v_mfma_f32_16x16x32_bf16 v[60:63], v[158:161], v[190:193], v[60:63]
	v_mfma_f32_16x16x32_bf16 v[56:59], v[166:169], v[190:193], v[56:59]
	v_mfma_f32_16x16x32_bf16 v[44:47], v[158:161], v[198:201], v[44:47]
	v_mfma_f32_16x16x32_bf16 v[40:43], v[166:169], v[198:201], v[40:43]
	v_mfma_f32_16x16x32_bf16 v[28:31], v[158:161], v[206:209], v[28:31]
	v_mfma_f32_16x16x32_bf16 v[24:27], v[166:169], v[206:209], v[24:27]
	v_mfma_f32_16x16x32_bf16 v[12:15], v[158:161], v[214:217], v[12:15]
	v_mfma_f32_16x16x32_bf16 v[8:11], v[166:169], v[214:217], v[8:11]
	v_mfma_f32_16x16x32_bf16 v[52:55], v[170:173], v[186:189], v[52:55]
	v_mfma_f32_16x16x32_bf16 v[48:51], v[178:181], v[186:189], v[48:51]
	v_mfma_f32_16x16x32_bf16 v[36:39], v[170:173], v[194:197], v[36:39]
	v_mfma_f32_16x16x32_bf16 v[32:35], v[178:181], v[194:197], v[32:35]
	v_mfma_f32_16x16x32_bf16 v[20:23], v[170:173], v[202:205], v[20:23]
	v_mfma_f32_16x16x32_bf16 v[16:19], v[178:181], v[202:205], v[16:19]
	v_mfma_f32_16x16x32_bf16 v[4:7], v[170:173], v[210:213], v[4:7]
	v_mfma_f32_16x16x32_bf16 v[0:3], v[178:181], v[210:213], v[0:3]
	v_mfma_f32_16x16x32_bf16 v[52:55], v[174:177], v[190:193], v[52:55]
	v_mfma_f32_16x16x32_bf16 v[48:51], v[182:185], v[190:193], v[48:51]
	v_mfma_f32_16x16x32_bf16 v[36:39], v[174:177], v[198:201], v[36:39]
	v_mfma_f32_16x16x32_bf16 v[32:35], v[182:185], v[198:201], v[32:35]
	v_mfma_f32_16x16x32_bf16 v[20:23], v[174:177], v[206:209], v[20:23]
	v_mfma_f32_16x16x32_bf16 v[16:19], v[182:185], v[206:209], v[16:19]
	v_mfma_f32_16x16x32_bf16 v[4:7], v[174:177], v[214:217], v[4:7]
	v_mfma_f32_16x16x32_bf16 v[0:3], v[182:185], v[214:217], v[0:3]
	s_setprio 0
	s_barrier
	s_add_i32 s21, s21, 2
	s_add_u32 s5, s5, 0x100
	s_addc_u32 s17, s17, 0
	s_add_u32 s26, s26, 0x100
	s_addc_u32 s27, s27, 0
	s_cmp_gt_u32 s21, 13
	s_cbranch_scc0 .LBB0_233
	s_and_b64 vcc, exec, s[12:13]
	s_cbranch_vccz .LBB0_236
	s_barrier

; #define PG8_WAIT_V(n) asm volatile("s_waitcnt vmcnt(" #n ")" ::: "memory")
; #define PG8_WAIT_L(n) asm volatile("s_waitcnt lgkmcnt(" #n ")" ::: "memory")
; #define PG8_BAR __builtin_amdgcn_s_barrier()
; #define PG8_SCHED __builtin_amdgcn_sched_barrier(0)
; #define PG8_STAGE_A(b, h, p) do { if constexpr (GATHER) { if ((h) == 0) PG8_STAGE(PG8_SA(b, h), p, vA0); else PG8_STAGE(PG8_SA(b, h), p, vA1); } else PG8_STAGE(PG8_SA(b, h), (p) + ((h) ? hstepA : (size_t)0), voffA); } while (0)
; #define PG8_GOFF1(un, h, d) do { int tz_ = tid; asm volatile("" : "+v"(tz_)); _Pragma("unroll") for (int i_ = 0; i_ < 2; ++i_) { int R_, C_; stage_rc(tz_ * 16 + i_ * 8192, R_, C_); \
;         d[i_] = S.gather(un, R_ + (h) * HALF) + (unsigned)C_ * 2u; } } while (0)
; template <class Epi, class Sched, bool ALIGN_EPI = true, bool SP2 = true, bool FP8 = false, bool GATHER = false>
; __device__ __forceinline__ void gemm_phase(LAS unsigned char* lds, const Dims g, const Sched& S, const Epi& E, const int wv) {
;     ...
;             const char* a1 = cA + (size_t)(t + 1) * kstep;
;             const char* a2 = last ? nA : cA + (size_t)(t + 2) * kstep; const char* b2 = last ? nB : cB + (size_t)(t + 2) * kstep;
;             const char* a3 = a2 + kstep; const char* b3 = b2 + kstep;
;             if constexpr (SP2) {
;             if constexpr (GATHER) { if (last) PG8_GOFF1(un_, 0, vA0); }
;             PG8_LDB(B0, 0, 0); PG8_LDB(B1, 0, 1); PG8_SCHED; PG8_LDA(At, 0, 0); PG8_STAGE_A(1, 1, a1);
;             if constexpr (GATHER) { if (last) PG8_GOFF1(un_, 1, vA1); }
;             PG8_WAIT_V(8); PG8_WAIT_L(0); PG8_BAR; PG8_MMA(0, 0, At, B0); PG8_MMA(0, 1, At, B1); PG8_BAR; PG8_SCHED;
;             PG8_LDA(At, 0, 1); PG8_STAGE(PG8_SB(0, 0), b2, voffB); PG8_STAGE(PG8_SB(0, 1), b2 + hstepB, voffB); PG8_STAGE_A(0, 0, a2);
.LBB0_412:
	s_add_u32 s46, s24, s40
	s_addc_u32 s47, s25, s41
	s_add_u32 s44, s46, 0x100
	s_addc_u32 s45, s47, 0
	s_and_b64 s[42:43], s[38:39], exec
	s_cselect_b32 s43, s21, s45
	s_cselect_b32 s42, s20, s44
	s_add_u32 s40, s26, s40
	s_addc_u32 s41, s27, s41
	s_add_u32 s40, s40, 0x100
	s_addc_u32 s41, s41, 0
	s_and_b64 s[38:39], s[38:39], exec
	s_cselect_b32 s45, s23, s41
	s_cselect_b32 s44, s22, s40
	s_add_u32 s48, s46, 0x10080
	ds_read_b128 v[142:145], v148
	ds_read_b128 v[152:155], v148 offset:1024
	ds_read_b128 v[156:159], v148 offset:2048
	ds_read_b128 v[160:163], v148 offset:3072
	ds_read_b128 v[164:167], v149
	ds_read_b128 v[168:171], v149 offset:1024
	ds_read_b128 v[172:175], v149 offset:2048
	ds_read_b128 v[176:179], v149 offset:3072
	s_addc_u32 s49, s47, 0
	s_add_i32 s81, s68, s56
	s_add_i32 m0, s57, 0xc000
	s_add_i32 s84, s57, 0xe000
	s_add_i32 s78, s81, 0x2000
	s_add_u32 s46, s44, 0x10000
	s_addc_u32 s47, s45, 0
	s_add_i32 s80, s69, s56
	s_add_i32 s79, s80, 0x2000
	s_add_i32 s77, 0, 0x18000
	s_add_i32 s76, 0, 0x1c000
	s_add_u32 s40, s42, 0x10000
	s_addc_u32 s41, s43, 0
	s_add_i32 s75, s77, s56
	s_add_i32 s74, s75, 0x2000
	s_add_u32 s38, s44, 0x10080
	s_addc_u32 s39, s45, 0
	s_add_i32 s83, s76, s56
	s_add_i32 s82, s83, 0x2000
	v_lshl_add_u64 v[212:213], s[48:49], 0, v[128:129]
	ds_read_b128 v[180:183], v150
	ds_read_b128 v[184:187], v150 offset:1024
	ds_read_b128 v[188:191], v150 offset:2048
	ds_read_b128 v[192:195], v150 offset:3072
	ds_read_b128 v[196:199], v150 offset:4096
	ds_read_b128 v[200:203], v150 offset:5120
	ds_read_b128 v[204:207], v150 offset:6144
	ds_read_b128 v[208:211], v150 offset:7168
	global_load_lds_dwordx4 v[212:213], off
	v_lshl_add_u64 v[212:213], s[48:49], 0, v[132:133]
	s_mov_b32 m0, s84
	s_nop 0
	global_load_lds_dwordx4 v[212:213], off
	s_waitcnt vmcnt(8)
	s_waitcnt lgkmcnt(0)
	s_barrier
	s_setprio 1
	v_mfma_f32_16x16x32_bf16 v[124:127], v[142:145], v[180:183], v[124:127]
	v_mfma_f32_16x16x32_bf16 v[120:123], v[156:159], v[180:183], v[120:123]
	v_mfma_f32_16x16x32_bf16 v[108:111], v[142:145], v[188:191], v[108:111]
	v_mfma_f32_16x16x32_bf16 v[104:107], v[156:159], v[188:191], v[104:107]
	v_mfma_f32_16x16x32_bf16 v[92:95], v[142:145], v[196:199], v[92:95]
	v_mfma_f32_16x16x32_bf16 v[88:91], v[156:159], v[196:199], v[88:91]
	v_mfma_f32_16x16x32_bf16 v[76:79], v[142:145], v[204:207], v[76:79]
	v_mfma_f32_16x16x32_bf16 v[72:75], v[156:159], v[204:207], v[72:75]
	v_mfma_f32_16x16x32_bf16 v[124:127], v[152:155], v[184:187], v[124:127]
	v_mfma_f32_16x16x32_bf16 v[120:123], v[160:163], v[184:187], v[120:123]
	v_mfma_f32_16x16x32_bf16 v[108:111], v[152:155], v[192:195], v[108:111]
	v_mfma_f32_16x16x32_bf16 v[104:107], v[160:163], v[192:195], v[104:107]
	v_mfma_f32_16x16x32_bf16 v[92:95], v[152:155], v[200:203], v[92:95]
	v_mfma_f32_16x16x32_bf16 v[88:91], v[160:163], v[200:203], v[88:91]
	v_mfma_f32_16x16x32_bf16 v[76:79], v[152:155], v[208:211], v[76:79]
	v_mfma_f32_16x16x32_bf16 v[72:75], v[160:163], v[208:211], v[72:75]
	v_mfma_f32_16x16x32_bf16 v[116:119], v[164:167], v[180:183], v[116:119]
	v_mfma_f32_16x16x32_bf16 v[112:115], v[172:175], v[180:183], v[112:115]
	v_mfma_f32_16x16x32_bf16 v[100:103], v[164:167], v[188:191], v[100:103]
	v_mfma_f32_16x16x32_bf16 v[96:99], v[172:175], v[188:191], v[96:99]
	v_mfma_f32_16x16x32_bf16 v[84:87], v[164:167], v[196:199], v[84:87]
	v_mfma_f32_16x16x32_bf16 v[80:83], v[172:175], v[196:199], v[80:83]
	v_mfma_f32_16x16x32_bf16 v[68:71], v[164:167], v[204:207], v[68:71]
	v_mfma_f32_16x16x32_bf16 v[64:67], v[172:175], v[204:207], v[64:67]
	v_mfma_f32_16x16x32_bf16 v[116:119], v[168:171], v[184:187], v[116:119]
	v_mfma_f32_16x16x32_bf16 v[112:115], v[176:179], v[184:187], v[112:115]
	v_mfma_f32_16x16x32_bf16 v[100:103], v[168:171], v[192:195], v[100:103]
	v_mfma_f32_16x16x32_bf16 v[96:99], v[176:179], v[192:195], v[96:99]
	v_mfma_f32_16x16x32_bf16 v[84:87], v[168:171], v[200:203], v[84:87]
	v_mfma_f32_16x16x32_bf16 v[80:83], v[176:179], v[200:203], v[80:83]
	v_mfma_f32_16x16x32_bf16 v[68:71], v[168:171], v[208:211], v[68:71]
	v_mfma_f32_16x16x32_bf16 v[64:67], v[176:179], v[208:211], v[64:67]
	s_setprio 0
	s_barrier
	s_mov_b32 m0, s81
	v_lshl_add_u64 v[212:213], s[44:45], 0, v[130:131]
	ds_read_b128 v[180:183], v150 offset:16384
	ds_read_b128 v[184:187], v150 offset:17408
	ds_read_b128 v[188:191], v150 offset:18432
	ds_read_b128 v[192:195], v150 offset:19456
	ds_read_b128 v[196:199], v150 offset:20480
	ds_read_b128 v[200:203], v150 offset:21504
	ds_read_b128 v[204:207], v150 offset:22528
	ds_read_b128 v[208:211], v150 offset:23552
	global_load_lds_dwordx4 v[212:213], off
	v_lshl_add_u64 v[214:215], s[44:45], 0, v[134:135]
	s_mov_b32 m0, s78
	v_lshl_add_u64 v[216:217], s[46:47], 0, v[130:131]
	global_load_lds_dwordx4 v[214:215], off
	s_mov_b32 m0, s80
	v_lshl_add_u64 v[218:219], s[42:43], 0, v[132:133]
	global_load_lds_dwordx4 v[216:217], off
	v_lshl_add_u64 v[216:217], s[46:47], 0, v[134:135]
	s_mov_b32 m0, s79
	s_nop 0
	global_load_lds_dwordx4 v[216:217], off
	v_lshl_add_u64 v[216:217], s[42:43], 0, v[128:129]
	s_mov_b32 m0, s57
	s_nop 0
	global_load_lds_dwordx4 v[216:217], off
	s_mov_b32 m0, s58
	s_nop 0
	global_load_lds_dwordx4 v[218:219], off
	s_waitcnt vmcnt(8)
	s_waitcnt lgkmcnt(0)
	s_barrier
; #define PG8_WAIT_V(n) asm volatile("s_waitcnt vmcnt(" #n ")" ::: "memory")
; #define PG8_WAIT_L(n) asm volatile("s_waitcnt lgkmcnt(" #n ")" ::: "memory")
; #define PG8_BAR __builtin_amdgcn_s_barrier()
; #define PG8_SCHED __builtin_amdgcn_sched_barrier(0)
; #define PG8_STAGE_A(b, h, p) do { if constexpr (GATHER) { if ((h) == 0) PG8_STAGE(PG8_SA(b, h), p, vA0); else PG8_STAGE(PG8_SA(b, h), p, vA1); } else PG8_STAGE(PG8_SA(b, h), (p) + ((h) ? hstepA : (size_t)0), voffA); } while (0)
; template <class Epi, class Sched, bool ALIGN_EPI = true, bool SP2 = true, bool FP8 = false, bool GATHER = false>
; __device__ __forceinline__ void gemm_phase(LAS unsigned char* lds, const Dims g, const Sched& S, const Epi& E, const int wv) {
;     ...
;             PG8_WAIT_V(8); PG8_WAIT_L(0); PG8_BAR; PG8_MMA(1, 0, At, B0); PG8_MMA(1, 1, At, B1); PG8_BAR; PG8_SCHED;
;             PG8_LDB(B0, 1, 0); PG8_LDB(B1, 1, 1); PG8_SCHED; PG8_LDA(At, 1, 0); PG8_STAGE_A(0, 1, a2);
;             PG8_WAIT_V(8); PG8_WAIT_L(0); PG8_BAR; PG8_MMA(0, 0, At, B0); PG8_MMA(0, 1, At, B1); PG8_BAR; PG8_SCHED;
;             PG8_LDA(At, 1, 1); PG8_STAGE(PG8_SB(1, 0), b3, voffB); PG8_STAGE(PG8_SB(1, 1), b3 + hstepB, voffB); PG8_STAGE_A(1, 0, a3);
	s_setprio 1
	v_mfma_f32_16x16x32_bf16 v[60:63], v[142:145], v[180:183], v[60:63]
	v_mfma_f32_16x16x32_bf16 v[56:59], v[156:159], v[180:183], v[56:59]
	v_mfma_f32_16x16x32_bf16 v[44:47], v[142:145], v[188:191], v[44:47]
	v_mfma_f32_16x16x32_bf16 v[40:43], v[156:159], v[188:191], v[40:43]
	v_mfma_f32_16x16x32_bf16 v[28:31], v[142:145], v[196:199], v[28:31]
	v_mfma_f32_16x16x32_bf16 v[24:27], v[156:159], v[196:199], v[24:27]
	v_mfma_f32_16x16x32_bf16 v[12:15], v[142:145], v[204:207], v[12:15]
	v_mfma_f32_16x16x32_bf16 v[8:11], v[156:159], v[204:207], v[8:11]
	v_mfma_f32_16x16x32_bf16 v[60:63], v[152:155], v[184:187], v[60:63]
	v_mfma_f32_16x16x32_bf16 v[56:59], v[160:163], v[184:187], v[56:59]
	v_mfma_f32_16x16x32_bf16 v[44:47], v[152:155], v[192:195], v[44:47]
	v_mfma_f32_16x16x32_bf16 v[40:43], v[160:163], v[192:195], v[40:43]
	v_mfma_f32_16x16x32_bf16 v[28:31], v[152:155], v[200:203], v[28:31]
	v_mfma_f32_16x16x32_bf16 v[24:27], v[160:163], v[200:203], v[24:27]
	v_mfma_f32_16x16x32_bf16 v[12:15], v[152:155], v[208:211], v[12:15]
	v_mfma_f32_16x16x32_bf16 v[8:11], v[160:163], v[208:211], v[8:11]
	v_mfma_f32_16x16x32_bf16 v[52:55], v[164:167], v[180:183], v[52:55]
	v_mfma_f32_16x16x32_bf16 v[48:51], v[172:175], v[180:183], v[48:51]
	v_mfma_f32_16x16x32_bf16 v[36:39], v[164:167], v[188:191], v[36:39]
	v_mfma_f32_16x16x32_bf16 v[32:35], v[172:175], v[188:191], v[32:35]
	v_mfma_f32_16x16x32_bf16 v[20:23], v[164:167], v[196:199], v[20:23]
	v_mfma_f32_16x16x32_bf16 v[16:19], v[172:175], v[196:199], v[16:19]
	v_mfma_f32_16x16x32_bf16 v[4:7], v[164:167], v[204:207], v[4:7]
	v_mfma_f32_16x16x32_bf16 v[0:3], v[172:175], v[204:207], v[0:3]
	v_mfma_f32_16x16x32_bf16 v[52:55], v[168:171], v[184:187], v[52:55]
	v_mfma_f32_16x16x32_bf16 v[48:51], v[176:179], v[184:187], v[48:51]
	v_mfma_f32_16x16x32_bf16 v[36:39], v[168:171], v[192:195], v[36:39]
	v_mfma_f32_16x16x32_bf16 v[32:35], v[176:179], v[192:195], v[32:35]
	v_mfma_f32_16x16x32_bf16 v[20:23], v[168:171], v[200:203], v[20:23]
	v_mfma_f32_16x16x32_bf16 v[16:19], v[176:179], v[200:203], v[16:19]
	v_mfma_f32_16x16x32_bf16 v[4:7], v[168:171], v[208:211], v[4:7]
	v_mfma_f32_16x16x32_bf16 v[0:3], v[176:179], v[208:211], v[0:3]
	s_setprio 0
	s_barrier
	v_add_u32_e32 v136, s77, v147
	ds_read_b128 v[142:145], v136
	ds_read_b128 v[152:155], v136 offset:1024
	ds_read_b128 v[156:159], v136 offset:2048
	ds_read_b128 v[160:163], v136 offset:3072
	v_add_u32_e32 v136, s76, v147
	ds_read_b128 v[164:167], v136
	ds_read_b128 v[168:171], v136 offset:1024
	ds_read_b128 v[172:175], v136 offset:2048
	ds_read_b128 v[176:179], v136 offset:3072
	s_mov_b32 m0, s59
	v_lshl_add_u64 v[220:221], s[40:41], 0, v[128:129]
	ds_read_b128 v[180:183], v150 offset:32768
	ds_read_b128 v[184:187], v150 offset:33792
	ds_read_b128 v[188:191], v150 offset:34816
	ds_read_b128 v[192:195], v150 offset:35840
	ds_read_b128 v[196:199], v150 offset:36864
	ds_read_b128 v[200:203], v150 offset:37888
	ds_read_b128 v[204:207], v150 offset:38912
	ds_read_b128 v[208:211], v150 offset:39936
	global_load_lds_dwordx4 v[220:221], off
	v_lshl_add_u64 v[220:221], s[40:41], 0, v[132:133]
	s_mov_b32 m0, s60
	s_nop 0
	global_load_lds_dwordx4 v[220:221], off
	s_waitcnt vmcnt(8)
	s_waitcnt lgkmcnt(0)
	s_barrier
	s_setprio 1
	v_mfma_f32_16x16x32_bf16 v[124:127], v[142:145], v[180:183], v[124:127]
	v_mfma_f32_16x16x32_bf16 v[120:123], v[156:159], v[180:183], v[120:123]
	v_mfma_f32_16x16x32_bf16 v[108:111], v[142:145], v[188:191], v[108:111]
	v_mfma_f32_16x16x32_bf16 v[104:107], v[156:159], v[188:191], v[104:107]
	v_mfma_f32_16x16x32_bf16 v[92:95], v[142:145], v[196:199], v[92:95]
	v_mfma_f32_16x16x32_bf16 v[88:91], v[156:159], v[196:199], v[88:91]
	v_mfma_f32_16x16x32_bf16 v[76:79], v[142:145], v[204:207], v[76:79]
	v_mfma_f32_16x16x32_bf16 v[72:75], v[156:159], v[204:207], v[72:75]
	v_mfma_f32_16x16x32_bf16 v[124:127], v[152:155], v[184:187], v[124:127]
	v_mfma_f32_16x16x32_bf16 v[120:123], v[160:163], v[184:187], v[120:123]
	v_mfma_f32_16x16x32_bf16 v[108:111], v[152:155], v[192:195], v[108:111]
	v_mfma_f32_16x16x32_bf16 v[104:107], v[160:163], v[192:195], v[104:107]
	v_mfma_f32_16x16x32_bf16 v[92:95], v[152:155], v[200:203], v[92:95]
	v_mfma_f32_16x16x32_bf16 v[88:91], v[160:163], v[200:203], v[88:91]
	v_mfma_f32_16x16x32_bf16 v[76:79], v[152:155], v[208:211], v[76:79]
	v_mfma_f32_16x16x32_bf16 v[72:75], v[160:163], v[208:211], v[72:75]
	v_mfma_f32_16x16x32_bf16 v[116:119], v[164:167], v[180:183], v[116:119]
	v_mfma_f32_16x16x32_bf16 v[112:115], v[172:175], v[180:183], v[112:115]
	v_mfma_f32_16x16x32_bf16 v[100:103], v[164:167], v[188:191], v[100:103]
	v_mfma_f32_16x16x32_bf16 v[96:99], v[172:175], v[188:191], v[96:99]
	v_mfma_f32_16x16x32_bf16 v[84:87], v[164:167], v[196:199], v[84:87]
	v_mfma_f32_16x16x32_bf16 v[80:83], v[172:175], v[196:199], v[80:83]
	v_mfma_f32_16x16x32_bf16 v[68:71], v[164:167], v[204:207], v[68:71]
	v_mfma_f32_16x16x32_bf16 v[64:67], v[172:175], v[204:207], v[64:67]
	v_mfma_f32_16x16x32_bf16 v[116:119], v[168:171], v[184:187], v[116:119]
	v_mfma_f32_16x16x32_bf16 v[112:115], v[176:179], v[184:187], v[112:115]
	v_mfma_f32_16x16x32_bf16 v[100:103], v[168:171], v[192:195], v[100:103]
	v_mfma_f32_16x16x32_bf16 v[96:99], v[176:179], v[192:195], v[96:99]
	v_mfma_f32_16x16x32_bf16 v[84:87], v[168:171], v[200:203], v[84:87]
	v_mfma_f32_16x16x32_bf16 v[80:83], v[176:179], v[200:203], v[80:83]
	v_mfma_f32_16x16x32_bf16 v[68:71], v[168:171], v[208:211], v[68:71]
	v_mfma_f32_16x16x32_bf16 v[64:67], v[176:179], v[208:211], v[64:67]
	s_setprio 0
	s_barrier
; #define PG8_WAIT_V(n) asm volatile("s_waitcnt vmcnt(" #n ")" ::: "memory")
; #define PG8_WAIT_L(n) asm volatile("s_waitcnt lgkmcnt(" #n ")" ::: "memory")
; #define PG8_BAR __builtin_amdgcn_s_barrier()
; #define PG8_SCHED __builtin_amdgcn_sched_barrier(0)
; #define PG8_STAGE_A(b, h, p) do { if constexpr (GATHER) { if ((h) == 0) PG8_STAGE(PG8_SA(b, h), p, vA0); else PG8_STAGE(PG8_SA(b, h), p, vA1); } else PG8_STAGE(PG8_SA(b, h), (p) + ((h) ? hstepA : (size_t)0), voffA); } while (0)
; template <class Epi, class Sched, bool ALIGN_EPI = true, bool SP2 = true, bool FP8 = false, bool GATHER = false>
; __device__ __forceinline__ void gemm_phase(LAS unsigned char* lds, const Dims g, const Sched& S, const Epi& E, const int wv) {
;     ...
;             PG8_LDA(At, 1, 1); PG8_STAGE(PG8_SB(1, 0), b3, voffB); PG8_STAGE(PG8_SB(1, 1), b3 + hstepB, voffB); PG8_STAGE_A(1, 0, a3);
;             PG8_WAIT_V(8); PG8_WAIT_L(0); PG8_BAR; PG8_MMA(1, 0, At, B0); PG8_MMA(1, 1, At, B1); PG8_BAR; PG8_SCHED;
	s_mov_b32 m0, s75
	v_lshl_add_u64 v[212:213], v[212:213], 0, s[12:13]
	ds_read_b128 v[180:183], v150 offset:49152
	ds_read_b128 v[184:187], v150 offset:50176
	ds_read_b128 v[188:191], v150 offset:51200
	ds_read_b128 v[192:195], v150 offset:52224
	ds_read_b128 v[196:199], v150 offset:53248
	ds_read_b128 v[200:203], v150 offset:54272
	ds_read_b128 v[204:207], v150 offset:55296
	ds_read_b128 v[208:211], v150 offset:56320
	global_load_lds_dwordx4 v[212:213], off
	v_lshl_add_u64 v[212:213], v[214:215], 0, s[12:13]
	s_mov_b32 m0, s74
	s_nop 0
	global_load_lds_dwordx4 v[212:213], off
	v_lshl_add_u64 v[212:213], s[38:39], 0, v[130:131]
	s_mov_b32 m0, s83
	s_nop 0
	global_load_lds_dwordx4 v[212:213], off
	v_lshl_add_u64 v[212:213], s[38:39], 0, v[134:135]
	s_mov_b32 m0, s82
	s_nop 0
	global_load_lds_dwordx4 v[212:213], off
	v_lshl_add_u64 v[212:213], v[216:217], 0, s[12:13]
	s_mov_b32 m0, s63
	s_nop 0
	global_load_lds_dwordx4 v[212:213], off
	v_lshl_add_u64 v[212:213], v[218:219], 0, s[12:13]
	s_mov_b32 m0, s64
	s_nop 0
	global_load_lds_dwordx4 v[212:213], off
	s_waitcnt vmcnt(8)
	s_waitcnt lgkmcnt(0)
	s_barrier
	s_setprio 1
	v_mfma_f32_16x16x32_bf16 v[60:63], v[142:145], v[180:183], v[60:63]
	v_mfma_f32_16x16x32_bf16 v[56:59], v[156:159], v[180:183], v[56:59]
	v_mfma_f32_16x16x32_bf16 v[44:47], v[142:145], v[188:191], v[44:47]
	v_mfma_f32_16x16x32_bf16 v[40:43], v[156:159], v[188:191], v[40:43]
	v_mfma_f32_16x16x32_bf16 v[28:31], v[142:145], v[196:199], v[28:31]
	v_mfma_f32_16x16x32_bf16 v[24:27], v[156:159], v[196:199], v[24:27]
	v_mfma_f32_16x16x32_bf16 v[12:15], v[142:145], v[204:207], v[12:15]
	v_mfma_f32_16x16x32_bf16 v[8:11], v[156:159], v[204:207], v[8:11]
	v_mfma_f32_16x16x32_bf16 v[60:63], v[152:155], v[184:187], v[60:63]
	v_mfma_f32_16x16x32_bf16 v[56:59], v[160:163], v[184:187], v[56:59]
	v_mfma_f32_16x16x32_bf16 v[44:47], v[152:155], v[192:195], v[44:47]
	v_mfma_f32_16x16x32_bf16 v[40:43], v[160:163], v[192:195], v[40:43]
	v_mfma_f32_16x16x32_bf16 v[28:31], v[152:155], v[200:203], v[28:31]
	v_mfma_f32_16x16x32_bf16 v[24:27], v[160:163], v[200:203], v[24:27]
	v_mfma_f32_16x16x32_bf16 v[12:15], v[152:155], v[208:211], v[12:15]
	v_mfma_f32_16x16x32_bf16 v[8:11], v[160:163], v[208:211], v[8:11]
	v_mfma_f32_16x16x32_bf16 v[52:55], v[164:167], v[180:183], v[52:55]
	v_mfma_f32_16x16x32_bf16 v[48:51], v[172:175], v[180:183], v[48:51]
	v_mfma_f32_16x16x32_bf16 v[36:39], v[164:167], v[188:191], v[36:39]
	v_mfma_f32_16x16x32_bf16 v[32:35], v[172:175], v[188:191], v[32:35]
	v_mfma_f32_16x16x32_bf16 v[20:23], v[164:167], v[196:199], v[20:23]
	v_mfma_f32_16x16x32_bf16 v[16:19], v[172:175], v[196:199], v[16:19]
	v_mfma_f32_16x16x32_bf16 v[4:7], v[164:167], v[204:207], v[4:7]
	v_mfma_f32_16x16x32_bf16 v[0:3], v[172:175], v[204:207], v[0:3]
	v_mfma_f32_16x16x32_bf16 v[52:55], v[168:171], v[184:187], v[52:55]
	v_mfma_f32_16x16x32_bf16 v[48:51], v[176:179], v[184:187], v[48:51]
	v_mfma_f32_16x16x32_bf16 v[36:39], v[168:171], v[192:195], v[36:39]
	v_mfma_f32_16x16x32_bf16 v[32:35], v[176:179], v[192:195], v[32:35]
	v_mfma_f32_16x16x32_bf16 v[20:23], v[168:171], v[200:203], v[20:23]
	v_mfma_f32_16x16x32_bf16 v[16:19], v[176:179], v[200:203], v[16:19]
	v_mfma_f32_16x16x32_bf16 v[4:7], v[168:171], v[208:211], v[4:7]
	v_mfma_f32_16x16x32_bf16 v[0:3], v[176:179], v[208:211], v[0:3]
	s_setprio 0
	s_barrier
	s_andn2_b64 vcc, exec, s[36:37]
	s_mov_b64 s[38:39], -1
	s_mov_b64 s[36:37], 0
	s_mov_b64 s[40:41], 0x100
	s_cbranch_vccz .LBB0_412
	s_and_b64 vcc, exec, s[14:15]
	s_cbranch_vccz .LBB0_415
	s_barrier

; #define PG8_WAIT_V(n) asm volatile("s_waitcnt vmcnt(" #n ")" ::: "memory")
; #define PG8_WAIT_L(n) asm volatile("s_waitcnt lgkmcnt(" #n ")" ::: "memory")
; #define PG8_BAR __builtin_amdgcn_s_barrier()
; #define PG8_SCHED __builtin_amdgcn_sched_barrier(0)
; #define PG8_STAGE_A(b, h, p) do { if constexpr (GATHER) { if ((h) == 0) PG8_STAGE(PG8_SA(b, h), p, vA0); else PG8_STAGE(PG8_SA(b, h), p, vA1); } else PG8_STAGE(PG8_SA(b, h), (p) + ((h) ? hstepA : (size_t)0), voffA); } while (0)
; #define PG8_GOFF1(un, h, d) do { int tz_ = tid; asm volatile("" : "+v"(tz_)); _Pragma("unroll") for (int i_ = 0; i_ < 2; ++i_) { int R_, C_; stage_rc(tz_ * 16 + i_ * 8192, R_, C_); \
;         d[i_] = S.gather(un, R_ + (h) * HALF) + (unsigned)C_ * 2u; } } while (0)
; template <class Epi, class Sched, bool ALIGN_EPI = true, bool SP2 = true, bool FP8 = false, bool GATHER = false>
; __device__ __forceinline__ void gemm_phase(LAS unsigned char* lds, const Dims g, const Sched& S, const Epi& E, const int wv) {
;     ...
;             PG8_LDB(B0, 0, 0); PG8_LDB(B1, 0, 1); PG8_SCHED; PG8_LDA(At, 0, 0); PG8_STAGE_A(1, 1, a1);
;             if constexpr (GATHER) { if (last) PG8_GOFF1(un_, 1, vA1); }
;             PG8_WAIT_V(8); PG8_WAIT_L(0); PG8_BAR; PG8_MMA(0, 0, At, B0); PG8_MMA(0, 1, At, B1); PG8_BAR; PG8_SCHED;
;             PG8_LDA(At, 0, 1); PG8_STAGE(PG8_SB(0, 0), b2, voffB); PG8_STAGE(PG8_SB(0, 1), b2 + hstepB, voffB); PG8_STAGE_A(0, 0, a2);
;             PG8_WAIT_V(8); PG8_WAIT_L(0); PG8_BAR; PG8_MMA(1, 0, At, B0); PG8_MMA(1, 1, At, B1); PG8_BAR; PG8_SCHED;
.LBB0_745:
	ds_read_b128 v[128:131], v169
	ds_read_b128 v[132:135], v169 offset:1024
	ds_read_b128 v[136:139], v169 offset:2048
	ds_read_b128 v[140:143], v169 offset:3072
	ds_read_b128 v[144:147], v170
	ds_read_b128 v[148:151], v170 offset:1024
	ds_read_b128 v[156:159], v170 offset:2048
	ds_read_b128 v[160:163], v170 offset:3072
	s_cmp_eq_u32 s82, 4
	s_cselect_b32 s50, s40, s39
	s_cselect_b32 s51, s41, s81
	s_cselect_b32 s48, s42, s5
	s_cselect_b32 s49, s43, s37
	s_add_u32 s46, s50, 0x80
	s_addc_u32 s47, s51, 0
	ds_read_b128 v[176:179], v171
	ds_read_b128 v[180:183], v171 offset:1024
	ds_read_b128 v[184:187], v171 offset:2048
	ds_read_b128 v[188:191], v171 offset:3072
	ds_read_b128 v[192:195], v171 offset:4096
	ds_read_b128 v[196:199], v171 offset:5120
	ds_read_b128 v[200:203], v171 offset:6144
	ds_read_b128 v[204:207], v171 offset:7168
	s_mov_b32 m0, s77
	s_nop 0
	global_load_lds_dwordx4 v165, s[44:45]
	s_nop 0
	s_mov_b32 m0, s78
	s_nop 0
	global_load_lds_dwordx4 v167, s[44:45]
	s_waitcnt vmcnt(8)
	s_waitcnt lgkmcnt(0)
	s_barrier
	s_setprio 1
	v_mfma_scale_f32_16x16x128_f8f6f4 v[124:127], v[128:135], v[176:183], v[124:127], v172, v172 op_sel_hi:[0,0,0]
	v_mfma_scale_f32_16x16x128_f8f6f4 v[120:123], v[136:143], v[176:183], v[120:123], v172, v172 op_sel_hi:[0,0,0]
	v_mfma_scale_f32_16x16x128_f8f6f4 v[108:111], v[128:135], v[184:191], v[108:111], v172, v172 op_sel_hi:[0,0,0]
	v_mfma_scale_f32_16x16x128_f8f6f4 v[104:107], v[136:143], v[184:191], v[104:107], v172, v172 op_sel_hi:[0,0,0]
	v_mfma_scale_f32_16x16x128_f8f6f4 v[208:211], v[128:135], v[192:199], v[92:95], v172, v172 op_sel_hi:[0,0,0]
	v_mfma_scale_f32_16x16x128_f8f6f4 v[212:215], v[136:143], v[192:199], v[88:91], v172, v172 op_sel_hi:[0,0,0]
	v_mfma_scale_f32_16x16x128_f8f6f4 v[216:219], v[128:135], v[200:207], v[76:79], v172, v172 op_sel_hi:[0,0,0]
	v_mfma_scale_f32_16x16x128_f8f6f4 v[220:223], v[136:143], v[200:207], v[72:75], v172, v172 op_sel_hi:[0,0,0]
	v_mfma_scale_f32_16x16x128_f8f6f4 v[116:119], v[144:151], v[176:183], v[116:119], v172, v172 op_sel_hi:[0,0,0]
	v_mfma_scale_f32_16x16x128_f8f6f4 v[112:115], v[156:163], v[176:183], v[112:115], v172, v172 op_sel_hi:[0,0,0]
	v_mfma_scale_f32_16x16x128_f8f6f4 v[100:103], v[144:151], v[184:191], v[100:103], v172, v172 op_sel_hi:[0,0,0]
	v_mfma_scale_f32_16x16x128_f8f6f4 v[96:99], v[156:163], v[184:191], v[96:99], v172, v172 op_sel_hi:[0,0,0]
	v_mfma_scale_f32_16x16x128_f8f6f4 v[176:179], v[144:151], v[192:199], v[84:87], v172, v172 op_sel_hi:[0,0,0]
	v_mfma_scale_f32_16x16x128_f8f6f4 v[180:183], v[156:163], v[192:199], v[80:83], v172, v172 op_sel_hi:[0,0,0]
	v_mfma_scale_f32_16x16x128_f8f6f4 v[184:187], v[144:151], v[200:207], v[68:71], v172, v172 op_sel_hi:[0,0,0]
	v_mfma_scale_f32_16x16x128_f8f6f4 v[188:191], v[156:163], v[200:207], v[64:67], v172, v172 op_sel_hi:[0,0,0]
	s_setprio 0
	s_barrier
	s_nop 4
	ds_read_b128 v[64:67], v171 offset:16384
	ds_read_b128 v[68:71], v171 offset:17408
	ds_read_b128 v[72:75], v171 offset:18432
	ds_read_b128 v[76:79], v171 offset:19456
	ds_read_b128 v[80:83], v171 offset:20480
	ds_read_b128 v[84:87], v171 offset:21504
	ds_read_b128 v[88:91], v171 offset:22528
	ds_read_b128 v[92:95], v171 offset:23552
	s_mov_b32 m0, s60
	s_nop 0
	global_load_lds_dwordx4 v166, s[48:49]
	s_add_u32 s84, s48, 0x20000
	s_mov_b32 m0, s61
	s_nop 0
	global_load_lds_dwordx4 v168, s[48:49]
	s_addc_u32 s85, s49, 0
	s_mov_b32 m0, s62
	s_nop 0
	global_load_lds_dwordx4 v166, s[84:85]
	s_nop 0
	s_mov_b32 m0, s63
	s_nop 0
	global_load_lds_dwordx4 v168, s[84:85]
	s_nop 0
	s_mov_b32 m0, s59
	s_nop 0
	global_load_lds_dwordx4 v165, s[50:51]
	s_nop 0
	s_mov_b32 m0, s64
	s_nop 0
	global_load_lds_dwordx4 v167, s[50:51]
	s_waitcnt vmcnt(8)
	s_waitcnt lgkmcnt(0)
	s_barrier
	s_setprio 1
	v_mfma_scale_f32_16x16x128_f8f6f4 v[60:63], v[128:135], v[64:71], v[60:63], v172, v172 op_sel_hi:[0,0,0]
	v_mfma_scale_f32_16x16x128_f8f6f4 v[56:59], v[136:143], v[64:71], v[56:59], v172, v172 op_sel_hi:[0,0,0]
	v_mfma_scale_f32_16x16x128_f8f6f4 v[192:195], v[128:135], v[72:79], v[44:47], v172, v172 op_sel_hi:[0,0,0]
	v_mfma_scale_f32_16x16x128_f8f6f4 v[196:199], v[136:143], v[72:79], v[40:43], v172, v172 op_sel_hi:[0,0,0]
	v_mfma_scale_f32_16x16x128_f8f6f4 v[200:203], v[128:135], v[80:87], v[28:31], v172, v172 op_sel_hi:[0,0,0]
	v_mfma_scale_f32_16x16x128_f8f6f4 v[204:207], v[136:143], v[80:87], v[24:27], v172, v172 op_sel_hi:[0,0,0]
	v_mfma_scale_f32_16x16x128_f8f6f4 v[224:227], v[128:135], v[88:95], v[12:15], v172, v172 op_sel_hi:[0,0,0]
	v_mfma_scale_f32_16x16x128_f8f6f4 v[228:231], v[136:143], v[88:95], v[8:11], v172, v172 op_sel_hi:[0,0,0]
	v_mfma_scale_f32_16x16x128_f8f6f4 v[52:55], v[144:151], v[64:71], v[52:55], v172, v172 op_sel_hi:[0,0,0]
	v_mfma_scale_f32_16x16x128_f8f6f4 v[48:51], v[156:163], v[64:71], v[48:51], v172, v172 op_sel_hi:[0,0,0]
	v_mfma_scale_f32_16x16x128_f8f6f4 v[232:235], v[144:151], v[72:79], v[36:39], v172, v172 op_sel_hi:[0,0,0]
	v_mfma_scale_f32_16x16x128_f8f6f4 v[236:239], v[156:163], v[72:79], v[32:35], v172, v172 op_sel_hi:[0,0,0]
	v_mfma_scale_f32_16x16x128_f8f6f4 v[240:243], v[144:151], v[80:87], v[20:23], v172, v172 op_sel_hi:[0,0,0]
	v_mfma_scale_f32_16x16x128_f8f6f4 v[244:247], v[156:163], v[80:87], v[16:19], v172, v172 op_sel_hi:[0,0,0]
	v_mfma_scale_f32_16x16x128_f8f6f4 v[248:251], v[144:151], v[88:95], v[4:7], v172, v172 op_sel_hi:[0,0,0]
	v_mfma_scale_f32_16x16x128_f8f6f4 v[252:255], v[156:163], v[88:95], v[0:3], v172, v172 op_sel_hi:[0,0,0]
	s_setprio 0
	s_barrier
; #define PG8_WAIT_V(n) asm volatile("s_waitcnt vmcnt(" #n ")" ::: "memory")
; #define PG8_WAIT_L(n) asm volatile("s_waitcnt lgkmcnt(" #n ")" ::: "memory")
; #define PG8_BAR __builtin_amdgcn_s_barrier()
; #define PG8_SCHED __builtin_amdgcn_sched_barrier(0)
; #define PG8_STAGE_A(b, h, p) do { if constexpr (GATHER) { if ((h) == 0) PG8_STAGE(PG8_SA(b, h), p, vA0); else PG8_STAGE(PG8_SA(b, h), p, vA1); } else PG8_STAGE(PG8_SA(b, h), (p) + ((h) ? hstepA : (size_t)0), voffA); } while (0)
; template <class Epi, class Sched, bool ALIGN_EPI = true, bool SP2 = true, bool FP8 = false, bool GATHER = false>
; __device__ __forceinline__ void gemm_phase(LAS unsigned char* lds, const Dims g, const Sched& S, const Epi& E, const int wv) {
;     ...
;             PG8_LDB(B0, 1, 0); PG8_LDB(B1, 1, 1); PG8_SCHED; PG8_LDA(At, 1, 0); PG8_STAGE_A(0, 1, a2);
;             PG8_WAIT_V(8); PG8_WAIT_L(0); PG8_BAR; PG8_MMA(0, 0, At, B0); PG8_MMA(0, 1, At, B1); PG8_BAR; PG8_SCHED;
;             PG8_LDA(At, 1, 1); PG8_STAGE(PG8_SB(1, 0), b3, voffB); PG8_STAGE(PG8_SB(1, 1), b3 + hstepB, voffB); PG8_STAGE_A(1, 0, a3);
;             PG8_WAIT_V(8); PG8_WAIT_L(0); PG8_BAR; PG8_MMA(1, 0, At, B0); PG8_MMA(1, 1, At, B1); PG8_BAR; PG8_SCHED;
	s_nop 4
	ds_read_b128 v[0:3], v173
	ds_read_b128 v[4:7], v173 offset:1024
	ds_read_b128 v[16:19], v173 offset:2048
	ds_read_b128 v[20:23], v173 offset:3072
	ds_read_b128 v[128:131], v174
	ds_read_b128 v[132:135], v174 offset:1024
	ds_read_b128 v[136:139], v174 offset:2048
	ds_read_b128 v[140:143], v174 offset:3072
	ds_read_b128 v[8:11], v171 offset:32768
	ds_read_b128 v[12:15], v171 offset:33792
	ds_read_b128 v[24:27], v171 offset:34816
	ds_read_b128 v[28:31], v171 offset:35840
	ds_read_b128 v[32:35], v171 offset:36864
	ds_read_b128 v[36:39], v171 offset:37888
	ds_read_b128 v[40:43], v171 offset:38912
	ds_read_b128 v[44:47], v171 offset:39936
	s_add_u32 s50, s50, 0x20000
	s_addc_u32 s51, s51, 0
	s_mov_b32 m0, s65
	s_nop 0
	global_load_lds_dwordx4 v165, s[50:51]
	s_nop 0
	s_mov_b32 m0, s66
	s_nop 0
	global_load_lds_dwordx4 v167, s[50:51]
	s_waitcnt vmcnt(8)
	s_waitcnt lgkmcnt(0)
	s_barrier
	s_setprio 1
	v_mfma_scale_f32_16x16x128_f8f6f4 v[124:127], v[0:7], v[8:15], v[124:127], v172, v172 op_sel_hi:[0,0,0]
	v_mfma_scale_f32_16x16x128_f8f6f4 v[120:123], v[16:23], v[8:15], v[120:123], v172, v172 op_sel_hi:[0,0,0]
	v_mfma_scale_f32_16x16x128_f8f6f4 v[108:111], v[0:7], v[24:31], v[108:111], v172, v172 op_sel_hi:[0,0,0]
	v_mfma_scale_f32_16x16x128_f8f6f4 v[104:107], v[16:23], v[24:31], v[104:107], v172, v172 op_sel_hi:[0,0,0]
	v_mfma_scale_f32_16x16x128_f8f6f4 v[92:95], v[0:7], v[32:39], v[208:211], v172, v172 op_sel_hi:[0,0,0]
	v_mfma_scale_f32_16x16x128_f8f6f4 v[88:91], v[16:23], v[32:39], v[212:215], v172, v172 op_sel_hi:[0,0,0]
	v_mfma_scale_f32_16x16x128_f8f6f4 v[76:79], v[0:7], v[40:47], v[216:219], v172, v172 op_sel_hi:[0,0,0]
	v_mfma_scale_f32_16x16x128_f8f6f4 v[72:75], v[16:23], v[40:47], v[220:223], v172, v172 op_sel_hi:[0,0,0]
	v_mfma_scale_f32_16x16x128_f8f6f4 v[116:119], v[128:135], v[8:15], v[116:119], v172, v172 op_sel_hi:[0,0,0]
	v_mfma_scale_f32_16x16x128_f8f6f4 v[112:115], v[136:143], v[8:15], v[112:115], v172, v172 op_sel_hi:[0,0,0]
	v_mfma_scale_f32_16x16x128_f8f6f4 v[100:103], v[128:135], v[24:31], v[100:103], v172, v172 op_sel_hi:[0,0,0]
	v_mfma_scale_f32_16x16x128_f8f6f4 v[96:99], v[136:143], v[24:31], v[96:99], v172, v172 op_sel_hi:[0,0,0]
	v_mfma_scale_f32_16x16x128_f8f6f4 v[84:87], v[128:135], v[32:39], v[176:179], v172, v172 op_sel_hi:[0,0,0]
	v_mfma_scale_f32_16x16x128_f8f6f4 v[80:83], v[136:143], v[32:39], v[180:183], v172, v172 op_sel_hi:[0,0,0]
	v_mfma_scale_f32_16x16x128_f8f6f4 v[68:71], v[128:135], v[40:47], v[184:187], v172, v172 op_sel_hi:[0,0,0]
	v_mfma_scale_f32_16x16x128_f8f6f4 v[64:67], v[136:143], v[40:47], v[188:191], v172, v172 op_sel_hi:[0,0,0]
	s_setprio 0
	s_barrier
	ds_read_b128 v[32:35], v171 offset:49152
	ds_read_b128 v[36:39], v171 offset:50176
	ds_read_b128 v[144:147], v171 offset:51200
	ds_read_b128 v[148:151], v171 offset:52224
	ds_read_b128 v[156:159], v171 offset:53248
	ds_read_b128 v[160:163], v171 offset:54272
	ds_read_b128 v[176:179], v171 offset:55296
	ds_read_b128 v[180:183], v171 offset:56320
	s_add_u32 s50, s48, 0x80
	s_addc_u32 s51, s49, 0
	s_mov_b32 m0, s71
	s_nop 0
	global_load_lds_dwordx4 v166, s[50:51]
	s_add_u32 s48, s48, 0x20080
	s_mov_b32 m0, s72
	s_nop 0
	global_load_lds_dwordx4 v168, s[50:51]
	s_addc_u32 s49, s49, 0
	s_mov_b32 m0, s75
	s_nop 0
	global_load_lds_dwordx4 v166, s[48:49]
	s_nop 0
	s_mov_b32 m0, s76
	s_nop 0
	global_load_lds_dwordx4 v168, s[48:49]
	s_mov_b32 m0, s73
	s_nop 0
	global_load_lds_dwordx4 v165, s[46:47]
	s_nop 0
	s_mov_b32 m0, s74
	s_nop 0
	global_load_lds_dwordx4 v167, s[46:47]
	s_waitcnt vmcnt(8)
	s_waitcnt lgkmcnt(0)
	s_barrier
	s_setprio 1
	v_mfma_scale_f32_16x16x128_f8f6f4 v[60:63], v[0:7], v[32:39], v[60:63], v172, v172 op_sel_hi:[0,0,0]
	v_mfma_scale_f32_16x16x128_f8f6f4 v[56:59], v[16:23], v[32:39], v[56:59], v172, v172 op_sel_hi:[0,0,0]
	v_mfma_scale_f32_16x16x128_f8f6f4 v[44:47], v[0:7], v[144:151], v[192:195], v172, v172 op_sel_hi:[0,0,0]
	v_mfma_scale_f32_16x16x128_f8f6f4 v[40:43], v[16:23], v[144:151], v[196:199], v172, v172 op_sel_hi:[0,0,0]
	v_mfma_scale_f32_16x16x128_f8f6f4 v[28:31], v[0:7], v[156:163], v[200:203], v172, v172 op_sel_hi:[0,0,0]
	v_mfma_scale_f32_16x16x128_f8f6f4 v[24:27], v[16:23], v[156:163], v[204:207], v172, v172 op_sel_hi:[0,0,0]
	v_mfma_scale_f32_16x16x128_f8f6f4 v[12:15], v[0:7], v[176:183], v[224:227], v172, v172 op_sel_hi:[0,0,0]
	v_mfma_scale_f32_16x16x128_f8f6f4 v[8:11], v[16:23], v[176:183], v[228:231], v172, v172 op_sel_hi:[0,0,0]
	v_mfma_scale_f32_16x16x128_f8f6f4 v[52:55], v[128:135], v[32:39], v[52:55], v172, v172 op_sel_hi:[0,0,0]
	v_mfma_scale_f32_16x16x128_f8f6f4 v[48:51], v[136:143], v[32:39], v[48:51], v172, v172 op_sel_hi:[0,0,0]
	v_mfma_scale_f32_16x16x128_f8f6f4 v[36:39], v[128:135], v[144:151], v[232:235], v172, v172 op_sel_hi:[0,0,0]
	v_mfma_scale_f32_16x16x128_f8f6f4 v[32:35], v[136:143], v[144:151], v[236:239], v172, v172 op_sel_hi:[0,0,0]
	v_mfma_scale_f32_16x16x128_f8f6f4 v[20:23], v[128:135], v[156:163], v[240:243], v172, v172 op_sel_hi:[0,0,0]
	v_mfma_scale_f32_16x16x128_f8f6f4 v[16:19], v[136:143], v[156:163], v[244:247], v172, v172 op_sel_hi:[0,0,0]
	v_mfma_scale_f32_16x16x128_f8f6f4 v[4:7], v[128:135], v[176:183], v[248:251], v172, v172 op_sel_hi:[0,0,0]
	v_mfma_scale_f32_16x16x128_f8f6f4 v[0:3], v[136:143], v[176:183], v[252:255], v172, v172 op_sel_hi:[0,0,0]
	s_setprio 0
	s_barrier
	s_add_i32 s82, s82, 2
	s_add_u32 s5, s5, 0x100
	s_addc_u32 s37, s37, 0
	s_add_u32 s39, s39, 0x100
	s_addc_u32 s81, s81, 0
	s_add_u32 s44, s44, 0x100
	s_addc_u32 s45, s45, 0
	s_cmp_gt_u32 s82, 5
	s_cbranch_scc0 .LBB0_745
	s_and_b64 vcc, exec, s[14:15]
	s_cbranch_vccz .LBB0_748
	s_barrier

; #define PG8_WAIT_V(n) asm volatile("s_waitcnt vmcnt(" #n ")" ::: "memory")
; #define PG8_WAIT_L(n) asm volatile("s_waitcnt lgkmcnt(" #n ")" ::: "memory")
; #define PG8_BAR __builtin_amdgcn_s_barrier()
; #define PG8_SCHED __builtin_amdgcn_sched_barrier(0)
; #define PG8_STAGE_A(b, h, p) do { if constexpr (GATHER) { if ((h) == 0) PG8_STAGE(PG8_SA(b, h), p, vA0); else PG8_STAGE(PG8_SA(b, h), p, vA1); } else PG8_STAGE(PG8_SA(b, h), (p) + ((h) ? hstepA : (size_t)0), voffA); } while (0)
; #define PG8_GOFF1(un, h, d) do { int tz_ = tid; asm volatile("" : "+v"(tz_)); _Pragma("unroll") for (int i_ = 0; i_ < 2; ++i_) { int R_, C_; stage_rc(tz_ * 16 + i_ * 8192, R_, C_); \
;         d[i_] = S.gather(un, R_ + (h) * HALF) + (unsigned)C_ * 2u; } } while (0)
; template <class Epi, class Sched, bool ALIGN_EPI = true, bool SP2 = true, bool FP8 = false, bool GATHER = false>
; __device__ __forceinline__ void gemm_phase(LAS unsigned char* lds, const Dims g, const Sched& S, const Epi& E, const int wv) {
;     ...
;             PG8_LDB(B0, 0, 0); PG8_LDB(B1, 0, 1); PG8_SCHED; PG8_LDA(At, 0, 0); PG8_STAGE_A(1, 1, a1);
;             if constexpr (GATHER) { if (last) PG8_GOFF1(un_, 1, vA1); }
;             PG8_WAIT_V(8); PG8_WAIT_L(0); PG8_BAR; PG8_MMA(0, 0, At, B0); PG8_MMA(0, 1, At, B1); PG8_BAR; PG8_SCHED;
;             PG8_LDA(At, 0, 1); PG8_STAGE(PG8_SB(0, 0), b2, voffB); PG8_STAGE(PG8_SB(0, 1), b2 + hstepB, voffB); PG8_STAGE_A(0, 0, a2);
;             PG8_WAIT_V(8); PG8_WAIT_L(0); PG8_BAR; PG8_MMA(1, 0, At, B0); PG8_MMA(1, 1, At, B1); PG8_BAR; PG8_SCHED;
;             PG8_LDB(B0, 1, 0); PG8_LDB(B1, 1, 1); PG8_SCHED; PG8_LDA(At, 1, 0); PG8_STAGE_A(0, 1, a2);
.LBB0_1426:
	s_add_u32 s40, s40, 0x100
	s_addc_u32 s41, s41, 0
	s_and_b64 s[42:43], s[42:43], exec
	s_cselect_b32 s48, s78, s40
	s_waitcnt vmcnt(8)
	s_cselect_b32 s49, s39, s41
	s_cselect_b32 s45, s79, s83
	s_cselect_b32 s44, s80, s82
	s_add_u32 s42, s48, 0x80
	s_waitcnt lgkmcnt(0)
	s_addc_u32 s43, s49, 0
	s_add_u32 s46, s44, 0x80
	s_addc_u32 s47, s45, 0
	s_barrier
	s_setprio 1
	s_waitcnt lgkmcnt(6)
	v_mfma_scale_f32_16x16x128_f8f6f4 v[188:191], v[16:23], v[56:63], v[188:191], v200, v200 op_sel_hi:[0,0,0]
	v_mfma_scale_f32_16x16x128_f8f6f4 v[184:187], v[24:31], v[56:63], v[184:187], v200, v200 op_sel_hi:[0,0,0]
	s_waitcnt lgkmcnt(4)
	v_mfma_scale_f32_16x16x128_f8f6f4 v[172:175], v[16:23], v[48:55], v[172:175], v200, v200 op_sel_hi:[0,0,0]
	v_mfma_scale_f32_16x16x128_f8f6f4 v[168:171], v[24:31], v[48:55], v[168:171], v200, v200 op_sel_hi:[0,0,0]
	s_waitcnt lgkmcnt(2)
	v_mfma_scale_f32_16x16x128_f8f6f4 v[156:159], v[16:23], v[40:47], v[156:159], v200, v200 op_sel_hi:[0,0,0]
	v_mfma_scale_f32_16x16x128_f8f6f4 v[152:155], v[24:31], v[40:47], v[152:155], v200, v200 op_sel_hi:[0,0,0]
	s_waitcnt lgkmcnt(0)
	v_mfma_scale_f32_16x16x128_f8f6f4 v[140:143], v[16:23], v[32:39], v[140:143], v200, v200 op_sel_hi:[0,0,0]
	v_mfma_scale_f32_16x16x128_f8f6f4 v[136:139], v[24:31], v[32:39], v[136:139], v200, v200 op_sel_hi:[0,0,0]
	v_mfma_scale_f32_16x16x128_f8f6f4 v[180:183], v[0:7], v[56:63], v[180:183], v200, v200 op_sel_hi:[0,0,0]
	v_mfma_scale_f32_16x16x128_f8f6f4 v[176:179], v[8:15], v[56:63], v[176:179], v200, v200 op_sel_hi:[0,0,0]
	v_mfma_scale_f32_16x16x128_f8f6f4 v[164:167], v[0:7], v[48:55], v[164:167], v200, v200 op_sel_hi:[0,0,0]
	v_mfma_scale_f32_16x16x128_f8f6f4 v[160:163], v[8:15], v[48:55], v[160:163], v200, v200 op_sel_hi:[0,0,0]
	v_mfma_scale_f32_16x16x128_f8f6f4 v[148:151], v[0:7], v[40:47], v[148:151], v200, v200 op_sel_hi:[0,0,0]
	v_mfma_scale_f32_16x16x128_f8f6f4 v[144:147], v[8:15], v[40:47], v[144:147], v200, v200 op_sel_hi:[0,0,0]
	v_mfma_scale_f32_16x16x128_f8f6f4 v[132:135], v[0:7], v[32:39], v[132:135], v200, v200 op_sel_hi:[0,0,0]
	v_mfma_scale_f32_16x16x128_f8f6f4 v[128:131], v[8:15], v[32:39], v[128:131], v200, v200 op_sel_hi:[0,0,0]
	s_setprio 0
	s_barrier
	ds_read_b128 v[32:35], v202 offset:16384
	ds_read_b128 v[36:39], v202 offset:17408
	ds_read_b128 v[40:43], v202 offset:18432
	ds_read_b128 v[44:47], v202 offset:19456
	ds_read_b128 v[48:51], v202 offset:20480
	ds_read_b128 v[52:55], v202 offset:21504
	ds_read_b128 v[56:59], v202 offset:22528
	ds_read_b128 v[60:63], v202 offset:23552
	s_mov_b32 m0, s56
	s_nop 0
	global_load_lds_dwordx4 v195, s[44:45]
	s_add_u32 s86, s44, 0x20000
	s_mov_b32 m0, s57
	s_nop 0
	global_load_lds_dwordx4 v199, s[44:45]
	s_addc_u32 s87, s45, 0
	s_mov_b32 m0, s58
	s_nop 0
	global_load_lds_dwordx4 v195, s[86:87]
	s_nop 0
	s_mov_b32 m0, s59
	s_nop 0
	global_load_lds_dwordx4 v199, s[86:87]
	s_nop 0
	s_mov_b32 m0, s37
	s_nop 0
	global_load_lds_dwordx4 v194, s[48:49]
	s_nop 0
	s_mov_b32 m0, s60
	s_nop 0
	global_load_lds_dwordx4 v196, s[48:49]
	s_waitcnt vmcnt(8)
	s_waitcnt lgkmcnt(0)
	s_barrier
	s_setprio 1
	v_mfma_scale_f32_16x16x128_f8f6f4 v[124:127], v[16:23], v[32:39], v[124:127], v200, v200 op_sel_hi:[0,0,0]
	v_mfma_scale_f32_16x16x128_f8f6f4 v[120:123], v[24:31], v[32:39], v[120:123], v200, v200 op_sel_hi:[0,0,0]
	v_mfma_scale_f32_16x16x128_f8f6f4 v[108:111], v[16:23], v[40:47], v[108:111], v200, v200 op_sel_hi:[0,0,0]
	v_mfma_scale_f32_16x16x128_f8f6f4 v[104:107], v[24:31], v[40:47], v[104:107], v200, v200 op_sel_hi:[0,0,0]
	v_mfma_scale_f32_16x16x128_f8f6f4 v[92:95], v[16:23], v[48:55], v[92:95], v200, v200 op_sel_hi:[0,0,0]
	v_mfma_scale_f32_16x16x128_f8f6f4 v[88:91], v[24:31], v[48:55], v[88:91], v200, v200 op_sel_hi:[0,0,0]
	v_mfma_scale_f32_16x16x128_f8f6f4 v[76:79], v[16:23], v[56:63], v[76:79], v200, v200 op_sel_hi:[0,0,0]
	v_mfma_scale_f32_16x16x128_f8f6f4 v[72:75], v[24:31], v[56:63], v[72:75], v200, v200 op_sel_hi:[0,0,0]
	v_mfma_scale_f32_16x16x128_f8f6f4 v[116:119], v[0:7], v[32:39], v[116:119], v200, v200 op_sel_hi:[0,0,0]
	v_mfma_scale_f32_16x16x128_f8f6f4 v[112:115], v[8:15], v[32:39], v[112:115], v200, v200 op_sel_hi:[0,0,0]
	v_mfma_scale_f32_16x16x128_f8f6f4 v[100:103], v[0:7], v[40:47], v[100:103], v200, v200 op_sel_hi:[0,0,0]
	v_mfma_scale_f32_16x16x128_f8f6f4 v[96:99], v[8:15], v[40:47], v[96:99], v200, v200 op_sel_hi:[0,0,0]
	v_mfma_scale_f32_16x16x128_f8f6f4 v[84:87], v[0:7], v[48:55], v[84:87], v200, v200 op_sel_hi:[0,0,0]
	v_mfma_scale_f32_16x16x128_f8f6f4 v[80:83], v[8:15], v[48:55], v[80:83], v200, v200 op_sel_hi:[0,0,0]
	v_mfma_scale_f32_16x16x128_f8f6f4 v[68:71], v[0:7], v[56:63], v[68:71], v200, v200 op_sel_hi:[0,0,0]
	v_mfma_scale_f32_16x16x128_f8f6f4 v[64:67], v[8:15], v[56:63], v[64:67], v200, v200 op_sel_hi:[0,0,0]
	s_setprio 0
	s_barrier
; #define PG8_WAIT_V(n) asm volatile("s_waitcnt vmcnt(" #n ")" ::: "memory")
; #define PG8_WAIT_L(n) asm volatile("s_waitcnt lgkmcnt(" #n ")" ::: "memory")
; #define PG8_BAR __builtin_amdgcn_s_barrier()
; #define PG8_SCHED __builtin_amdgcn_sched_barrier(0)
; #define PG8_STAGE_A(b, h, p) do { if constexpr (GATHER) { if ((h) == 0) PG8_STAGE(PG8_SA(b, h), p, vA0); else PG8_STAGE(PG8_SA(b, h), p, vA1); } else PG8_STAGE(PG8_SA(b, h), (p) + ((h) ? hstepA : (size_t)0), voffA); } while (0)
; template <class Epi, class Sched, bool ALIGN_EPI = true, bool SP2 = true, bool FP8 = false, bool GATHER = false>
; __device__ __forceinline__ void gemm_phase(LAS unsigned char* lds, const Dims g, const Sched& S, const Epi& E, const int wv) {
;     ...
;             PG8_LDB(B0, 1, 0); PG8_LDB(B1, 1, 1); PG8_SCHED; PG8_LDA(At, 1, 0); PG8_STAGE_A(0, 1, a2);
;             PG8_WAIT_V(8); PG8_WAIT_L(0); PG8_BAR; PG8_MMA(0, 0, At, B0); PG8_MMA(0, 1, At, B1); PG8_BAR; PG8_SCHED;
;             PG8_LDA(At, 1, 1); PG8_STAGE(PG8_SB(1, 0), b3, voffB); PG8_STAGE(PG8_SB(1, 1), b3 + hstepB, voffB); PG8_STAGE_A(1, 0, a3);
;             PG8_WAIT_V(8); PG8_WAIT_L(0); PG8_BAR; PG8_MMA(1, 0, At, B0); PG8_MMA(1, 1, At, B1); PG8_BAR; PG8_SCHED;
	v_add_u32_e32 v12, 0x18000, v201
	v_add_u32_e32 v28, 0x1c000, v201
	ds_read_b128 v[0:3], v12
	ds_read_b128 v[4:7], v12 offset:1024
	ds_read_b128 v[8:11], v12 offset:2048
	ds_read_b128 v[12:15], v12 offset:3072
	ds_read_b128 v[16:19], v28
	ds_read_b128 v[20:23], v28 offset:1024
	ds_read_b128 v[24:27], v28 offset:2048
	ds_read_b128 v[28:31], v28 offset:3072
	ds_read_b128 v[32:35], v202 offset:32768
	ds_read_b128 v[36:39], v202 offset:33792
	ds_read_b128 v[40:43], v202 offset:34816
	ds_read_b128 v[44:47], v202 offset:35840
	ds_read_b128 v[48:51], v202 offset:36864
	ds_read_b128 v[52:55], v202 offset:37888
	ds_read_b128 v[56:59], v202 offset:38912
	ds_read_b128 v[60:63], v202 offset:39936
	s_mov_b32 m0, s61
	s_nop 0
	global_load_lds_dwordx4 v197, s[48:49]
	s_nop 0
	s_mov_b32 m0, s62
	s_nop 0
	global_load_lds_dwordx4 v198, s[48:49]
	s_waitcnt vmcnt(8)
	s_waitcnt lgkmcnt(0)
	s_barrier
	s_setprio 1
	v_mfma_scale_f32_16x16x128_f8f6f4 v[188:191], v[0:7], v[32:39], v[188:191], v200, v200 op_sel_hi:[0,0,0]
	v_mfma_scale_f32_16x16x128_f8f6f4 v[184:187], v[8:15], v[32:39], v[184:187], v200, v200 op_sel_hi:[0,0,0]
	v_mfma_scale_f32_16x16x128_f8f6f4 v[172:175], v[0:7], v[40:47], v[172:175], v200, v200 op_sel_hi:[0,0,0]
	v_mfma_scale_f32_16x16x128_f8f6f4 v[168:171], v[8:15], v[40:47], v[168:171], v200, v200 op_sel_hi:[0,0,0]
	v_mfma_scale_f32_16x16x128_f8f6f4 v[156:159], v[0:7], v[48:55], v[156:159], v200, v200 op_sel_hi:[0,0,0]
	v_mfma_scale_f32_16x16x128_f8f6f4 v[152:155], v[8:15], v[48:55], v[152:155], v200, v200 op_sel_hi:[0,0,0]
	v_mfma_scale_f32_16x16x128_f8f6f4 v[140:143], v[0:7], v[56:63], v[140:143], v200, v200 op_sel_hi:[0,0,0]
	v_mfma_scale_f32_16x16x128_f8f6f4 v[136:139], v[8:15], v[56:63], v[136:139], v200, v200 op_sel_hi:[0,0,0]
	v_mfma_scale_f32_16x16x128_f8f6f4 v[180:183], v[16:23], v[32:39], v[180:183], v200, v200 op_sel_hi:[0,0,0]
	v_mfma_scale_f32_16x16x128_f8f6f4 v[176:179], v[24:31], v[32:39], v[176:179], v200, v200 op_sel_hi:[0,0,0]
	v_mfma_scale_f32_16x16x128_f8f6f4 v[164:167], v[16:23], v[40:47], v[164:167], v200, v200 op_sel_hi:[0,0,0]
	v_mfma_scale_f32_16x16x128_f8f6f4 v[160:163], v[24:31], v[40:47], v[160:163], v200, v200 op_sel_hi:[0,0,0]
	v_mfma_scale_f32_16x16x128_f8f6f4 v[148:151], v[16:23], v[48:55], v[148:151], v200, v200 op_sel_hi:[0,0,0]
	v_mfma_scale_f32_16x16x128_f8f6f4 v[144:147], v[24:31], v[48:55], v[144:147], v200, v200 op_sel_hi:[0,0,0]
	v_mfma_scale_f32_16x16x128_f8f6f4 v[132:135], v[16:23], v[56:63], v[132:135], v200, v200 op_sel_hi:[0,0,0]
	v_mfma_scale_f32_16x16x128_f8f6f4 v[128:131], v[24:31], v[56:63], v[128:131], v200, v200 op_sel_hi:[0,0,0]
	s_setprio 0
	s_barrier
	ds_read_b128 v[32:35], v202 offset:49152
	ds_read_b128 v[36:39], v202 offset:50176
	ds_read_b128 v[40:43], v202 offset:51200
	ds_read_b128 v[44:47], v202 offset:52224
	ds_read_b128 v[48:51], v202 offset:53248
	ds_read_b128 v[52:55], v202 offset:54272
	ds_read_b128 v[56:59], v202 offset:55296
	ds_read_b128 v[60:63], v202 offset:56320
	s_mov_b32 m0, s65
	s_nop 0
	global_load_lds_dwordx4 v195, s[46:47]
	s_add_u32 s44, s44, 0x20080
	s_mov_b32 m0, s66
	s_nop 0
	global_load_lds_dwordx4 v199, s[46:47]
	s_addc_u32 s45, s45, 0
	s_mov_b32 m0, s69
	s_nop 0
	global_load_lds_dwordx4 v195, s[44:45]
	s_nop 0
	s_mov_b32 m0, s70
	s_nop 0
	global_load_lds_dwordx4 v199, s[44:45]
	s_mov_b32 m0, s67
	s_nop 0
	global_load_lds_dwordx4 v194, s[42:43]
	s_nop 0
	s_mov_b32 m0, s68
	s_nop 0
	global_load_lds_dwordx4 v196, s[42:43]
	s_waitcnt vmcnt(8)
	s_waitcnt lgkmcnt(0)
	s_barrier
	s_setprio 1
	v_mfma_scale_f32_16x16x128_f8f6f4 v[124:127], v[0:7], v[32:39], v[124:127], v200, v200 op_sel_hi:[0,0,0]
	v_mfma_scale_f32_16x16x128_f8f6f4 v[120:123], v[8:15], v[32:39], v[120:123], v200, v200 op_sel_hi:[0,0,0]
	v_mfma_scale_f32_16x16x128_f8f6f4 v[108:111], v[0:7], v[40:47], v[108:111], v200, v200 op_sel_hi:[0,0,0]
	v_mfma_scale_f32_16x16x128_f8f6f4 v[104:107], v[8:15], v[40:47], v[104:107], v200, v200 op_sel_hi:[0,0,0]
	v_mfma_scale_f32_16x16x128_f8f6f4 v[92:95], v[0:7], v[48:55], v[92:95], v200, v200 op_sel_hi:[0,0,0]
	v_mfma_scale_f32_16x16x128_f8f6f4 v[88:91], v[8:15], v[48:55], v[88:91], v200, v200 op_sel_hi:[0,0,0]
	v_mfma_scale_f32_16x16x128_f8f6f4 v[76:79], v[0:7], v[56:63], v[76:79], v200, v200 op_sel_hi:[0,0,0]
	v_mfma_scale_f32_16x16x128_f8f6f4 v[72:75], v[8:15], v[56:63], v[72:75], v200, v200 op_sel_hi:[0,0,0]
	v_mfma_scale_f32_16x16x128_f8f6f4 v[116:119], v[16:23], v[32:39], v[116:119], v200, v200 op_sel_hi:[0,0,0]
	v_mfma_scale_f32_16x16x128_f8f6f4 v[112:115], v[24:31], v[32:39], v[112:115], v200, v200 op_sel_hi:[0,0,0]
	v_mfma_scale_f32_16x16x128_f8f6f4 v[100:103], v[16:23], v[40:47], v[100:103], v200, v200 op_sel_hi:[0,0,0]
	v_mfma_scale_f32_16x16x128_f8f6f4 v[96:99], v[24:31], v[40:47], v[96:99], v200, v200 op_sel_hi:[0,0,0]
	v_mfma_scale_f32_16x16x128_f8f6f4 v[84:87], v[16:23], v[48:55], v[84:87], v200, v200 op_sel_hi:[0,0,0]
	v_mfma_scale_f32_16x16x128_f8f6f4 v[80:83], v[24:31], v[48:55], v[80:83], v200, v200 op_sel_hi:[0,0,0]
	v_mfma_scale_f32_16x16x128_f8f6f4 v[68:71], v[16:23], v[56:63], v[68:71], v200, v200 op_sel_hi:[0,0,0]
	v_mfma_scale_f32_16x16x128_f8f6f4 v[64:67], v[24:31], v[56:63], v[64:67], v200, v200 op_sel_hi:[0,0,0]
	s_setprio 0
	s_barrier
	s_add_i32 s84, s84, 2
	s_add_u32 s82, s82, 0x100
	s_addc_u32 s83, s83, 0
	s_cmp_gt_u32 s84, 5
	s_cbranch_scc1 .LBB0_1431

; #define PG8_WAIT_V(n) asm volatile("s_waitcnt vmcnt(" #n ")" ::: "memory")
; #define PG8_WAIT_L(n) asm volatile("s_waitcnt lgkmcnt(" #n ")" ::: "memory")
; #define PG8_BAR __builtin_amdgcn_s_barrier()
; #define PG8_SCHED __builtin_amdgcn_sched_barrier(0)
; #define PG8_STAGE_A(b, h, p) do { if constexpr (GATHER) { if ((h) == 0) PG8_STAGE(PG8_SA(b, h), p, vA0); else PG8_STAGE(PG8_SA(b, h), p, vA1); } else PG8_STAGE(PG8_SA(b, h), (p) + ((h) ? hstepA : (size_t)0), voffA); } while (0)
; #define PG8_GOFF1(un, h, d) do { int tz_ = tid; asm volatile("" : "+v"(tz_)); _Pragma("unroll") for (int i_ = 0; i_ < 2; ++i_) { int R_, C_; stage_rc(tz_ * 16 + i_ * 8192, R_, C_); \
;         d[i_] = S.gather(un, R_ + (h) * HALF) + (unsigned)C_ * 2u; } } while (0)
; template <class Epi, class Sched, bool ALIGN_EPI = true, bool SP2 = true, bool FP8 = false, bool GATHER = false>
; __device__ __forceinline__ void gemm_phase(LAS unsigned char* lds, const Dims g, const Sched& S, const Epi& E, const int wv) {
;     ...
;             PG8_LDB(B0, 0, 0); PG8_LDB(B1, 0, 1); PG8_SCHED; PG8_LDA(At, 0, 0); PG8_STAGE_A(1, 1, a1);
;             if constexpr (GATHER) { if (last) PG8_GOFF1(un_, 1, vA1); }
;             PG8_WAIT_V(8); PG8_WAIT_L(0); PG8_BAR; PG8_MMA(0, 0, At, B0); PG8_MMA(0, 1, At, B1); PG8_BAR; PG8_SCHED;
;             PG8_LDA(At, 0, 1); PG8_STAGE(PG8_SB(0, 0), b2, voffB); PG8_STAGE(PG8_SB(0, 1), b2 + hstepB, voffB); PG8_STAGE_A(0, 0, a2);
;             PG8_WAIT_V(8); PG8_WAIT_L(0); PG8_BAR; PG8_MMA(1, 0, At, B0); PG8_MMA(1, 1, At, B1); PG8_BAR; PG8_SCHED;
.LBB0_1528:
	ds_read_b128 v[128:131], v157
	ds_read_b128 v[132:135], v157 offset:1024
	ds_read_b128 v[136:139], v157 offset:2048
	ds_read_b128 v[140:143], v157 offset:3072
	ds_read_b128 v[144:147], v158
	ds_read_b128 v[148:151], v158 offset:1024
	ds_read_b128 v[164:167], v158 offset:2048
	ds_read_b128 v[168:171], v158 offset:3072
	s_add_u32 s46, s44, 0x100
	s_addc_u32 s47, s45, 0
	s_cmp_eq_u32 s86, 4
	s_cselect_b32 s52, s43, s46
	s_cselect_b32 s53, s39, s47
	s_cselect_b32 s50, s55, s84
	s_cselect_b32 s51, s54, s85
	s_add_u32 s48, s52, 0x80
	s_addc_u32 s49, s53, 0
	ds_read_b128 v[172:175], v159
	ds_read_b128 v[176:179], v159 offset:1024
	ds_read_b128 v[180:183], v159 offset:2048
	ds_read_b128 v[184:187], v159 offset:3072
	ds_read_b128 v[188:191], v159 offset:4096
	ds_read_b128 v[192:195], v159 offset:5120
	ds_read_b128 v[196:199], v159 offset:6144
	ds_read_b128 v[200:203], v159 offset:7168
	s_add_u32 s44, s44, 0x20080
	s_addc_u32 s45, s45, 0
	s_mov_b32 m0, s76
	s_nop 0
	global_load_lds_dwordx4 v153, s[44:45]
	s_nop 0
	s_mov_b32 m0, s77
	s_nop 0
	global_load_lds_dwordx4 v155, s[44:45]
	s_waitcnt vmcnt(8)
	s_waitcnt lgkmcnt(0)
	s_barrier
	s_setprio 1
	v_mfma_scale_f32_16x16x128_f8f6f4 v[124:127], v[128:135], v[172:179], v[124:127], v160, v160 op_sel_hi:[0,0,0]
	v_mfma_scale_f32_16x16x128_f8f6f4 v[120:123], v[136:143], v[172:179], v[120:123], v160, v160 op_sel_hi:[0,0,0]
	v_mfma_scale_f32_16x16x128_f8f6f4 v[116:119], v[128:135], v[180:187], v[116:119], v160, v160 op_sel_hi:[0,0,0]
	v_mfma_scale_f32_16x16x128_f8f6f4 v[112:115], v[136:143], v[180:187], v[112:115], v160, v160 op_sel_hi:[0,0,0]
	v_mfma_scale_f32_16x16x128_f8f6f4 v[204:207], v[128:135], v[188:195], v[92:95], v160, v160 op_sel_hi:[0,0,0]
	v_mfma_scale_f32_16x16x128_f8f6f4 v[208:211], v[136:143], v[188:195], v[88:91], v160, v160 op_sel_hi:[0,0,0]
	v_mfma_scale_f32_16x16x128_f8f6f4 v[212:215], v[128:135], v[196:203], v[76:79], v160, v160 op_sel_hi:[0,0,0]
	v_mfma_scale_f32_16x16x128_f8f6f4 v[216:219], v[136:143], v[196:203], v[72:75], v160, v160 op_sel_hi:[0,0,0]
	v_mfma_scale_f32_16x16x128_f8f6f4 v[108:111], v[144:151], v[172:179], v[108:111], v160, v160 op_sel_hi:[0,0,0]
	v_mfma_scale_f32_16x16x128_f8f6f4 v[104:107], v[164:171], v[172:179], v[104:107], v160, v160 op_sel_hi:[0,0,0]
	v_mfma_scale_f32_16x16x128_f8f6f4 v[100:103], v[144:151], v[180:187], v[100:103], v160, v160 op_sel_hi:[0,0,0]
	v_mfma_scale_f32_16x16x128_f8f6f4 v[96:99], v[164:171], v[180:187], v[96:99], v160, v160 op_sel_hi:[0,0,0]
	v_mfma_scale_f32_16x16x128_f8f6f4 v[172:175], v[144:151], v[188:195], v[84:87], v160, v160 op_sel_hi:[0,0,0]
	v_mfma_scale_f32_16x16x128_f8f6f4 v[176:179], v[164:171], v[188:195], v[80:83], v160, v160 op_sel_hi:[0,0,0]
	v_mfma_scale_f32_16x16x128_f8f6f4 v[180:183], v[144:151], v[196:203], v[68:71], v160, v160 op_sel_hi:[0,0,0]
	v_mfma_scale_f32_16x16x128_f8f6f4 v[184:187], v[164:171], v[196:203], v[64:67], v160, v160 op_sel_hi:[0,0,0]
	s_setprio 0
	s_barrier
	s_nop 4
	ds_read_b128 v[64:67], v159 offset:16384
	ds_read_b128 v[68:71], v159 offset:17408
	ds_read_b128 v[72:75], v159 offset:18432
	ds_read_b128 v[76:79], v159 offset:19456
	ds_read_b128 v[80:83], v159 offset:20480
	ds_read_b128 v[84:87], v159 offset:21504
	ds_read_b128 v[88:91], v159 offset:22528
	ds_read_b128 v[92:95], v159 offset:23552
	s_mov_b32 m0, s62
	s_nop 0
	global_load_lds_dwordx4 v154, s[50:51]
	s_nop 0
	s_mov_b32 m0, s63
	s_nop 0
	global_load_lds_dwordx4 v156, s[50:51]
	s_add_u32 s44, s50, 0x20000
	s_addc_u32 s45, s51, 0
	s_mov_b32 m0, s64
	s_nop 0
	global_load_lds_dwordx4 v154, s[44:45]
	s_nop 0
	s_mov_b32 m0, s65
	s_nop 0
	global_load_lds_dwordx4 v156, s[44:45]
	s_mov_b32 m0, s61
	s_nop 0
	global_load_lds_dwordx4 v153, s[52:53]
	s_nop 0
	s_mov_b32 m0, s66
	s_nop 0
	global_load_lds_dwordx4 v155, s[52:53]
	s_waitcnt vmcnt(8)
	s_waitcnt lgkmcnt(0)
	s_barrier
	s_setprio 1
	v_mfma_scale_f32_16x16x128_f8f6f4 v[60:63], v[128:135], v[64:71], v[60:63], v160, v160 op_sel_hi:[0,0,0]
	v_mfma_scale_f32_16x16x128_f8f6f4 v[56:59], v[136:143], v[64:71], v[56:59], v160, v160 op_sel_hi:[0,0,0]
	v_mfma_scale_f32_16x16x128_f8f6f4 v[188:191], v[128:135], v[72:79], v[44:47], v160, v160 op_sel_hi:[0,0,0]
	v_mfma_scale_f32_16x16x128_f8f6f4 v[192:195], v[136:143], v[72:79], v[40:43], v160, v160 op_sel_hi:[0,0,0]
	v_mfma_scale_f32_16x16x128_f8f6f4 v[196:199], v[128:135], v[80:87], v[28:31], v160, v160 op_sel_hi:[0,0,0]
	v_mfma_scale_f32_16x16x128_f8f6f4 v[200:203], v[136:143], v[80:87], v[24:27], v160, v160 op_sel_hi:[0,0,0]
	v_mfma_scale_f32_16x16x128_f8f6f4 v[220:223], v[128:135], v[88:95], v[12:15], v160, v160 op_sel_hi:[0,0,0]
	v_mfma_scale_f32_16x16x128_f8f6f4 v[224:227], v[136:143], v[88:95], v[8:11], v160, v160 op_sel_hi:[0,0,0]
	v_mfma_scale_f32_16x16x128_f8f6f4 v[52:55], v[144:151], v[64:71], v[52:55], v160, v160 op_sel_hi:[0,0,0]
	v_mfma_scale_f32_16x16x128_f8f6f4 v[48:51], v[164:171], v[64:71], v[48:51], v160, v160 op_sel_hi:[0,0,0]
	v_mfma_scale_f32_16x16x128_f8f6f4 v[228:231], v[144:151], v[72:79], v[36:39], v160, v160 op_sel_hi:[0,0,0]
	v_mfma_scale_f32_16x16x128_f8f6f4 v[232:235], v[164:171], v[72:79], v[32:35], v160, v160 op_sel_hi:[0,0,0]
	v_mfma_scale_f32_16x16x128_f8f6f4 v[236:239], v[144:151], v[80:87], v[20:23], v160, v160 op_sel_hi:[0,0,0]
	v_mfma_scale_f32_16x16x128_f8f6f4 v[240:243], v[164:171], v[80:87], v[16:19], v160, v160 op_sel_hi:[0,0,0]
	v_mfma_scale_f32_16x16x128_f8f6f4 v[244:247], v[144:151], v[88:95], v[4:7], v160, v160 op_sel_hi:[0,0,0]
	v_mfma_scale_f32_16x16x128_f8f6f4 v[248:251], v[164:171], v[88:95], v[0:3], v160, v160 op_sel_hi:[0,0,0]
	s_setprio 0
	s_barrier
; #define PG8_WAIT_V(n) asm volatile("s_waitcnt vmcnt(" #n ")" ::: "memory")
; #define PG8_WAIT_L(n) asm volatile("s_waitcnt lgkmcnt(" #n ")" ::: "memory")
; #define PG8_BAR __builtin_amdgcn_s_barrier()
; #define PG8_SCHED __builtin_amdgcn_sched_barrier(0)
; #define PG8_STAGE_A(b, h, p) do { if constexpr (GATHER) { if ((h) == 0) PG8_STAGE(PG8_SA(b, h), p, vA0); else PG8_STAGE(PG8_SA(b, h), p, vA1); } else PG8_STAGE(PG8_SA(b, h), (p) + ((h) ? hstepA : (size_t)0), voffA); } while (0)
; template <class Epi, class Sched, bool ALIGN_EPI = true, bool SP2 = true, bool FP8 = false, bool GATHER = false>
; __device__ __forceinline__ void gemm_phase(LAS unsigned char* lds, const Dims g, const Sched& S, const Epi& E, const int wv) {
;     ...
;             PG8_LDB(B0, 1, 0); PG8_LDB(B1, 1, 1); PG8_SCHED; PG8_LDA(At, 1, 0); PG8_STAGE_A(0, 1, a2);
;             PG8_WAIT_V(8); PG8_WAIT_L(0); PG8_BAR; PG8_MMA(0, 0, At, B0); PG8_MMA(0, 1, At, B1); PG8_BAR; PG8_SCHED;
;             PG8_LDA(At, 1, 1); PG8_STAGE(PG8_SB(1, 0), b3, voffB); PG8_STAGE(PG8_SB(1, 1), b3 + hstepB, voffB); PG8_STAGE_A(1, 0, a3);
;             PG8_WAIT_V(8); PG8_WAIT_L(0); PG8_BAR; PG8_MMA(1, 0, At, B0); PG8_MMA(1, 1, At, B1); PG8_BAR; PG8_SCHED;
	s_nop 4
	ds_read_b128 v[0:3], v161
	ds_read_b128 v[4:7], v161 offset:1024
	ds_read_b128 v[16:19], v161 offset:2048
	ds_read_b128 v[20:23], v161 offset:3072
	ds_read_b128 v[128:131], v162
	ds_read_b128 v[132:135], v162 offset:1024
	ds_read_b128 v[136:139], v162 offset:2048
	ds_read_b128 v[140:143], v162 offset:3072
	ds_read_b128 v[8:11], v159 offset:32768
	ds_read_b128 v[12:15], v159 offset:33792
	ds_read_b128 v[24:27], v159 offset:34816
	ds_read_b128 v[28:31], v159 offset:35840
	ds_read_b128 v[32:35], v159 offset:36864
	ds_read_b128 v[36:39], v159 offset:37888
	ds_read_b128 v[40:43], v159 offset:38912
	ds_read_b128 v[44:47], v159 offset:39936
	s_add_u32 s44, s52, 0x20000
	s_addc_u32 s45, s53, 0
	s_mov_b32 m0, s67
	s_nop 0
	global_load_lds_dwordx4 v153, s[44:45]
	s_nop 0
	s_mov_b32 m0, s68
	s_nop 0
	global_load_lds_dwordx4 v155, s[44:45]
	s_waitcnt vmcnt(8)
	s_waitcnt lgkmcnt(0)
	s_barrier
	s_setprio 1
	v_mfma_scale_f32_16x16x128_f8f6f4 v[124:127], v[0:7], v[8:15], v[124:127], v160, v160 op_sel_hi:[0,0,0]
	v_mfma_scale_f32_16x16x128_f8f6f4 v[120:123], v[16:23], v[8:15], v[120:123], v160, v160 op_sel_hi:[0,0,0]
	v_mfma_scale_f32_16x16x128_f8f6f4 v[116:119], v[0:7], v[24:31], v[116:119], v160, v160 op_sel_hi:[0,0,0]
	v_mfma_scale_f32_16x16x128_f8f6f4 v[112:115], v[16:23], v[24:31], v[112:115], v160, v160 op_sel_hi:[0,0,0]
	v_mfma_scale_f32_16x16x128_f8f6f4 v[92:95], v[0:7], v[32:39], v[204:207], v160, v160 op_sel_hi:[0,0,0]
	v_mfma_scale_f32_16x16x128_f8f6f4 v[88:91], v[16:23], v[32:39], v[208:211], v160, v160 op_sel_hi:[0,0,0]
	v_mfma_scale_f32_16x16x128_f8f6f4 v[76:79], v[0:7], v[40:47], v[212:215], v160, v160 op_sel_hi:[0,0,0]
	v_mfma_scale_f32_16x16x128_f8f6f4 v[72:75], v[16:23], v[40:47], v[216:219], v160, v160 op_sel_hi:[0,0,0]
	v_mfma_scale_f32_16x16x128_f8f6f4 v[108:111], v[128:135], v[8:15], v[108:111], v160, v160 op_sel_hi:[0,0,0]
	v_mfma_scale_f32_16x16x128_f8f6f4 v[104:107], v[136:143], v[8:15], v[104:107], v160, v160 op_sel_hi:[0,0,0]
	v_mfma_scale_f32_16x16x128_f8f6f4 v[100:103], v[128:135], v[24:31], v[100:103], v160, v160 op_sel_hi:[0,0,0]
	v_mfma_scale_f32_16x16x128_f8f6f4 v[96:99], v[136:143], v[24:31], v[96:99], v160, v160 op_sel_hi:[0,0,0]
	v_mfma_scale_f32_16x16x128_f8f6f4 v[84:87], v[128:135], v[32:39], v[172:175], v160, v160 op_sel_hi:[0,0,0]
	v_mfma_scale_f32_16x16x128_f8f6f4 v[80:83], v[136:143], v[32:39], v[176:179], v160, v160 op_sel_hi:[0,0,0]
	v_mfma_scale_f32_16x16x128_f8f6f4 v[68:71], v[128:135], v[40:47], v[180:183], v160, v160 op_sel_hi:[0,0,0]
	v_mfma_scale_f32_16x16x128_f8f6f4 v[64:67], v[136:143], v[40:47], v[184:187], v160, v160 op_sel_hi:[0,0,0]
	s_setprio 0
	s_barrier
	ds_read_b128 v[32:35], v159 offset:49152
	ds_read_b128 v[36:39], v159 offset:50176
	ds_read_b128 v[144:147], v159 offset:51200
	ds_read_b128 v[148:151], v159 offset:52224
	ds_read_b128 v[164:167], v159 offset:53248
	ds_read_b128 v[168:171], v159 offset:54272
	ds_read_b128 v[172:175], v159 offset:55296
	ds_read_b128 v[176:179], v159 offset:56320
	s_add_u32 s44, s50, 0x80
	s_addc_u32 s45, s51, 0
	s_mov_b32 m0, s70
	s_nop 0
	global_load_lds_dwordx4 v154, s[44:45]
	s_nop 0
	s_mov_b32 m0, s71
	s_nop 0
	global_load_lds_dwordx4 v156, s[44:45]
	s_add_u32 s44, s50, 0x20080
	s_addc_u32 s45, s51, 0
	s_mov_b32 m0, s74
	s_nop 0
	global_load_lds_dwordx4 v154, s[44:45]
	s_nop 0
	s_mov_b32 m0, s75
	s_nop 0
	global_load_lds_dwordx4 v156, s[44:45]
	s_mov_b32 m0, s72
	s_nop 0
	global_load_lds_dwordx4 v153, s[48:49]
	s_nop 0
	s_mov_b32 m0, s73
	s_nop 0
	global_load_lds_dwordx4 v155, s[48:49]
	s_waitcnt vmcnt(8)
	s_waitcnt lgkmcnt(0)
	s_barrier
	s_setprio 1
	v_mfma_scale_f32_16x16x128_f8f6f4 v[60:63], v[0:7], v[32:39], v[60:63], v160, v160 op_sel_hi:[0,0,0]
	v_mfma_scale_f32_16x16x128_f8f6f4 v[56:59], v[16:23], v[32:39], v[56:59], v160, v160 op_sel_hi:[0,0,0]
	v_mfma_scale_f32_16x16x128_f8f6f4 v[44:47], v[0:7], v[144:151], v[188:191], v160, v160 op_sel_hi:[0,0,0]
	v_mfma_scale_f32_16x16x128_f8f6f4 v[40:43], v[16:23], v[144:151], v[192:195], v160, v160 op_sel_hi:[0,0,0]
	v_mfma_scale_f32_16x16x128_f8f6f4 v[28:31], v[0:7], v[164:171], v[196:199], v160, v160 op_sel_hi:[0,0,0]
	v_mfma_scale_f32_16x16x128_f8f6f4 v[24:27], v[16:23], v[164:171], v[200:203], v160, v160 op_sel_hi:[0,0,0]
	v_mfma_scale_f32_16x16x128_f8f6f4 v[12:15], v[0:7], v[172:179], v[220:223], v160, v160 op_sel_hi:[0,0,0]
	v_mfma_scale_f32_16x16x128_f8f6f4 v[8:11], v[16:23], v[172:179], v[224:227], v160, v160 op_sel_hi:[0,0,0]
	v_mfma_scale_f32_16x16x128_f8f6f4 v[52:55], v[128:135], v[32:39], v[52:55], v160, v160 op_sel_hi:[0,0,0]
	v_mfma_scale_f32_16x16x128_f8f6f4 v[48:51], v[136:143], v[32:39], v[48:51], v160, v160 op_sel_hi:[0,0,0]
	v_mfma_scale_f32_16x16x128_f8f6f4 v[36:39], v[128:135], v[144:151], v[228:231], v160, v160 op_sel_hi:[0,0,0]
	v_mfma_scale_f32_16x16x128_f8f6f4 v[32:35], v[136:143], v[144:151], v[232:235], v160, v160 op_sel_hi:[0,0,0]
	v_mfma_scale_f32_16x16x128_f8f6f4 v[20:23], v[128:135], v[164:171], v[236:239], v160, v160 op_sel_hi:[0,0,0]
	v_mfma_scale_f32_16x16x128_f8f6f4 v[16:19], v[136:143], v[164:171], v[240:243], v160, v160 op_sel_hi:[0,0,0]
	v_mfma_scale_f32_16x16x128_f8f6f4 v[4:7], v[128:135], v[172:179], v[244:247], v160, v160 op_sel_hi:[0,0,0]
	v_mfma_scale_f32_16x16x128_f8f6f4 v[0:3], v[136:143], v[172:179], v[248:251], v160, v160 op_sel_hi:[0,0,0]
	s_setprio 0
	s_barrier
	s_add_i32 s86, s86, 2
	s_add_u32 s84, s84, 0x100
	s_addc_u32 s85, s85, 0
	s_cmp_gt_u32 s86, 5
	s_mov_b64 s[44:45], s[46:47]
	s_cbranch_scc0 .LBB0_1528
	s_and_b64 vcc, exec, s[14:15]
	s_cbranch_vccz .LBB0_1531
	s_barrier

; #define PG8_WAIT_V(n) asm volatile("s_waitcnt vmcnt(" #n ")" ::: "memory")
; #define PG8_WAIT_L(n) asm volatile("s_waitcnt lgkmcnt(" #n ")" ::: "memory")
; #define PG8_BAR __builtin_amdgcn_s_barrier()
; #define PG8_SCHED __builtin_amdgcn_sched_barrier(0)
; #define PG8_STAGE_A(b, h, p) do { if constexpr (GATHER) { if ((h) == 0) PG8_STAGE(PG8_SA(b, h), p, vA0); else PG8_STAGE(PG8_SA(b, h), p, vA1); } else PG8_STAGE(PG8_SA(b, h), (p) + ((h) ? hstepA : (size_t)0), voffA); } while (0)
; #define PG8_GOFF1(un, h, d) do { int tz_ = tid; asm volatile("" : "+v"(tz_)); _Pragma("unroll") for (int i_ = 0; i_ < 2; ++i_) { int R_, C_; stage_rc(tz_ * 16 + i_ * 8192, R_, C_); \
;         d[i_] = S.gather(un, R_ + (h) * HALF) + (unsigned)C_ * 2u; } } while (0)
; template <class Epi, class Sched, bool ALIGN_EPI = true, bool SP2 = true, bool FP8 = false, bool GATHER = false>
; __device__ __forceinline__ void gemm_phase(LAS unsigned char* lds, const Dims g, const Sched& S, const Epi& E, const int wv) {
;     ...
;             PG8_LDB(B0, 0, 0); PG8_LDB(B1, 0, 1); PG8_SCHED; PG8_LDA(At, 0, 0); PG8_STAGE_A(1, 1, a1);
;             if constexpr (GATHER) { if (last) PG8_GOFF1(un_, 1, vA1); }
;             PG8_WAIT_V(8); PG8_WAIT_L(0); PG8_BAR; PG8_MMA(0, 0, At, B0); PG8_MMA(0, 1, At, B1); PG8_BAR; PG8_SCHED;
;             PG8_LDA(At, 0, 1); PG8_STAGE(PG8_SB(0, 0), b2, voffB); PG8_STAGE(PG8_SB(0, 1), b2 + hstepB, voffB); PG8_STAGE_A(0, 0, a2);
;             PG8_WAIT_V(8); PG8_WAIT_L(0); PG8_BAR; PG8_MMA(1, 0, At, B0); PG8_MMA(1, 1, At, B1); PG8_BAR; PG8_SCHED;
.LBB0_1670:
	ds_read_b128 v[154:157], v145
	ds_read_b128 v[158:161], v145 offset:1024
	ds_read_b128 v[162:165], v145 offset:2048
	ds_read_b128 v[166:169], v145 offset:3072
	ds_read_b128 v[170:173], v146
	ds_read_b128 v[174:177], v146 offset:1024
	ds_read_b128 v[178:181], v146 offset:2048
	ds_read_b128 v[182:185], v146 offset:3072
	s_add_u32 s42, s40, 0x100
	s_addc_u32 s43, s41, 0
	s_cmp_eq_u32 s25, 4
	s_cselect_b32 s48, s36, s42
	s_cselect_b32 s49, s37, s43
	s_cselect_b32 s46, s38, s5
	s_cselect_b32 s47, s39, s6
	s_add_u32 s44, s48, 0x80
	s_addc_u32 s45, s49, 0
	ds_read_b128 v[186:189], v147
	ds_read_b128 v[190:193], v147 offset:1024
	ds_read_b128 v[194:197], v147 offset:2048
	ds_read_b128 v[198:201], v147 offset:3072
	ds_read_b128 v[202:205], v147 offset:4096
	ds_read_b128 v[206:209], v147 offset:5120
	ds_read_b128 v[210:213], v147 offset:6144
	ds_read_b128 v[214:217], v147 offset:7168
	s_add_u32 s40, s40, 0x20080
	s_addc_u32 s41, s41, 0
	s_mov_b32 m0, s71
	s_nop 0
	global_load_lds_dwordx4 v255, s[40:41]
	s_nop 0
	s_mov_b32 m0, s72
	s_nop 0
	global_load_lds_dwordx4 v143, s[40:41]
	s_waitcnt vmcnt(8)
	s_waitcnt lgkmcnt(0)
	s_barrier
	s_setprio 1
	v_mfma_scale_f32_16x16x128_f8f6f4 v[124:127], v[154:161], v[186:193], v[124:127], v148, v148 op_sel_hi:[0,0,0]
	v_mfma_scale_f32_16x16x128_f8f6f4 v[120:123], v[162:169], v[186:193], v[120:123], v148, v148 op_sel_hi:[0,0,0]
	v_mfma_scale_f32_16x16x128_f8f6f4 v[108:111], v[154:161], v[194:201], v[108:111], v148, v148 op_sel_hi:[0,0,0]
	v_mfma_scale_f32_16x16x128_f8f6f4 v[104:107], v[162:169], v[194:201], v[104:107], v148, v148 op_sel_hi:[0,0,0]
	v_mfma_scale_f32_16x16x128_f8f6f4 v[134:137], v[154:161], v[202:209], v[92:95], v148, v148 op_sel_hi:[0,0,0]
	v_mfma_scale_f32_16x16x128_f8f6f4 v[218:221], v[162:169], v[202:209], v[88:91], v148, v148 op_sel_hi:[0,0,0]
	v_mfma_scale_f32_16x16x128_f8f6f4 v[222:225], v[154:161], v[210:217], v[76:79], v148, v148 op_sel_hi:[0,0,0]
	v_mfma_scale_f32_16x16x128_f8f6f4 v[226:229], v[162:169], v[210:217], v[72:75], v148, v148 op_sel_hi:[0,0,0]
	v_mfma_scale_f32_16x16x128_f8f6f4 v[116:119], v[170:177], v[186:193], v[116:119], v148, v148 op_sel_hi:[0,0,0]
	v_mfma_scale_f32_16x16x128_f8f6f4 v[112:115], v[178:185], v[186:193], v[112:115], v148, v148 op_sel_hi:[0,0,0]
	v_mfma_scale_f32_16x16x128_f8f6f4 v[100:103], v[170:177], v[194:201], v[100:103], v148, v148 op_sel_hi:[0,0,0]
	v_mfma_scale_f32_16x16x128_f8f6f4 v[96:99], v[178:185], v[194:201], v[96:99], v148, v148 op_sel_hi:[0,0,0]
	v_mfma_scale_f32_16x16x128_f8f6f4 v[186:189], v[170:177], v[202:209], v[84:87], v148, v148 op_sel_hi:[0,0,0]
	v_mfma_scale_f32_16x16x128_f8f6f4 v[190:193], v[178:185], v[202:209], v[80:83], v148, v148 op_sel_hi:[0,0,0]
	v_mfma_scale_f32_16x16x128_f8f6f4 v[194:197], v[170:177], v[210:217], v[68:71], v148, v148 op_sel_hi:[0,0,0]
	v_mfma_scale_f32_16x16x128_f8f6f4 v[198:201], v[178:185], v[210:217], v[64:67], v148, v148 op_sel_hi:[0,0,0]
	s_setprio 0
	s_barrier
	s_nop 4
	ds_read_b128 v[64:67], v147 offset:16384
	ds_read_b128 v[68:71], v147 offset:17408
	ds_read_b128 v[72:75], v147 offset:18432
	ds_read_b128 v[76:79], v147 offset:19456
	ds_read_b128 v[80:83], v147 offset:20480
	ds_read_b128 v[84:87], v147 offset:21504
	ds_read_b128 v[88:91], v147 offset:22528
	ds_read_b128 v[92:95], v147 offset:23552
	s_mov_b32 m0, s57
	s_nop 0
	global_load_lds_dwordx4 v142, s[46:47]
	s_add_u32 s40, s46, 0x20000
	s_mov_b32 m0, s58
	s_nop 0
	global_load_lds_dwordx4 v144, s[46:47]
	s_addc_u32 s41, s47, 0
	s_mov_b32 m0, s59
	s_nop 0
	global_load_lds_dwordx4 v142, s[40:41]
	s_nop 0
	s_mov_b32 m0, s60
	s_nop 0
	global_load_lds_dwordx4 v144, s[40:41]
	s_nop 0
	s_mov_b32 m0, s56
	s_nop 0
	global_load_lds_dwordx4 v255, s[48:49]
	s_nop 0
	s_mov_b32 m0, s61
	s_nop 0
	global_load_lds_dwordx4 v143, s[48:49]
	s_waitcnt vmcnt(8)
	s_waitcnt lgkmcnt(0)
	s_barrier
	s_setprio 1
	v_mfma_scale_f32_16x16x128_f8f6f4 v[60:63], v[154:161], v[64:71], v[60:63], v148, v148 op_sel_hi:[0,0,0]
	v_mfma_scale_f32_16x16x128_f8f6f4 v[56:59], v[162:169], v[64:71], v[56:59], v148, v148 op_sel_hi:[0,0,0]
	v_mfma_scale_f32_16x16x128_f8f6f4 v[202:205], v[154:161], v[72:79], v[44:47], v148, v148 op_sel_hi:[0,0,0]
	v_mfma_scale_f32_16x16x128_f8f6f4 v[206:209], v[162:169], v[72:79], v[40:43], v148, v148 op_sel_hi:[0,0,0]
	v_mfma_scale_f32_16x16x128_f8f6f4 v[210:213], v[154:161], v[80:87], v[28:31], v148, v148 op_sel_hi:[0,0,0]
	v_mfma_scale_f32_16x16x128_f8f6f4 v[214:217], v[162:169], v[80:87], v[24:27], v148, v148 op_sel_hi:[0,0,0]
	v_mfma_scale_f32_16x16x128_f8f6f4 v[230:233], v[154:161], v[88:95], v[12:15], v148, v148 op_sel_hi:[0,0,0]
	v_mfma_scale_f32_16x16x128_f8f6f4 v[234:237], v[162:169], v[88:95], v[8:11], v148, v148 op_sel_hi:[0,0,0]
	v_mfma_scale_f32_16x16x128_f8f6f4 v[52:55], v[170:177], v[64:71], v[52:55], v148, v148 op_sel_hi:[0,0,0]
	v_mfma_scale_f32_16x16x128_f8f6f4 v[48:51], v[178:185], v[64:71], v[48:51], v148, v148 op_sel_hi:[0,0,0]
	v_mfma_scale_f32_16x16x128_f8f6f4 v[238:241], v[170:177], v[72:79], v[36:39], v148, v148 op_sel_hi:[0,0,0]
	v_mfma_scale_f32_16x16x128_f8f6f4 v[242:245], v[178:185], v[72:79], v[32:35], v148, v148 op_sel_hi:[0,0,0]
	v_mfma_scale_f32_16x16x128_f8f6f4 v[246:249], v[170:177], v[80:87], v[20:23], v148, v148 op_sel_hi:[0,0,0]
	v_mfma_scale_f32_16x16x128_f8f6f4 v[250:253], v[178:185], v[80:87], v[16:19], v148, v148 op_sel_hi:[0,0,0]
	v_mfma_scale_f32_16x16x128_f8f6f4 v[128:131], v[170:177], v[88:95], v[4:7], v148, v148 op_sel_hi:[0,0,0]
	v_mfma_scale_f32_16x16x128_f8f6f4 v[138:141], v[178:185], v[88:95], v[0:3], v148, v148 op_sel_hi:[0,0,0]
	s_setprio 0
	s_barrier
; #define PG8_WAIT_V(n) asm volatile("s_waitcnt vmcnt(" #n ")" ::: "memory")
; #define PG8_WAIT_L(n) asm volatile("s_waitcnt lgkmcnt(" #n ")" ::: "memory")
; #define PG8_BAR __builtin_amdgcn_s_barrier()
; #define PG8_SCHED __builtin_amdgcn_sched_barrier(0)
; #define PG8_STAGE_A(b, h, p) do { if constexpr (GATHER) { if ((h) == 0) PG8_STAGE(PG8_SA(b, h), p, vA0); else PG8_STAGE(PG8_SA(b, h), p, vA1); } else PG8_STAGE(PG8_SA(b, h), (p) + ((h) ? hstepA : (size_t)0), voffA); } while (0)
; template <class Epi, class Sched, bool ALIGN_EPI = true, bool SP2 = true, bool FP8 = false, bool GATHER = false>
; __device__ __forceinline__ void gemm_phase(LAS unsigned char* lds, const Dims g, const Sched& S, const Epi& E, const int wv) {
;     ...
;             PG8_LDB(B0, 1, 0); PG8_LDB(B1, 1, 1); PG8_SCHED; PG8_LDA(At, 1, 0); PG8_STAGE_A(0, 1, a2);
;             PG8_WAIT_V(8); PG8_WAIT_L(0); PG8_BAR; PG8_MMA(0, 0, At, B0); PG8_MMA(0, 1, At, B1); PG8_BAR; PG8_SCHED;
;             PG8_LDA(At, 1, 1); PG8_STAGE(PG8_SB(1, 0), b3, voffB); PG8_STAGE(PG8_SB(1, 1), b3 + hstepB, voffB); PG8_STAGE_A(1, 0, a3);
;             PG8_WAIT_V(8); PG8_WAIT_L(0); PG8_BAR; PG8_MMA(1, 0, At, B0); PG8_MMA(1, 1, At, B1); PG8_BAR; PG8_SCHED;
	s_nop 4
	ds_read_b128 v[0:3], v149
	ds_read_b128 v[4:7], v149 offset:1024
	ds_read_b128 v[16:19], v149 offset:2048
	ds_read_b128 v[20:23], v149 offset:3072
	ds_read_b128 v[154:157], v150
	ds_read_b128 v[158:161], v150 offset:1024
	ds_read_b128 v[162:165], v150 offset:2048
	ds_read_b128 v[166:169], v150 offset:3072
	ds_read_b128 v[8:11], v147 offset:32768
	ds_read_b128 v[12:15], v147 offset:33792
	ds_read_b128 v[24:27], v147 offset:34816
	ds_read_b128 v[28:31], v147 offset:35840
	ds_read_b128 v[32:35], v147 offset:36864
	ds_read_b128 v[36:39], v147 offset:37888
	ds_read_b128 v[40:43], v147 offset:38912
	ds_read_b128 v[44:47], v147 offset:39936
	s_add_u32 s40, s48, 0x20000
	s_addc_u32 s41, s49, 0
	s_mov_b32 m0, s62
	s_nop 0
	global_load_lds_dwordx4 v255, s[40:41]
	s_nop 0
	s_mov_b32 m0, s63
	s_nop 0
	global_load_lds_dwordx4 v143, s[40:41]
	s_waitcnt vmcnt(8)
	s_waitcnt lgkmcnt(0)
	s_barrier
	s_setprio 1
	v_mfma_scale_f32_16x16x128_f8f6f4 v[124:127], v[0:7], v[8:15], v[124:127], v148, v148 op_sel_hi:[0,0,0]
	v_mfma_scale_f32_16x16x128_f8f6f4 v[120:123], v[16:23], v[8:15], v[120:123], v148, v148 op_sel_hi:[0,0,0]
	v_mfma_scale_f32_16x16x128_f8f6f4 v[108:111], v[0:7], v[24:31], v[108:111], v148, v148 op_sel_hi:[0,0,0]
	v_mfma_scale_f32_16x16x128_f8f6f4 v[104:107], v[16:23], v[24:31], v[104:107], v148, v148 op_sel_hi:[0,0,0]
	v_mfma_scale_f32_16x16x128_f8f6f4 v[92:95], v[0:7], v[32:39], v[134:137], v148, v148 op_sel_hi:[0,0,0]
	v_mfma_scale_f32_16x16x128_f8f6f4 v[88:91], v[16:23], v[32:39], v[218:221], v148, v148 op_sel_hi:[0,0,0]
	v_mfma_scale_f32_16x16x128_f8f6f4 v[76:79], v[0:7], v[40:47], v[222:225], v148, v148 op_sel_hi:[0,0,0]
	v_mfma_scale_f32_16x16x128_f8f6f4 v[72:75], v[16:23], v[40:47], v[226:229], v148, v148 op_sel_hi:[0,0,0]
	v_mfma_scale_f32_16x16x128_f8f6f4 v[116:119], v[154:161], v[8:15], v[116:119], v148, v148 op_sel_hi:[0,0,0]
	v_mfma_scale_f32_16x16x128_f8f6f4 v[112:115], v[162:169], v[8:15], v[112:115], v148, v148 op_sel_hi:[0,0,0]
	v_mfma_scale_f32_16x16x128_f8f6f4 v[100:103], v[154:161], v[24:31], v[100:103], v148, v148 op_sel_hi:[0,0,0]
	v_mfma_scale_f32_16x16x128_f8f6f4 v[96:99], v[162:169], v[24:31], v[96:99], v148, v148 op_sel_hi:[0,0,0]
	v_mfma_scale_f32_16x16x128_f8f6f4 v[84:87], v[154:161], v[32:39], v[186:189], v148, v148 op_sel_hi:[0,0,0]
	v_mfma_scale_f32_16x16x128_f8f6f4 v[80:83], v[162:169], v[32:39], v[190:193], v148, v148 op_sel_hi:[0,0,0]
	v_mfma_scale_f32_16x16x128_f8f6f4 v[68:71], v[154:161], v[40:47], v[194:197], v148, v148 op_sel_hi:[0,0,0]
	v_mfma_scale_f32_16x16x128_f8f6f4 v[64:67], v[162:169], v[40:47], v[198:201], v148, v148 op_sel_hi:[0,0,0]
	s_setprio 0
	s_barrier
	ds_read_b128 v[32:35], v147 offset:49152
	ds_read_b128 v[36:39], v147 offset:50176
	ds_read_b128 v[170:173], v147 offset:51200
	ds_read_b128 v[174:177], v147 offset:52224
	ds_read_b128 v[178:181], v147 offset:53248
	ds_read_b128 v[182:185], v147 offset:54272
	ds_read_b128 v[186:189], v147 offset:55296
	ds_read_b128 v[190:193], v147 offset:56320
	s_add_u32 s40, s46, 0x80
	s_addc_u32 s41, s47, 0
	s_mov_b32 m0, s65
	s_nop 0
	global_load_lds_dwordx4 v142, s[40:41]
	s_nop 0
	s_mov_b32 m0, s66
	s_nop 0
	global_load_lds_dwordx4 v144, s[40:41]
	s_add_u32 s40, s46, 0x20080
	s_addc_u32 s41, s47, 0
	s_mov_b32 m0, s69
	s_nop 0
	global_load_lds_dwordx4 v142, s[40:41]
	s_nop 0
	s_mov_b32 m0, s70
	s_nop 0
	global_load_lds_dwordx4 v144, s[40:41]
	s_nop 0
	s_mov_b32 m0, s67
	s_nop 0
	global_load_lds_dwordx4 v255, s[44:45]
	s_nop 0
	s_mov_b32 m0, s68
	s_nop 0
	global_load_lds_dwordx4 v143, s[44:45]
	s_waitcnt vmcnt(8)
	s_waitcnt lgkmcnt(0)
	s_barrier
	s_setprio 1
	v_mfma_scale_f32_16x16x128_f8f6f4 v[60:63], v[0:7], v[32:39], v[60:63], v148, v148 op_sel_hi:[0,0,0]
	v_mfma_scale_f32_16x16x128_f8f6f4 v[56:59], v[16:23], v[32:39], v[56:59], v148, v148 op_sel_hi:[0,0,0]
	v_mfma_scale_f32_16x16x128_f8f6f4 v[44:47], v[0:7], v[170:177], v[202:205], v148, v148 op_sel_hi:[0,0,0]
	v_mfma_scale_f32_16x16x128_f8f6f4 v[40:43], v[16:23], v[170:177], v[206:209], v148, v148 op_sel_hi:[0,0,0]
	v_mfma_scale_f32_16x16x128_f8f6f4 v[28:31], v[0:7], v[178:185], v[210:213], v148, v148 op_sel_hi:[0,0,0]
	v_mfma_scale_f32_16x16x128_f8f6f4 v[24:27], v[16:23], v[178:185], v[214:217], v148, v148 op_sel_hi:[0,0,0]
	v_mfma_scale_f32_16x16x128_f8f6f4 v[12:15], v[0:7], v[186:193], v[230:233], v148, v148 op_sel_hi:[0,0,0]
	v_mfma_scale_f32_16x16x128_f8f6f4 v[8:11], v[16:23], v[186:193], v[234:237], v148, v148 op_sel_hi:[0,0,0]
	v_mfma_scale_f32_16x16x128_f8f6f4 v[52:55], v[154:161], v[32:39], v[52:55], v148, v148 op_sel_hi:[0,0,0]
	v_mfma_scale_f32_16x16x128_f8f6f4 v[48:51], v[162:169], v[32:39], v[48:51], v148, v148 op_sel_hi:[0,0,0]
	v_mfma_scale_f32_16x16x128_f8f6f4 v[36:39], v[154:161], v[170:177], v[238:241], v148, v148 op_sel_hi:[0,0,0]
	v_mfma_scale_f32_16x16x128_f8f6f4 v[32:35], v[162:169], v[170:177], v[242:245], v148, v148 op_sel_hi:[0,0,0]
	v_mfma_scale_f32_16x16x128_f8f6f4 v[20:23], v[154:161], v[178:185], v[246:249], v148, v148 op_sel_hi:[0,0,0]
	v_mfma_scale_f32_16x16x128_f8f6f4 v[16:19], v[162:169], v[178:185], v[250:253], v148, v148 op_sel_hi:[0,0,0]
	v_mfma_scale_f32_16x16x128_f8f6f4 v[4:7], v[154:161], v[186:193], v[128:131], v148, v148 op_sel_hi:[0,0,0]
	v_mfma_scale_f32_16x16x128_f8f6f4 v[0:3], v[162:169], v[186:193], v[138:141], v148, v148 op_sel_hi:[0,0,0]
	s_setprio 0
	s_barrier
	s_add_i32 s25, s25, 2
	s_add_u32 s5, s5, 0x100
	s_addc_u32 s6, s6, 0
	s_cmp_gt_u32 s25, 5
	s_mov_b64 s[40:41], s[42:43]
	s_cbranch_scc0 .LBB0_1670
	s_and_b64 vcc, exec, s[16:17]
	s_cbranch_vccz .LBB0_1673
	s_barrier

; #define PG8_WAIT_V(n) asm volatile("s_waitcnt vmcnt(" #n ")" ::: "memory")
; #define PG8_WAIT_L(n) asm volatile("s_waitcnt lgkmcnt(" #n ")" ::: "memory")
; #define PG8_BAR __builtin_amdgcn_s_barrier()
; #define PG8_SCHED __builtin_amdgcn_sched_barrier(0)
; #define PG8_STAGE_A(b, h, p) do { if constexpr (GATHER) { if ((h) == 0) PG8_STAGE(PG8_SA(b, h), p, vA0); else PG8_STAGE(PG8_SA(b, h), p, vA1); } else PG8_STAGE(PG8_SA(b, h), (p) + ((h) ? hstepA : (size_t)0), voffA); } while (0)
; #define PG8_GOFF1(un, h, d) do { int tz_ = tid; asm volatile("" : "+v"(tz_)); _Pragma("unroll") for (int i_ = 0; i_ < 2; ++i_) { int R_, C_; stage_rc(tz_ * 16 + i_ * 8192, R_, C_); \
;         d[i_] = S.gather(un, R_ + (h) * HALF) + (unsigned)C_ * 2u; } } while (0)
; template <class Epi, class Sched, bool ALIGN_EPI = true, bool SP2 = true, bool FP8 = false, bool GATHER = false>
; __device__ __forceinline__ void gemm_phase(LAS unsigned char* lds, const Dims g, const Sched& S, const Epi& E, const int wv) {
;     ...
;             PG8_LDB(B0, 0, 0); PG8_LDB(B1, 0, 1); PG8_SCHED; PG8_LDA(At, 0, 0); PG8_STAGE_A(1, 1, a1);
;             if constexpr (GATHER) { if (last) PG8_GOFF1(un_, 1, vA1); }
;             PG8_WAIT_V(8); PG8_WAIT_L(0); PG8_BAR; PG8_MMA(0, 0, At, B0); PG8_MMA(0, 1, At, B1); PG8_BAR; PG8_SCHED;
;             PG8_LDA(At, 0, 1); PG8_STAGE(PG8_SB(0, 0), b2, voffB); PG8_STAGE(PG8_SB(0, 1), b2 + hstepB, voffB); PG8_STAGE_A(0, 0, a2);
;             PG8_WAIT_V(8); PG8_WAIT_L(0); PG8_BAR; PG8_MMA(1, 0, At, B0); PG8_MMA(1, 1, At, B1); PG8_BAR; PG8_SCHED;
.LBB0_1913:
	ds_read_b128 v[132:135], v151
	ds_read_b128 v[136:139], v151 offset:1024
	ds_read_b128 v[158:161], v151 offset:2048
	ds_read_b128 v[162:165], v151 offset:3072
	ds_read_b128 v[166:169], v152
	ds_read_b128 v[170:173], v152 offset:1024
	ds_read_b128 v[174:177], v152 offset:2048
	ds_read_b128 v[178:181], v152 offset:3072
	s_cmp_eq_u32 s82, 12
	s_cselect_b32 s46, s26, s80
	s_cselect_b32 s47, s27, s81
	s_cselect_b32 s44, s36, s23
	s_cselect_b32 s45, s37, s25
	s_add_u32 s42, s46, 0x80
	s_addc_u32 s43, s47, 0
	ds_read_b128 v[182:185], v153
	ds_read_b128 v[186:189], v153 offset:1024
	ds_read_b128 v[190:193], v153 offset:2048
	ds_read_b128 v[194:197], v153 offset:3072
	ds_read_b128 v[198:201], v153 offset:4096
	ds_read_b128 v[202:205], v153 offset:5120
	ds_read_b128 v[206:209], v153 offset:6144
	ds_read_b128 v[210:213], v153 offset:7168
	s_mov_b32 m0, s72
	s_nop 0
	global_load_lds_dwordx4 v147, s[40:41]
	s_nop 0
	s_mov_b32 m0, s73
	s_nop 0
	global_load_lds_dwordx4 v149, s[40:41]
	s_waitcnt vmcnt(8)
	s_waitcnt lgkmcnt(0)
	s_barrier
	s_setprio 1
	v_mfma_scale_f32_16x16x128_f8f6f4 v[124:127], v[132:139], v[182:189], v[124:127], v154, v154 op_sel_hi:[0,0,0]
	v_mfma_scale_f32_16x16x128_f8f6f4 v[120:123], v[158:165], v[182:189], v[120:123], v154, v154 op_sel_hi:[0,0,0]
	v_mfma_scale_f32_16x16x128_f8f6f4 v[116:119], v[132:139], v[190:197], v[116:119], v154, v154 op_sel_hi:[0,0,0]
	v_mfma_scale_f32_16x16x128_f8f6f4 v[104:107], v[158:165], v[190:197], v[104:107], v154, v154 op_sel_hi:[0,0,0]
	v_mfma_scale_f32_16x16x128_f8f6f4 v[100:103], v[132:139], v[198:205], v[100:103], v154, v154 op_sel_hi:[0,0,0]
	v_mfma_scale_f32_16x16x128_f8f6f4 v[140:143], v[158:165], v[198:205], v[88:91], v154, v154 op_sel_hi:[0,0,0]
	v_mfma_scale_f32_16x16x128_f8f6f4 v[214:217], v[132:139], v[206:213], v[84:87], v154, v154 op_sel_hi:[0,0,0]
	v_mfma_scale_f32_16x16x128_f8f6f4 v[218:221], v[158:165], v[206:213], v[72:75], v154, v154 op_sel_hi:[0,0,0]
	v_mfma_scale_f32_16x16x128_f8f6f4 v[112:115], v[166:173], v[182:189], v[112:115], v154, v154 op_sel_hi:[0,0,0]
	v_mfma_scale_f32_16x16x128_f8f6f4 v[108:111], v[174:181], v[182:189], v[108:111], v154, v154 op_sel_hi:[0,0,0]
	v_mfma_scale_f32_16x16x128_f8f6f4 v[96:99], v[166:173], v[190:197], v[96:99], v154, v154 op_sel_hi:[0,0,0]
	v_mfma_scale_f32_16x16x128_f8f6f4 v[182:185], v[174:181], v[190:197], v[92:95], v154, v154 op_sel_hi:[0,0,0]
	v_mfma_scale_f32_16x16x128_f8f6f4 v[186:189], v[166:173], v[198:205], v[80:83], v154, v154 op_sel_hi:[0,0,0]
	v_mfma_scale_f32_16x16x128_f8f6f4 v[190:193], v[174:181], v[198:205], v[76:79], v154, v154 op_sel_hi:[0,0,0]
	v_mfma_scale_f32_16x16x128_f8f6f4 v[194:197], v[166:173], v[206:213], v[68:71], v154, v154 op_sel_hi:[0,0,0]
	v_mfma_scale_f32_16x16x128_f8f6f4 v[198:201], v[174:181], v[206:213], v[64:67], v154, v154 op_sel_hi:[0,0,0]
	s_setprio 0
	s_barrier
	s_nop 4
	ds_read_b128 v[64:67], v153 offset:16384
	ds_read_b128 v[68:71], v153 offset:17408
	ds_read_b128 v[72:75], v153 offset:18432
	ds_read_b128 v[76:79], v153 offset:19456
	ds_read_b128 v[80:83], v153 offset:20480
	ds_read_b128 v[84:87], v153 offset:21504
	ds_read_b128 v[88:91], v153 offset:22528
	ds_read_b128 v[92:95], v153 offset:23552
	s_mov_b32 m0, s55
	s_nop 0
	global_load_lds_dwordx4 v148, s[44:45]
	s_add_u32 s84, s44, 0x40000
	s_mov_b32 m0, s56
	s_nop 0
	global_load_lds_dwordx4 v150, s[44:45]
	s_addc_u32 s85, s45, 0
	s_mov_b32 m0, s57
	s_nop 0
	global_load_lds_dwordx4 v148, s[84:85]
	s_nop 0
	s_mov_b32 m0, s58
	s_nop 0
	global_load_lds_dwordx4 v150, s[84:85]
	s_nop 0
	s_mov_b32 m0, s54
	s_nop 0
	global_load_lds_dwordx4 v147, s[46:47]
	s_nop 0
	s_mov_b32 m0, s59
	s_nop 0
	global_load_lds_dwordx4 v149, s[46:47]
	s_waitcnt vmcnt(8)
	s_waitcnt lgkmcnt(0)
	s_barrier
	s_setprio 1
	v_mfma_scale_f32_16x16x128_f8f6f4 v[60:63], v[132:139], v[64:71], v[60:63], v154, v154 op_sel_hi:[0,0,0]
	v_mfma_scale_f32_16x16x128_f8f6f4 v[56:59], v[158:165], v[64:71], v[56:59], v154, v154 op_sel_hi:[0,0,0]
	v_mfma_scale_f32_16x16x128_f8f6f4 v[48:51], v[132:139], v[72:79], v[48:51], v154, v154 op_sel_hi:[0,0,0]
	v_mfma_scale_f32_16x16x128_f8f6f4 v[202:205], v[158:165], v[72:79], v[40:43], v154, v154 op_sel_hi:[0,0,0]
	v_mfma_scale_f32_16x16x128_f8f6f4 v[206:209], v[132:139], v[80:87], v[32:35], v154, v154 op_sel_hi:[0,0,0]
	v_mfma_scale_f32_16x16x128_f8f6f4 v[210:213], v[158:165], v[80:87], v[24:27], v154, v154 op_sel_hi:[0,0,0]
	v_mfma_scale_f32_16x16x128_f8f6f4 v[222:225], v[132:139], v[88:95], v[16:19], v154, v154 op_sel_hi:[0,0,0]
	v_mfma_scale_f32_16x16x128_f8f6f4 v[226:229], v[158:165], v[88:95], v[8:11], v154, v154 op_sel_hi:[0,0,0]
	v_mfma_scale_f32_16x16x128_f8f6f4 v[52:55], v[166:173], v[64:71], v[52:55], v154, v154 op_sel_hi:[0,0,0]
	v_mfma_scale_f32_16x16x128_f8f6f4 v[230:233], v[174:181], v[64:71], v[44:47], v154, v154 op_sel_hi:[0,0,0]
	v_mfma_scale_f32_16x16x128_f8f6f4 v[234:237], v[166:173], v[72:79], v[36:39], v154, v154 op_sel_hi:[0,0,0]
	v_mfma_scale_f32_16x16x128_f8f6f4 v[238:241], v[174:181], v[72:79], v[28:31], v154, v154 op_sel_hi:[0,0,0]
	v_mfma_scale_f32_16x16x128_f8f6f4 v[242:245], v[166:173], v[80:87], v[20:23], v154, v154 op_sel_hi:[0,0,0]
	v_mfma_scale_f32_16x16x128_f8f6f4 v[246:249], v[174:181], v[80:87], v[12:15], v154, v154 op_sel_hi:[0,0,0]
	v_mfma_scale_f32_16x16x128_f8f6f4 v[250:253], v[166:173], v[88:95], v[4:7], v154, v154 op_sel_hi:[0,0,0]
	v_mfma_scale_f32_16x16x128_f8f6f4 v[128:131], v[174:181], v[88:95], v[0:3], v154, v154 op_sel_hi:[0,0,0]
	s_setprio 0
	s_barrier
; #define PG8_WAIT_V(n) asm volatile("s_waitcnt vmcnt(" #n ")" ::: "memory")
; #define PG8_WAIT_L(n) asm volatile("s_waitcnt lgkmcnt(" #n ")" ::: "memory")
; #define PG8_BAR __builtin_amdgcn_s_barrier()
; #define PG8_SCHED __builtin_amdgcn_sched_barrier(0)
; #define PG8_STAGE_A(b, h, p) do { if constexpr (GATHER) { if ((h) == 0) PG8_STAGE(PG8_SA(b, h), p, vA0); else PG8_STAGE(PG8_SA(b, h), p, vA1); } else PG8_STAGE(PG8_SA(b, h), (p) + ((h) ? hstepA : (size_t)0), voffA); } while (0)
; template <class Epi, class Sched, bool ALIGN_EPI = true, bool SP2 = true, bool FP8 = false, bool GATHER = false>
; __device__ __forceinline__ void gemm_phase(LAS unsigned char* lds, const Dims g, const Sched& S, const Epi& E, const int wv) {
;     ...
;             PG8_LDB(B0, 1, 0); PG8_LDB(B1, 1, 1); PG8_SCHED; PG8_LDA(At, 1, 0); PG8_STAGE_A(0, 1, a2);
;             PG8_WAIT_V(8); PG8_WAIT_L(0); PG8_BAR; PG8_MMA(0, 0, At, B0); PG8_MMA(0, 1, At, B1); PG8_BAR; PG8_SCHED;
;             PG8_LDA(At, 1, 1); PG8_STAGE(PG8_SB(1, 0), b3, voffB); PG8_STAGE(PG8_SB(1, 1), b3 + hstepB, voffB); PG8_STAGE_A(1, 0, a3);
;             PG8_WAIT_V(8); PG8_WAIT_L(0); PG8_BAR; PG8_MMA(1, 0, At, B0); PG8_MMA(1, 1, At, B1); PG8_BAR; PG8_SCHED;
	s_nop 4
	ds_read_b128 v[0:3], v155
	ds_read_b128 v[4:7], v155 offset:1024
	ds_read_b128 v[8:11], v155 offset:2048
	ds_read_b128 v[12:15], v155 offset:3072
	ds_read_b128 v[132:135], v156
	ds_read_b128 v[136:139], v156 offset:1024
	ds_read_b128 v[158:161], v156 offset:2048
	ds_read_b128 v[162:165], v156 offset:3072
	ds_read_b128 v[16:19], v153 offset:32768
	ds_read_b128 v[20:23], v153 offset:33792
	ds_read_b128 v[24:27], v153 offset:34816
	ds_read_b128 v[28:31], v153 offset:35840
	ds_read_b128 v[32:35], v153 offset:36864
	ds_read_b128 v[36:39], v153 offset:37888
	ds_read_b128 v[40:43], v153 offset:38912
	ds_read_b128 v[44:47], v153 offset:39936
	s_add_u32 s46, s46, 0x40000
	s_addc_u32 s47, s47, 0
	s_mov_b32 m0, s60
	s_nop 0
	global_load_lds_dwordx4 v147, s[46:47]
	s_nop 0
	s_mov_b32 m0, s61
	s_nop 0
	global_load_lds_dwordx4 v149, s[46:47]
	s_waitcnt vmcnt(8)
	s_waitcnt lgkmcnt(0)
	s_barrier
	s_setprio 1
	v_mfma_scale_f32_16x16x128_f8f6f4 v[124:127], v[0:7], v[16:23], v[124:127], v154, v154 op_sel_hi:[0,0,0]
	v_mfma_scale_f32_16x16x128_f8f6f4 v[120:123], v[8:15], v[16:23], v[120:123], v154, v154 op_sel_hi:[0,0,0]
	v_mfma_scale_f32_16x16x128_f8f6f4 v[116:119], v[0:7], v[24:31], v[116:119], v154, v154 op_sel_hi:[0,0,0]
	v_mfma_scale_f32_16x16x128_f8f6f4 v[104:107], v[8:15], v[24:31], v[104:107], v154, v154 op_sel_hi:[0,0,0]
	v_mfma_scale_f32_16x16x128_f8f6f4 v[100:103], v[0:7], v[32:39], v[100:103], v154, v154 op_sel_hi:[0,0,0]
	v_mfma_scale_f32_16x16x128_f8f6f4 v[88:91], v[8:15], v[32:39], v[140:143], v154, v154 op_sel_hi:[0,0,0]
	v_mfma_scale_f32_16x16x128_f8f6f4 v[84:87], v[0:7], v[40:47], v[214:217], v154, v154 op_sel_hi:[0,0,0]
	v_mfma_scale_f32_16x16x128_f8f6f4 v[72:75], v[8:15], v[40:47], v[218:221], v154, v154 op_sel_hi:[0,0,0]
	v_mfma_scale_f32_16x16x128_f8f6f4 v[112:115], v[132:139], v[16:23], v[112:115], v154, v154 op_sel_hi:[0,0,0]
	v_mfma_scale_f32_16x16x128_f8f6f4 v[108:111], v[158:165], v[16:23], v[108:111], v154, v154 op_sel_hi:[0,0,0]
	v_mfma_scale_f32_16x16x128_f8f6f4 v[96:99], v[132:139], v[24:31], v[96:99], v154, v154 op_sel_hi:[0,0,0]
	v_mfma_scale_f32_16x16x128_f8f6f4 v[92:95], v[158:165], v[24:31], v[182:185], v154, v154 op_sel_hi:[0,0,0]
	v_mfma_scale_f32_16x16x128_f8f6f4 v[80:83], v[132:139], v[32:39], v[186:189], v154, v154 op_sel_hi:[0,0,0]
	v_mfma_scale_f32_16x16x128_f8f6f4 v[76:79], v[158:165], v[32:39], v[190:193], v154, v154 op_sel_hi:[0,0,0]
	v_mfma_scale_f32_16x16x128_f8f6f4 v[68:71], v[132:139], v[40:47], v[194:197], v154, v154 op_sel_hi:[0,0,0]
	v_mfma_scale_f32_16x16x128_f8f6f4 v[64:67], v[158:165], v[40:47], v[198:201], v154, v154 op_sel_hi:[0,0,0]
	s_setprio 0
	s_barrier
	ds_read_b128 v[166:169], v153 offset:49152
	ds_read_b128 v[170:173], v153 offset:50176
	ds_read_b128 v[174:177], v153 offset:51200
	ds_read_b128 v[178:181], v153 offset:52224
	ds_read_b128 v[182:185], v153 offset:53248
	ds_read_b128 v[186:189], v153 offset:54272
	ds_read_b128 v[190:193], v153 offset:55296
	ds_read_b128 v[194:197], v153 offset:56320
	s_add_u32 s46, s44, 0x80
	s_addc_u32 s47, s45, 0
	s_mov_b32 m0, s66
	s_nop 0
	global_load_lds_dwordx4 v148, s[46:47]
	s_add_u32 s44, s44, 0x40080
	s_mov_b32 m0, s67
	s_nop 0
	global_load_lds_dwordx4 v150, s[46:47]
	s_addc_u32 s45, s45, 0
	s_mov_b32 m0, s70
	s_nop 0
	global_load_lds_dwordx4 v148, s[44:45]
	s_nop 0
	s_mov_b32 m0, s71
	s_nop 0
	global_load_lds_dwordx4 v150, s[44:45]
	s_mov_b32 m0, s68
	s_nop 0
	global_load_lds_dwordx4 v147, s[42:43]
	s_nop 0
	s_mov_b32 m0, s69
	s_nop 0
	global_load_lds_dwordx4 v149, s[42:43]
	s_waitcnt vmcnt(8)
	s_waitcnt lgkmcnt(0)
	s_barrier
	s_setprio 1
	v_mfma_scale_f32_16x16x128_f8f6f4 v[60:63], v[0:7], v[166:173], v[60:63], v154, v154 op_sel_hi:[0,0,0]
	v_mfma_scale_f32_16x16x128_f8f6f4 v[56:59], v[8:15], v[166:173], v[56:59], v154, v154 op_sel_hi:[0,0,0]
	v_mfma_scale_f32_16x16x128_f8f6f4 v[48:51], v[0:7], v[174:181], v[48:51], v154, v154 op_sel_hi:[0,0,0]
	v_mfma_scale_f32_16x16x128_f8f6f4 v[40:43], v[8:15], v[174:181], v[202:205], v154, v154 op_sel_hi:[0,0,0]
	v_mfma_scale_f32_16x16x128_f8f6f4 v[32:35], v[0:7], v[182:189], v[206:209], v154, v154 op_sel_hi:[0,0,0]
	v_mfma_scale_f32_16x16x128_f8f6f4 v[24:27], v[8:15], v[182:189], v[210:213], v154, v154 op_sel_hi:[0,0,0]
	v_mfma_scale_f32_16x16x128_f8f6f4 v[16:19], v[0:7], v[190:197], v[222:225], v154, v154 op_sel_hi:[0,0,0]
	v_mfma_scale_f32_16x16x128_f8f6f4 v[8:11], v[8:15], v[190:197], v[226:229], v154, v154 op_sel_hi:[0,0,0]
	v_mfma_scale_f32_16x16x128_f8f6f4 v[52:55], v[132:139], v[166:173], v[52:55], v154, v154 op_sel_hi:[0,0,0]
	v_mfma_scale_f32_16x16x128_f8f6f4 v[44:47], v[158:165], v[166:173], v[230:233], v154, v154 op_sel_hi:[0,0,0]
	v_mfma_scale_f32_16x16x128_f8f6f4 v[36:39], v[132:139], v[174:181], v[234:237], v154, v154 op_sel_hi:[0,0,0]
	v_mfma_scale_f32_16x16x128_f8f6f4 v[28:31], v[158:165], v[174:181], v[238:241], v154, v154 op_sel_hi:[0,0,0]
	v_mfma_scale_f32_16x16x128_f8f6f4 v[20:23], v[132:139], v[182:189], v[242:245], v154, v154 op_sel_hi:[0,0,0]
	v_mfma_scale_f32_16x16x128_f8f6f4 v[12:15], v[158:165], v[182:189], v[246:249], v154, v154 op_sel_hi:[0,0,0]
	v_mfma_scale_f32_16x16x128_f8f6f4 v[4:7], v[132:139], v[190:197], v[250:253], v154, v154 op_sel_hi:[0,0,0]
	v_mfma_scale_f32_16x16x128_f8f6f4 v[0:3], v[158:165], v[190:197], v[128:131], v154, v154 op_sel_hi:[0,0,0]
	s_setprio 0
	s_barrier
	s_add_i32 s82, s82, 2
	s_add_u32 s23, s23, 0x100
	s_addc_u32 s25, s25, 0
	s_add_u32 s80, s80, 0x100
	s_addc_u32 s81, s81, 0
	s_add_u32 s40, s40, 0x100
	s_addc_u32 s41, s41, 0
	s_cmp_gt_u32 s82, 13
	s_cbranch_scc0 .LBB0_1913
	s_and_b64 vcc, exec, s[10:11]
	s_cbranch_vccz .LBB0_1916
	s_barrier

; #define PG8_WAIT_V(n) asm volatile("s_waitcnt vmcnt(" #n ")" ::: "memory")
; #define PG8_WAIT_L(n) asm volatile("s_waitcnt lgkmcnt(" #n ")" ::: "memory")
; #define PG8_BAR __builtin_amdgcn_s_barrier()
; #define PG8_SCHED __builtin_amdgcn_sched_barrier(0)
; #define PG8_STAGE_A(b, h, p) do { if constexpr (GATHER) { if ((h) == 0) PG8_STAGE(PG8_SA(b, h), p, vA0); else PG8_STAGE(PG8_SA(b, h), p, vA1); } else PG8_STAGE(PG8_SA(b, h), (p) + ((h) ? hstepA : (size_t)0), voffA); } while (0)
; #define PG8_GOFF1(un, h, d) do { int tz_ = tid; asm volatile("" : "+v"(tz_)); _Pragma("unroll") for (int i_ = 0; i_ < 2; ++i_) { int R_, C_; stage_rc(tz_ * 16 + i_ * 8192, R_, C_); \
;         d[i_] = S.gather(un, R_ + (h) * HALF) + (unsigned)C_ * 2u; } } while (0)
; template <class Epi, class Sched, bool ALIGN_EPI = true, bool SP2 = true, bool FP8 = false, bool GATHER = false>
; __device__ __forceinline__ void gemm_phase(LAS unsigned char* lds, const Dims g, const Sched& S, const Epi& E, const int wv) {
;     ...
;             const bool last = (t == nt - 2);
;             const char* a1 = cA + (size_t)(t + 1) * kstep;
;             const char* a2 = last ? nA : cA + (size_t)(t + 2) * kstep; const char* b2 = last ? nB : cB + (size_t)(t + 2) * kstep;
;             const char* a3 = a2 + kstep; const char* b3 = b2 + kstep;
;             if constexpr (SP2) {
;             if constexpr (GATHER) { if (last) PG8_GOFF1(un_, 0, vA0); }
;             PG8_LDB(B0, 0, 0); PG8_LDB(B1, 0, 1); PG8_SCHED; PG8_LDA(At, 0, 0); PG8_STAGE_A(1, 1, a1);
;             if constexpr (GATHER) { if (last) PG8_GOFF1(un_, 1, vA1); }
;             PG8_WAIT_V(8); PG8_WAIT_L(0); PG8_BAR; PG8_MMA(0, 0, At, B0); PG8_MMA(0, 1, At, B1); PG8_BAR; PG8_SCHED;
;             PG8_LDA(At, 0, 1); PG8_STAGE(PG8_SB(0, 0), b2, voffB); PG8_STAGE(PG8_SB(0, 1), b2 + hstepB, voffB); PG8_STAGE_A(0, 0, a2);
;             PG8_WAIT_V(8); PG8_WAIT_L(0); PG8_BAR; PG8_MMA(1, 0, At, B0); PG8_MMA(1, 1, At, B1); PG8_BAR; PG8_SCHED;
.LBB0_2530:
	s_add_u32 s38, s38, 0x100
	s_addc_u32 s39, s39, 0
	s_and_b64 s[40:41], s[40:41], exec
	s_cselect_b32 s46, s78, s38
	s_waitcnt vmcnt(8)
	s_cselect_b32 s47, s37, s39
	s_cselect_b32 s43, s79, s83
	s_cselect_b32 s42, s80, s82
	s_add_u32 s40, s46, 0x80
	s_waitcnt lgkmcnt(0)
	s_addc_u32 s41, s47, 0
	s_add_u32 s44, s42, 0x80
	s_addc_u32 s45, s43, 0
	s_barrier
	s_setprio 1
	s_waitcnt lgkmcnt(6)
	v_mfma_scale_f32_16x16x128_f8f6f4 v[188:191], v[16:23], v[56:63], v[188:191], v200, v200 op_sel_hi:[0,0,0]
	v_mfma_scale_f32_16x16x128_f8f6f4 v[184:187], v[24:31], v[56:63], v[184:187], v200, v200 op_sel_hi:[0,0,0]
	s_waitcnt lgkmcnt(4)
	v_mfma_scale_f32_16x16x128_f8f6f4 v[172:175], v[16:23], v[48:55], v[172:175], v200, v200 op_sel_hi:[0,0,0]
	v_mfma_scale_f32_16x16x128_f8f6f4 v[168:171], v[24:31], v[48:55], v[168:171], v200, v200 op_sel_hi:[0,0,0]
	s_waitcnt lgkmcnt(2)
	v_mfma_scale_f32_16x16x128_f8f6f4 v[156:159], v[16:23], v[40:47], v[156:159], v200, v200 op_sel_hi:[0,0,0]
	v_mfma_scale_f32_16x16x128_f8f6f4 v[152:155], v[24:31], v[40:47], v[152:155], v200, v200 op_sel_hi:[0,0,0]
	s_waitcnt lgkmcnt(0)
	v_mfma_scale_f32_16x16x128_f8f6f4 v[140:143], v[16:23], v[32:39], v[140:143], v200, v200 op_sel_hi:[0,0,0]
	v_mfma_scale_f32_16x16x128_f8f6f4 v[136:139], v[24:31], v[32:39], v[136:139], v200, v200 op_sel_hi:[0,0,0]
	v_mfma_scale_f32_16x16x128_f8f6f4 v[180:183], v[0:7], v[56:63], v[180:183], v200, v200 op_sel_hi:[0,0,0]
	v_mfma_scale_f32_16x16x128_f8f6f4 v[176:179], v[8:15], v[56:63], v[176:179], v200, v200 op_sel_hi:[0,0,0]
	v_mfma_scale_f32_16x16x128_f8f6f4 v[164:167], v[0:7], v[48:55], v[164:167], v200, v200 op_sel_hi:[0,0,0]
	v_mfma_scale_f32_16x16x128_f8f6f4 v[160:163], v[8:15], v[48:55], v[160:163], v200, v200 op_sel_hi:[0,0,0]
	v_mfma_scale_f32_16x16x128_f8f6f4 v[148:151], v[0:7], v[40:47], v[148:151], v200, v200 op_sel_hi:[0,0,0]
	v_mfma_scale_f32_16x16x128_f8f6f4 v[144:147], v[8:15], v[40:47], v[144:147], v200, v200 op_sel_hi:[0,0,0]
	v_mfma_scale_f32_16x16x128_f8f6f4 v[132:135], v[0:7], v[32:39], v[132:135], v200, v200 op_sel_hi:[0,0,0]
	v_mfma_scale_f32_16x16x128_f8f6f4 v[128:131], v[8:15], v[32:39], v[128:131], v200, v200 op_sel_hi:[0,0,0]
	s_setprio 0
	s_barrier
	ds_read_b128 v[32:35], v202 offset:16384
	ds_read_b128 v[36:39], v202 offset:17408
	ds_read_b128 v[40:43], v202 offset:18432
	ds_read_b128 v[44:47], v202 offset:19456
	ds_read_b128 v[48:51], v202 offset:20480
	ds_read_b128 v[52:55], v202 offset:21504
	ds_read_b128 v[56:59], v202 offset:22528
	ds_read_b128 v[60:63], v202 offset:23552
	s_mov_b32 m0, s54
	s_nop 0
	global_load_lds_dwordx4 v195, s[42:43]
	s_add_u32 s86, s42, 0x20000
	s_mov_b32 m0, s55
	s_nop 0
	global_load_lds_dwordx4 v199, s[42:43]
	s_addc_u32 s87, s43, 0
	s_mov_b32 m0, s56
	s_nop 0
	global_load_lds_dwordx4 v195, s[86:87]
	s_nop 0
	s_mov_b32 m0, s57
	s_nop 0
	global_load_lds_dwordx4 v199, s[86:87]
	s_nop 0
	s_mov_b32 m0, s27
	s_nop 0
	global_load_lds_dwordx4 v194, s[46:47]
	s_nop 0
	s_mov_b32 m0, s58
	s_nop 0
	global_load_lds_dwordx4 v196, s[46:47]
	s_waitcnt vmcnt(8)
	s_waitcnt lgkmcnt(0)
	s_barrier
	s_setprio 1
	v_mfma_scale_f32_16x16x128_f8f6f4 v[124:127], v[16:23], v[32:39], v[124:127], v200, v200 op_sel_hi:[0,0,0]
	v_mfma_scale_f32_16x16x128_f8f6f4 v[120:123], v[24:31], v[32:39], v[120:123], v200, v200 op_sel_hi:[0,0,0]
	v_mfma_scale_f32_16x16x128_f8f6f4 v[108:111], v[16:23], v[40:47], v[108:111], v200, v200 op_sel_hi:[0,0,0]
	v_mfma_scale_f32_16x16x128_f8f6f4 v[104:107], v[24:31], v[40:47], v[104:107], v200, v200 op_sel_hi:[0,0,0]
	v_mfma_scale_f32_16x16x128_f8f6f4 v[92:95], v[16:23], v[48:55], v[92:95], v200, v200 op_sel_hi:[0,0,0]
	v_mfma_scale_f32_16x16x128_f8f6f4 v[88:91], v[24:31], v[48:55], v[88:91], v200, v200 op_sel_hi:[0,0,0]
	v_mfma_scale_f32_16x16x128_f8f6f4 v[76:79], v[16:23], v[56:63], v[76:79], v200, v200 op_sel_hi:[0,0,0]
	v_mfma_scale_f32_16x16x128_f8f6f4 v[72:75], v[24:31], v[56:63], v[72:75], v200, v200 op_sel_hi:[0,0,0]
	v_mfma_scale_f32_16x16x128_f8f6f4 v[116:119], v[0:7], v[32:39], v[116:119], v200, v200 op_sel_hi:[0,0,0]
	v_mfma_scale_f32_16x16x128_f8f6f4 v[112:115], v[8:15], v[32:39], v[112:115], v200, v200 op_sel_hi:[0,0,0]
	v_mfma_scale_f32_16x16x128_f8f6f4 v[100:103], v[0:7], v[40:47], v[100:103], v200, v200 op_sel_hi:[0,0,0]
	v_mfma_scale_f32_16x16x128_f8f6f4 v[96:99], v[8:15], v[40:47], v[96:99], v200, v200 op_sel_hi:[0,0,0]
	v_mfma_scale_f32_16x16x128_f8f6f4 v[84:87], v[0:7], v[48:55], v[84:87], v200, v200 op_sel_hi:[0,0,0]
	v_mfma_scale_f32_16x16x128_f8f6f4 v[80:83], v[8:15], v[48:55], v[80:83], v200, v200 op_sel_hi:[0,0,0]
	v_mfma_scale_f32_16x16x128_f8f6f4 v[68:71], v[0:7], v[56:63], v[68:71], v200, v200 op_sel_hi:[0,0,0]
	v_mfma_scale_f32_16x16x128_f8f6f4 v[64:67], v[8:15], v[56:63], v[64:67], v200, v200 op_sel_hi:[0,0,0]
	s_setprio 0
	s_barrier
; #define PG8_WAIT_V(n) asm volatile("s_waitcnt vmcnt(" #n ")" ::: "memory")
; #define PG8_WAIT_L(n) asm volatile("s_waitcnt lgkmcnt(" #n ")" ::: "memory")
; #define PG8_BAR __builtin_amdgcn_s_barrier()
; #define PG8_SCHED __builtin_amdgcn_sched_barrier(0)
; #define PG8_STAGE_A(b, h, p) do { if constexpr (GATHER) { if ((h) == 0) PG8_STAGE(PG8_SA(b, h), p, vA0); else PG8_STAGE(PG8_SA(b, h), p, vA1); } else PG8_STAGE(PG8_SA(b, h), (p) + ((h) ? hstepA : (size_t)0), voffA); } while (0)
; template <class Epi, class Sched, bool ALIGN_EPI = true, bool SP2 = true, bool FP8 = false, bool GATHER = false>
; __device__ __forceinline__ void gemm_phase(LAS unsigned char* lds, const Dims g, const Sched& S, const Epi& E, const int wv) {
;     ...
;         for (int t = 0; t < nt; t += 2) {
;     ...
;             PG8_LDB(B0, 1, 0); PG8_LDB(B1, 1, 1); PG8_SCHED; PG8_LDA(At, 1, 0); PG8_STAGE_A(0, 1, a2);
;             PG8_WAIT_V(8); PG8_WAIT_L(0); PG8_BAR; PG8_MMA(0, 0, At, B0); PG8_MMA(0, 1, At, B1); PG8_BAR; PG8_SCHED;
;             PG8_LDA(At, 1, 1); PG8_STAGE(PG8_SB(1, 0), b3, voffB); PG8_STAGE(PG8_SB(1, 1), b3 + hstepB, voffB); PG8_STAGE_A(1, 0, a3);
;             PG8_WAIT_V(8); PG8_WAIT_L(0); PG8_BAR; PG8_MMA(1, 0, At, B0); PG8_MMA(1, 1, At, B1); PG8_BAR; PG8_SCHED;
	v_add_u32_e32 v12, 0x18000, v201
	v_add_u32_e32 v28, 0x1c000, v201
	ds_read_b128 v[0:3], v12
	ds_read_b128 v[4:7], v12 offset:1024
	ds_read_b128 v[8:11], v12 offset:2048
	ds_read_b128 v[12:15], v12 offset:3072
	ds_read_b128 v[16:19], v28
	ds_read_b128 v[20:23], v28 offset:1024
	ds_read_b128 v[24:27], v28 offset:2048
	ds_read_b128 v[28:31], v28 offset:3072
	ds_read_b128 v[32:35], v202 offset:32768
	ds_read_b128 v[36:39], v202 offset:33792
	ds_read_b128 v[40:43], v202 offset:34816
	ds_read_b128 v[44:47], v202 offset:35840
	ds_read_b128 v[48:51], v202 offset:36864
	ds_read_b128 v[52:55], v202 offset:37888
	ds_read_b128 v[56:59], v202 offset:38912
	ds_read_b128 v[60:63], v202 offset:39936
	s_mov_b32 m0, s59
	s_nop 0
	global_load_lds_dwordx4 v197, s[46:47]
	s_nop 0
	s_mov_b32 m0, s60
	s_nop 0
	global_load_lds_dwordx4 v198, s[46:47]
	s_waitcnt vmcnt(8)
	s_waitcnt lgkmcnt(0)
	s_barrier
	s_setprio 1
	v_mfma_scale_f32_16x16x128_f8f6f4 v[188:191], v[0:7], v[32:39], v[188:191], v200, v200 op_sel_hi:[0,0,0]
	v_mfma_scale_f32_16x16x128_f8f6f4 v[184:187], v[8:15], v[32:39], v[184:187], v200, v200 op_sel_hi:[0,0,0]
	v_mfma_scale_f32_16x16x128_f8f6f4 v[172:175], v[0:7], v[40:47], v[172:175], v200, v200 op_sel_hi:[0,0,0]
	v_mfma_scale_f32_16x16x128_f8f6f4 v[168:171], v[8:15], v[40:47], v[168:171], v200, v200 op_sel_hi:[0,0,0]
	v_mfma_scale_f32_16x16x128_f8f6f4 v[156:159], v[0:7], v[48:55], v[156:159], v200, v200 op_sel_hi:[0,0,0]
	v_mfma_scale_f32_16x16x128_f8f6f4 v[152:155], v[8:15], v[48:55], v[152:155], v200, v200 op_sel_hi:[0,0,0]
	v_mfma_scale_f32_16x16x128_f8f6f4 v[140:143], v[0:7], v[56:63], v[140:143], v200, v200 op_sel_hi:[0,0,0]
	v_mfma_scale_f32_16x16x128_f8f6f4 v[136:139], v[8:15], v[56:63], v[136:139], v200, v200 op_sel_hi:[0,0,0]
	v_mfma_scale_f32_16x16x128_f8f6f4 v[180:183], v[16:23], v[32:39], v[180:183], v200, v200 op_sel_hi:[0,0,0]
	v_mfma_scale_f32_16x16x128_f8f6f4 v[176:179], v[24:31], v[32:39], v[176:179], v200, v200 op_sel_hi:[0,0,0]
	v_mfma_scale_f32_16x16x128_f8f6f4 v[164:167], v[16:23], v[40:47], v[164:167], v200, v200 op_sel_hi:[0,0,0]
	v_mfma_scale_f32_16x16x128_f8f6f4 v[160:163], v[24:31], v[40:47], v[160:163], v200, v200 op_sel_hi:[0,0,0]
	v_mfma_scale_f32_16x16x128_f8f6f4 v[148:151], v[16:23], v[48:55], v[148:151], v200, v200 op_sel_hi:[0,0,0]
	v_mfma_scale_f32_16x16x128_f8f6f4 v[144:147], v[24:31], v[48:55], v[144:147], v200, v200 op_sel_hi:[0,0,0]
	v_mfma_scale_f32_16x16x128_f8f6f4 v[132:135], v[16:23], v[56:63], v[132:135], v200, v200 op_sel_hi:[0,0,0]
	v_mfma_scale_f32_16x16x128_f8f6f4 v[128:131], v[24:31], v[56:63], v[128:131], v200, v200 op_sel_hi:[0,0,0]
	s_setprio 0
	s_barrier
	ds_read_b128 v[32:35], v202 offset:49152
	ds_read_b128 v[36:39], v202 offset:50176
	ds_read_b128 v[40:43], v202 offset:51200
	ds_read_b128 v[44:47], v202 offset:52224
	ds_read_b128 v[48:51], v202 offset:53248
	ds_read_b128 v[52:55], v202 offset:54272
	ds_read_b128 v[56:59], v202 offset:55296
	ds_read_b128 v[60:63], v202 offset:56320
	s_mov_b32 m0, s65
	s_nop 0
	global_load_lds_dwordx4 v195, s[44:45]
	s_add_u32 s42, s42, 0x20080
	s_mov_b32 m0, s66
	s_nop 0
	global_load_lds_dwordx4 v199, s[44:45]
	s_addc_u32 s43, s43, 0
	s_mov_b32 m0, s69
	s_nop 0
	global_load_lds_dwordx4 v195, s[42:43]
	s_nop 0
	s_mov_b32 m0, s70
	s_nop 0
	global_load_lds_dwordx4 v199, s[42:43]
	s_mov_b32 m0, s67
	s_nop 0
	global_load_lds_dwordx4 v194, s[40:41]
	s_nop 0
	s_mov_b32 m0, s68
	s_nop 0
	global_load_lds_dwordx4 v196, s[40:41]
	s_waitcnt vmcnt(8)
	s_waitcnt lgkmcnt(0)
	s_barrier
	s_setprio 1
	v_mfma_scale_f32_16x16x128_f8f6f4 v[124:127], v[0:7], v[32:39], v[124:127], v200, v200 op_sel_hi:[0,0,0]
	v_mfma_scale_f32_16x16x128_f8f6f4 v[120:123], v[8:15], v[32:39], v[120:123], v200, v200 op_sel_hi:[0,0,0]
	v_mfma_scale_f32_16x16x128_f8f6f4 v[108:111], v[0:7], v[40:47], v[108:111], v200, v200 op_sel_hi:[0,0,0]
	v_mfma_scale_f32_16x16x128_f8f6f4 v[104:107], v[8:15], v[40:47], v[104:107], v200, v200 op_sel_hi:[0,0,0]
	v_mfma_scale_f32_16x16x128_f8f6f4 v[92:95], v[0:7], v[48:55], v[92:95], v200, v200 op_sel_hi:[0,0,0]
	v_mfma_scale_f32_16x16x128_f8f6f4 v[88:91], v[8:15], v[48:55], v[88:91], v200, v200 op_sel_hi:[0,0,0]
	v_mfma_scale_f32_16x16x128_f8f6f4 v[76:79], v[0:7], v[56:63], v[76:79], v200, v200 op_sel_hi:[0,0,0]
	v_mfma_scale_f32_16x16x128_f8f6f4 v[72:75], v[8:15], v[56:63], v[72:75], v200, v200 op_sel_hi:[0,0,0]
	v_mfma_scale_f32_16x16x128_f8f6f4 v[116:119], v[16:23], v[32:39], v[116:119], v200, v200 op_sel_hi:[0,0,0]
	v_mfma_scale_f32_16x16x128_f8f6f4 v[112:115], v[24:31], v[32:39], v[112:115], v200, v200 op_sel_hi:[0,0,0]
	v_mfma_scale_f32_16x16x128_f8f6f4 v[100:103], v[16:23], v[40:47], v[100:103], v200, v200 op_sel_hi:[0,0,0]
	v_mfma_scale_f32_16x16x128_f8f6f4 v[96:99], v[24:31], v[40:47], v[96:99], v200, v200 op_sel_hi:[0,0,0]
	v_mfma_scale_f32_16x16x128_f8f6f4 v[84:87], v[16:23], v[48:55], v[84:87], v200, v200 op_sel_hi:[0,0,0]
	v_mfma_scale_f32_16x16x128_f8f6f4 v[80:83], v[24:31], v[48:55], v[80:83], v200, v200 op_sel_hi:[0,0,0]
	v_mfma_scale_f32_16x16x128_f8f6f4 v[68:71], v[16:23], v[56:63], v[68:71], v200, v200 op_sel_hi:[0,0,0]
	v_mfma_scale_f32_16x16x128_f8f6f4 v[64:67], v[24:31], v[56:63], v[64:67], v200, v200 op_sel_hi:[0,0,0]
	s_setprio 0
	s_barrier
	s_add_i32 s84, s84, 2
	s_add_u32 s82, s82, 0x100
	s_addc_u32 s83, s83, 0
	s_cmp_gt_u32 s84, 5
	s_cbranch_scc1 .LBB0_2535

; #define PG8_WAIT_V(n) asm volatile("s_waitcnt vmcnt(" #n ")" ::: "memory")
; #define PG8_WAIT_L(n) asm volatile("s_waitcnt lgkmcnt(" #n ")" ::: "memory")
; #define PG8_BAR __builtin_amdgcn_s_barrier()
; #define PG8_SCHED __builtin_amdgcn_sched_barrier(0)
; #define PG8_STAGE_A(b, h, p) do { if constexpr (GATHER) { if ((h) == 0) PG8_STAGE(PG8_SA(b, h), p, vA0); else PG8_STAGE(PG8_SA(b, h), p, vA1); } else PG8_STAGE(PG8_SA(b, h), (p) + ((h) ? hstepA : (size_t)0), voffA); } while (0)
; #define PG8_GOFF1(un, h, d) do { int tz_ = tid; asm volatile("" : "+v"(tz_)); _Pragma("unroll") for (int i_ = 0; i_ < 2; ++i_) { int R_, C_; stage_rc(tz_ * 16 + i_ * 8192, R_, C_); \
;         d[i_] = S.gather(un, R_ + (h) * HALF) + (unsigned)C_ * 2u; } } while (0)
; template <class Epi, class Sched, bool ALIGN_EPI = true, bool SP2 = true, bool FP8 = false, bool GATHER = false>
; __device__ __forceinline__ void gemm_phase(LAS unsigned char* lds, const Dims g, const Sched& S, const Epi& E, const int wv) {
;     ...
;             const bool last = (t == nt - 2);
;             const char* a1 = cA + (size_t)(t + 1) * kstep;
;             const char* a2 = last ? nA : cA + (size_t)(t + 2) * kstep; const char* b2 = last ? nB : cB + (size_t)(t + 2) * kstep;
;             const char* a3 = a2 + kstep; const char* b3 = b2 + kstep;
;             if constexpr (SP2) {
;             if constexpr (GATHER) { if (last) PG8_GOFF1(un_, 0, vA0); }
;             PG8_LDB(B0, 0, 0); PG8_LDB(B1, 0, 1); PG8_SCHED; PG8_LDA(At, 0, 0); PG8_STAGE_A(1, 1, a1);
;             if constexpr (GATHER) { if (last) PG8_GOFF1(un_, 1, vA1); }
;             PG8_WAIT_V(8); PG8_WAIT_L(0); PG8_BAR; PG8_MMA(0, 0, At, B0); PG8_MMA(0, 1, At, B1); PG8_BAR; PG8_SCHED;
;             PG8_LDA(At, 0, 1); PG8_STAGE(PG8_SB(0, 0), b2, voffB); PG8_STAGE(PG8_SB(0, 1), b2 + hstepB, voffB); PG8_STAGE_A(0, 0, a2);
;             PG8_WAIT_V(8); PG8_WAIT_L(0); PG8_BAR; PG8_MMA(1, 0, At, B0); PG8_MMA(1, 1, At, B1); PG8_BAR; PG8_SCHED;
.LBB0_2632:
	ds_read_b128 v[128:131], v157
	ds_read_b128 v[132:135], v157 offset:1024
	ds_read_b128 v[136:139], v157 offset:2048
	ds_read_b128 v[140:143], v157 offset:3072
	ds_read_b128 v[144:147], v158
	ds_read_b128 v[148:151], v158 offset:1024
	ds_read_b128 v[164:167], v158 offset:2048
	ds_read_b128 v[168:171], v158 offset:3072
	s_add_u32 s44, s42, 0x100
	s_addc_u32 s45, s43, 0
	s_cmp_eq_u32 s86, 4
	s_cselect_b32 s50, s41, s44
	s_cselect_b32 s51, s37, s45
	s_cselect_b32 s48, s53, s84
	s_cselect_b32 s49, s52, s85
	s_add_u32 s46, s50, 0x80
	s_addc_u32 s47, s51, 0
	ds_read_b128 v[172:175], v159
	ds_read_b128 v[176:179], v159 offset:1024
	ds_read_b128 v[180:183], v159 offset:2048
	ds_read_b128 v[184:187], v159 offset:3072
	ds_read_b128 v[188:191], v159 offset:4096
	ds_read_b128 v[192:195], v159 offset:5120
	ds_read_b128 v[196:199], v159 offset:6144
	ds_read_b128 v[200:203], v159 offset:7168
	s_add_u32 s42, s42, 0x20080
	s_addc_u32 s43, s43, 0
	s_mov_b32 m0, s76
	s_nop 0
	global_load_lds_dwordx4 v153, s[42:43]
	s_nop 0
	s_mov_b32 m0, s77
	s_nop 0
	global_load_lds_dwordx4 v155, s[42:43]
	s_waitcnt vmcnt(8)
	s_waitcnt lgkmcnt(0)
	s_barrier
	s_setprio 1
	v_mfma_scale_f32_16x16x128_f8f6f4 v[124:127], v[128:135], v[172:179], v[124:127], v160, v160 op_sel_hi:[0,0,0]
	v_mfma_scale_f32_16x16x128_f8f6f4 v[120:123], v[136:143], v[172:179], v[120:123], v160, v160 op_sel_hi:[0,0,0]
	v_mfma_scale_f32_16x16x128_f8f6f4 v[116:119], v[128:135], v[180:187], v[116:119], v160, v160 op_sel_hi:[0,0,0]
	v_mfma_scale_f32_16x16x128_f8f6f4 v[112:115], v[136:143], v[180:187], v[112:115], v160, v160 op_sel_hi:[0,0,0]
	v_mfma_scale_f32_16x16x128_f8f6f4 v[204:207], v[128:135], v[188:195], v[92:95], v160, v160 op_sel_hi:[0,0,0]
	v_mfma_scale_f32_16x16x128_f8f6f4 v[208:211], v[136:143], v[188:195], v[88:91], v160, v160 op_sel_hi:[0,0,0]
	v_mfma_scale_f32_16x16x128_f8f6f4 v[212:215], v[128:135], v[196:203], v[76:79], v160, v160 op_sel_hi:[0,0,0]
	v_mfma_scale_f32_16x16x128_f8f6f4 v[216:219], v[136:143], v[196:203], v[72:75], v160, v160 op_sel_hi:[0,0,0]
	v_mfma_scale_f32_16x16x128_f8f6f4 v[108:111], v[144:151], v[172:179], v[108:111], v160, v160 op_sel_hi:[0,0,0]
	v_mfma_scale_f32_16x16x128_f8f6f4 v[104:107], v[164:171], v[172:179], v[104:107], v160, v160 op_sel_hi:[0,0,0]
	v_mfma_scale_f32_16x16x128_f8f6f4 v[100:103], v[144:151], v[180:187], v[100:103], v160, v160 op_sel_hi:[0,0,0]
	v_mfma_scale_f32_16x16x128_f8f6f4 v[96:99], v[164:171], v[180:187], v[96:99], v160, v160 op_sel_hi:[0,0,0]
	v_mfma_scale_f32_16x16x128_f8f6f4 v[172:175], v[144:151], v[188:195], v[84:87], v160, v160 op_sel_hi:[0,0,0]
	v_mfma_scale_f32_16x16x128_f8f6f4 v[176:179], v[164:171], v[188:195], v[80:83], v160, v160 op_sel_hi:[0,0,0]
	v_mfma_scale_f32_16x16x128_f8f6f4 v[180:183], v[144:151], v[196:203], v[68:71], v160, v160 op_sel_hi:[0,0,0]
	v_mfma_scale_f32_16x16x128_f8f6f4 v[184:187], v[164:171], v[196:203], v[64:67], v160, v160 op_sel_hi:[0,0,0]
	s_setprio 0
	s_barrier
	s_nop 4
	ds_read_b128 v[64:67], v159 offset:16384
	ds_read_b128 v[68:71], v159 offset:17408
	ds_read_b128 v[72:75], v159 offset:18432
	ds_read_b128 v[76:79], v159 offset:19456
	ds_read_b128 v[80:83], v159 offset:20480
	ds_read_b128 v[84:87], v159 offset:21504
	ds_read_b128 v[88:91], v159 offset:22528
	ds_read_b128 v[92:95], v159 offset:23552
	s_mov_b32 m0, s60
	s_nop 0
	global_load_lds_dwordx4 v154, s[48:49]
	s_nop 0
	s_mov_b32 m0, s61
	s_nop 0
	global_load_lds_dwordx4 v156, s[48:49]
	s_add_u32 s42, s48, 0x20000
	s_addc_u32 s43, s49, 0
	s_mov_b32 m0, s62
	s_nop 0
	global_load_lds_dwordx4 v154, s[42:43]
	s_nop 0
	s_mov_b32 m0, s63
	s_nop 0
	global_load_lds_dwordx4 v156, s[42:43]
	s_mov_b32 m0, s59
	s_nop 0
	global_load_lds_dwordx4 v153, s[50:51]
	s_nop 0
	s_mov_b32 m0, s64
	s_nop 0
	global_load_lds_dwordx4 v155, s[50:51]
	s_waitcnt vmcnt(8)
	s_waitcnt lgkmcnt(0)
	s_barrier
	s_setprio 1
	v_mfma_scale_f32_16x16x128_f8f6f4 v[60:63], v[128:135], v[64:71], v[60:63], v160, v160 op_sel_hi:[0,0,0]
	v_mfma_scale_f32_16x16x128_f8f6f4 v[56:59], v[136:143], v[64:71], v[56:59], v160, v160 op_sel_hi:[0,0,0]
	v_mfma_scale_f32_16x16x128_f8f6f4 v[188:191], v[128:135], v[72:79], v[44:47], v160, v160 op_sel_hi:[0,0,0]
	v_mfma_scale_f32_16x16x128_f8f6f4 v[192:195], v[136:143], v[72:79], v[40:43], v160, v160 op_sel_hi:[0,0,0]
	v_mfma_scale_f32_16x16x128_f8f6f4 v[196:199], v[128:135], v[80:87], v[28:31], v160, v160 op_sel_hi:[0,0,0]
	v_mfma_scale_f32_16x16x128_f8f6f4 v[200:203], v[136:143], v[80:87], v[24:27], v160, v160 op_sel_hi:[0,0,0]
	v_mfma_scale_f32_16x16x128_f8f6f4 v[220:223], v[128:135], v[88:95], v[12:15], v160, v160 op_sel_hi:[0,0,0]
	v_mfma_scale_f32_16x16x128_f8f6f4 v[224:227], v[136:143], v[88:95], v[8:11], v160, v160 op_sel_hi:[0,0,0]
	v_mfma_scale_f32_16x16x128_f8f6f4 v[52:55], v[144:151], v[64:71], v[52:55], v160, v160 op_sel_hi:[0,0,0]
	v_mfma_scale_f32_16x16x128_f8f6f4 v[48:51], v[164:171], v[64:71], v[48:51], v160, v160 op_sel_hi:[0,0,0]
	v_mfma_scale_f32_16x16x128_f8f6f4 v[228:231], v[144:151], v[72:79], v[36:39], v160, v160 op_sel_hi:[0,0,0]
	v_mfma_scale_f32_16x16x128_f8f6f4 v[232:235], v[164:171], v[72:79], v[32:35], v160, v160 op_sel_hi:[0,0,0]
	v_mfma_scale_f32_16x16x128_f8f6f4 v[236:239], v[144:151], v[80:87], v[20:23], v160, v160 op_sel_hi:[0,0,0]
	v_mfma_scale_f32_16x16x128_f8f6f4 v[240:243], v[164:171], v[80:87], v[16:19], v160, v160 op_sel_hi:[0,0,0]
	v_mfma_scale_f32_16x16x128_f8f6f4 v[244:247], v[144:151], v[88:95], v[4:7], v160, v160 op_sel_hi:[0,0,0]
	v_mfma_scale_f32_16x16x128_f8f6f4 v[248:251], v[164:171], v[88:95], v[0:3], v160, v160 op_sel_hi:[0,0,0]
	s_setprio 0
	s_barrier
; #define PG8_WAIT_V(n) asm volatile("s_waitcnt vmcnt(" #n ")" ::: "memory")
; #define PG8_WAIT_L(n) asm volatile("s_waitcnt lgkmcnt(" #n ")" ::: "memory")
; #define PG8_BAR __builtin_amdgcn_s_barrier()
; #define PG8_SCHED __builtin_amdgcn_sched_barrier(0)
; #define PG8_STAGE_A(b, h, p) do { if constexpr (GATHER) { if ((h) == 0) PG8_STAGE(PG8_SA(b, h), p, vA0); else PG8_STAGE(PG8_SA(b, h), p, vA1); } else PG8_STAGE(PG8_SA(b, h), (p) + ((h) ? hstepA : (size_t)0), voffA); } while (0)
; template <class Epi, class Sched, bool ALIGN_EPI = true, bool SP2 = true, bool FP8 = false, bool GATHER = false>
; __device__ __forceinline__ void gemm_phase(LAS unsigned char* lds, const Dims g, const Sched& S, const Epi& E, const int wv) {
;     ...
;             PG8_LDB(B0, 1, 0); PG8_LDB(B1, 1, 1); PG8_SCHED; PG8_LDA(At, 1, 0); PG8_STAGE_A(0, 1, a2);
;             PG8_WAIT_V(8); PG8_WAIT_L(0); PG8_BAR; PG8_MMA(0, 0, At, B0); PG8_MMA(0, 1, At, B1); PG8_BAR; PG8_SCHED;
;             PG8_LDA(At, 1, 1); PG8_STAGE(PG8_SB(1, 0), b3, voffB); PG8_STAGE(PG8_SB(1, 1), b3 + hstepB, voffB); PG8_STAGE_A(1, 0, a3);
;             PG8_WAIT_V(8); PG8_WAIT_L(0); PG8_BAR; PG8_MMA(1, 0, At, B0); PG8_MMA(1, 1, At, B1); PG8_BAR; PG8_SCHED;
	s_nop 4
	ds_read_b128 v[0:3], v161
	ds_read_b128 v[4:7], v161 offset:1024
	ds_read_b128 v[16:19], v161 offset:2048
	ds_read_b128 v[20:23], v161 offset:3072
	ds_read_b128 v[128:131], v162
	ds_read_b128 v[132:135], v162 offset:1024
	ds_read_b128 v[136:139], v162 offset:2048
	ds_read_b128 v[140:143], v162 offset:3072
	ds_read_b128 v[8:11], v159 offset:32768
	ds_read_b128 v[12:15], v159 offset:33792
	ds_read_b128 v[24:27], v159 offset:34816
	ds_read_b128 v[28:31], v159 offset:35840
	ds_read_b128 v[32:35], v159 offset:36864
	ds_read_b128 v[36:39], v159 offset:37888
	ds_read_b128 v[40:43], v159 offset:38912
	ds_read_b128 v[44:47], v159 offset:39936
	s_add_u32 s42, s50, 0x20000
	s_addc_u32 s43, s51, 0
	s_mov_b32 m0, s65
	s_nop 0
	global_load_lds_dwordx4 v153, s[42:43]
	s_nop 0
	s_mov_b32 m0, s66
	s_nop 0
	global_load_lds_dwordx4 v155, s[42:43]
	s_waitcnt vmcnt(8)
	s_waitcnt lgkmcnt(0)
	s_barrier
	s_setprio 1
	v_mfma_scale_f32_16x16x128_f8f6f4 v[124:127], v[0:7], v[8:15], v[124:127], v160, v160 op_sel_hi:[0,0,0]
	v_mfma_scale_f32_16x16x128_f8f6f4 v[120:123], v[16:23], v[8:15], v[120:123], v160, v160 op_sel_hi:[0,0,0]
	v_mfma_scale_f32_16x16x128_f8f6f4 v[116:119], v[0:7], v[24:31], v[116:119], v160, v160 op_sel_hi:[0,0,0]
	v_mfma_scale_f32_16x16x128_f8f6f4 v[112:115], v[16:23], v[24:31], v[112:115], v160, v160 op_sel_hi:[0,0,0]
	v_mfma_scale_f32_16x16x128_f8f6f4 v[92:95], v[0:7], v[32:39], v[204:207], v160, v160 op_sel_hi:[0,0,0]
	v_mfma_scale_f32_16x16x128_f8f6f4 v[88:91], v[16:23], v[32:39], v[208:211], v160, v160 op_sel_hi:[0,0,0]
	v_mfma_scale_f32_16x16x128_f8f6f4 v[76:79], v[0:7], v[40:47], v[212:215], v160, v160 op_sel_hi:[0,0,0]
	v_mfma_scale_f32_16x16x128_f8f6f4 v[72:75], v[16:23], v[40:47], v[216:219], v160, v160 op_sel_hi:[0,0,0]
	v_mfma_scale_f32_16x16x128_f8f6f4 v[108:111], v[128:135], v[8:15], v[108:111], v160, v160 op_sel_hi:[0,0,0]
	v_mfma_scale_f32_16x16x128_f8f6f4 v[104:107], v[136:143], v[8:15], v[104:107], v160, v160 op_sel_hi:[0,0,0]
	v_mfma_scale_f32_16x16x128_f8f6f4 v[100:103], v[128:135], v[24:31], v[100:103], v160, v160 op_sel_hi:[0,0,0]
	v_mfma_scale_f32_16x16x128_f8f6f4 v[96:99], v[136:143], v[24:31], v[96:99], v160, v160 op_sel_hi:[0,0,0]
	v_mfma_scale_f32_16x16x128_f8f6f4 v[84:87], v[128:135], v[32:39], v[172:175], v160, v160 op_sel_hi:[0,0,0]
	v_mfma_scale_f32_16x16x128_f8f6f4 v[80:83], v[136:143], v[32:39], v[176:179], v160, v160 op_sel_hi:[0,0,0]
	v_mfma_scale_f32_16x16x128_f8f6f4 v[68:71], v[128:135], v[40:47], v[180:183], v160, v160 op_sel_hi:[0,0,0]
	v_mfma_scale_f32_16x16x128_f8f6f4 v[64:67], v[136:143], v[40:47], v[184:187], v160, v160 op_sel_hi:[0,0,0]
	s_setprio 0
	s_barrier
	ds_read_b128 v[32:35], v159 offset:49152
	ds_read_b128 v[36:39], v159 offset:50176
	ds_read_b128 v[144:147], v159 offset:51200
	ds_read_b128 v[148:151], v159 offset:52224
	ds_read_b128 v[164:167], v159 offset:53248
	ds_read_b128 v[168:171], v159 offset:54272
	ds_read_b128 v[172:175], v159 offset:55296
	ds_read_b128 v[176:179], v159 offset:56320
	s_add_u32 s42, s48, 0x80
	s_addc_u32 s43, s49, 0
	s_mov_b32 m0, s70
	s_nop 0
	global_load_lds_dwordx4 v154, s[42:43]
	s_nop 0
	s_mov_b32 m0, s71
	s_nop 0
	global_load_lds_dwordx4 v156, s[42:43]
	s_add_u32 s42, s48, 0x20080
	s_addc_u32 s43, s49, 0
	s_mov_b32 m0, s74
	s_nop 0
	global_load_lds_dwordx4 v154, s[42:43]
	s_nop 0
	s_mov_b32 m0, s75
	s_nop 0
	global_load_lds_dwordx4 v156, s[42:43]
	s_mov_b32 m0, s72
	s_nop 0
	global_load_lds_dwordx4 v153, s[46:47]
	s_nop 0
	s_mov_b32 m0, s73
	s_nop 0
	global_load_lds_dwordx4 v155, s[46:47]
	s_waitcnt vmcnt(8)
	s_waitcnt lgkmcnt(0)
	s_barrier
	s_setprio 1
	v_mfma_scale_f32_16x16x128_f8f6f4 v[60:63], v[0:7], v[32:39], v[60:63], v160, v160 op_sel_hi:[0,0,0]
	v_mfma_scale_f32_16x16x128_f8f6f4 v[56:59], v[16:23], v[32:39], v[56:59], v160, v160 op_sel_hi:[0,0,0]
	v_mfma_scale_f32_16x16x128_f8f6f4 v[44:47], v[0:7], v[144:151], v[188:191], v160, v160 op_sel_hi:[0,0,0]
	v_mfma_scale_f32_16x16x128_f8f6f4 v[40:43], v[16:23], v[144:151], v[192:195], v160, v160 op_sel_hi:[0,0,0]
	v_mfma_scale_f32_16x16x128_f8f6f4 v[28:31], v[0:7], v[164:171], v[196:199], v160, v160 op_sel_hi:[0,0,0]
	v_mfma_scale_f32_16x16x128_f8f6f4 v[24:27], v[16:23], v[164:171], v[200:203], v160, v160 op_sel_hi:[0,0,0]
	v_mfma_scale_f32_16x16x128_f8f6f4 v[12:15], v[0:7], v[172:179], v[220:223], v160, v160 op_sel_hi:[0,0,0]
	v_mfma_scale_f32_16x16x128_f8f6f4 v[8:11], v[16:23], v[172:179], v[224:227], v160, v160 op_sel_hi:[0,0,0]
	v_mfma_scale_f32_16x16x128_f8f6f4 v[52:55], v[128:135], v[32:39], v[52:55], v160, v160 op_sel_hi:[0,0,0]
	v_mfma_scale_f32_16x16x128_f8f6f4 v[48:51], v[136:143], v[32:39], v[48:51], v160, v160 op_sel_hi:[0,0,0]
	v_mfma_scale_f32_16x16x128_f8f6f4 v[36:39], v[128:135], v[144:151], v[228:231], v160, v160 op_sel_hi:[0,0,0]
	v_mfma_scale_f32_16x16x128_f8f6f4 v[32:35], v[136:143], v[144:151], v[232:235], v160, v160 op_sel_hi:[0,0,0]
	v_mfma_scale_f32_16x16x128_f8f6f4 v[20:23], v[128:135], v[164:171], v[236:239], v160, v160 op_sel_hi:[0,0,0]
	v_mfma_scale_f32_16x16x128_f8f6f4 v[16:19], v[136:143], v[164:171], v[240:243], v160, v160 op_sel_hi:[0,0,0]
	v_mfma_scale_f32_16x16x128_f8f6f4 v[4:7], v[128:135], v[172:179], v[244:247], v160, v160 op_sel_hi:[0,0,0]
	v_mfma_scale_f32_16x16x128_f8f6f4 v[0:3], v[136:143], v[172:179], v[248:251], v160, v160 op_sel_hi:[0,0,0]
	s_setprio 0
	s_barrier
	s_add_i32 s86, s86, 2
	s_add_u32 s84, s84, 0x100
	s_addc_u32 s85, s85, 0
	s_cmp_gt_u32 s86, 5
	s_mov_b64 s[42:43], s[44:45]
	s_cbranch_scc0 .LBB0_2632
	s_and_b64 vcc, exec, s[12:13]
	s_cbranch_vccz .LBB0_2635
	s_barrier

; #define PG8_WAIT_V(n) asm volatile("s_waitcnt vmcnt(" #n ")" ::: "memory")
; #define PG8_WAIT_L(n) asm volatile("s_waitcnt lgkmcnt(" #n ")" ::: "memory")
; #define PG8_BAR __builtin_amdgcn_s_barrier()
; #define PG8_SCHED __builtin_amdgcn_sched_barrier(0)
; #define PG8_STAGE_A(b, h, p) do { if constexpr (GATHER) { if ((h) == 0) PG8_STAGE(PG8_SA(b, h), p, vA0); else PG8_STAGE(PG8_SA(b, h), p, vA1); } else PG8_STAGE(PG8_SA(b, h), (p) + ((h) ? hstepA : (size_t)0), voffA); } while (0)
; #define PG8_GOFF1(un, h, d) do { int tz_ = tid; asm volatile("" : "+v"(tz_)); _Pragma("unroll") for (int i_ = 0; i_ < 2; ++i_) { int R_, C_; stage_rc(tz_ * 16 + i_ * 8192, R_, C_); \
;         d[i_] = S.gather(un, R_ + (h) * HALF) + (unsigned)C_ * 2u; } } while (0)
; template <class Epi, class Sched, bool ALIGN_EPI = true, bool SP2 = true, bool FP8 = false, bool GATHER = false>
; __device__ __forceinline__ void gemm_phase(LAS unsigned char* lds, const Dims g, const Sched& S, const Epi& E, const int wv) {
;     ...
;             const bool last = (t == nt - 2);
;             const char* a1 = cA + (size_t)(t + 1) * kstep;
;             const char* a2 = last ? nA : cA + (size_t)(t + 2) * kstep; const char* b2 = last ? nB : cB + (size_t)(t + 2) * kstep;
;             const char* a3 = a2 + kstep; const char* b3 = b2 + kstep;
;             if constexpr (SP2) {
;             if constexpr (GATHER) { if (last) PG8_GOFF1(un_, 0, vA0); }
;             PG8_LDB(B0, 0, 0); PG8_LDB(B1, 0, 1); PG8_SCHED; PG8_LDA(At, 0, 0); PG8_STAGE_A(1, 1, a1);
;             if constexpr (GATHER) { if (last) PG8_GOFF1(un_, 1, vA1); }
;             PG8_WAIT_V(8); PG8_WAIT_L(0); PG8_BAR; PG8_MMA(0, 0, At, B0); PG8_MMA(0, 1, At, B1); PG8_BAR; PG8_SCHED;
;             PG8_LDA(At, 0, 1); PG8_STAGE(PG8_SB(0, 0), b2, voffB); PG8_STAGE(PG8_SB(0, 1), b2 + hstepB, voffB); PG8_STAGE_A(0, 0, a2);
;             PG8_WAIT_V(8); PG8_WAIT_L(0); PG8_BAR; PG8_MMA(1, 0, At, B0); PG8_MMA(1, 1, At, B1); PG8_BAR; PG8_SCHED;
.LBB0_3284:
	ds_read_b128 v[132:135], v151
	ds_read_b128 v[136:139], v151 offset:1024
	ds_read_b128 v[158:161], v151 offset:2048
	ds_read_b128 v[162:165], v151 offset:3072
	ds_read_b128 v[166:169], v152
	ds_read_b128 v[170:173], v152 offset:1024
	ds_read_b128 v[174:177], v152 offset:2048
	ds_read_b128 v[178:181], v152 offset:3072
	s_cmp_eq_u32 s82, 4
	s_cselect_b32 s46, s26, s80
	s_cselect_b32 s47, s27, s81
	s_cselect_b32 s44, s36, s23
	s_cselect_b32 s45, s37, s25
	s_add_u32 s42, s46, 0x80
	s_addc_u32 s43, s47, 0
	ds_read_b128 v[182:185], v153
	ds_read_b128 v[186:189], v153 offset:1024
	ds_read_b128 v[190:193], v153 offset:2048
	ds_read_b128 v[194:197], v153 offset:3072
	ds_read_b128 v[198:201], v153 offset:4096
	ds_read_b128 v[202:205], v153 offset:5120
	ds_read_b128 v[206:209], v153 offset:6144
	ds_read_b128 v[210:213], v153 offset:7168
	s_mov_b32 m0, s72
	s_nop 0
	global_load_lds_dwordx4 v147, s[40:41]
	s_nop 0
	s_mov_b32 m0, s73
	s_nop 0
	global_load_lds_dwordx4 v149, s[40:41]
	s_waitcnt vmcnt(8)
	s_waitcnt lgkmcnt(0)
	s_barrier
	s_setprio 1
	v_mfma_scale_f32_16x16x128_f8f6f4 v[124:127], v[132:139], v[182:189], v[124:127], v154, v154 op_sel_hi:[0,0,0]
	v_mfma_scale_f32_16x16x128_f8f6f4 v[120:123], v[158:165], v[182:189], v[120:123], v154, v154 op_sel_hi:[0,0,0]
	v_mfma_scale_f32_16x16x128_f8f6f4 v[116:119], v[132:139], v[190:197], v[116:119], v154, v154 op_sel_hi:[0,0,0]
	v_mfma_scale_f32_16x16x128_f8f6f4 v[104:107], v[158:165], v[190:197], v[104:107], v154, v154 op_sel_hi:[0,0,0]
	v_mfma_scale_f32_16x16x128_f8f6f4 v[100:103], v[132:139], v[198:205], v[100:103], v154, v154 op_sel_hi:[0,0,0]
	v_mfma_scale_f32_16x16x128_f8f6f4 v[140:143], v[158:165], v[198:205], v[88:91], v154, v154 op_sel_hi:[0,0,0]
	v_mfma_scale_f32_16x16x128_f8f6f4 v[214:217], v[132:139], v[206:213], v[84:87], v154, v154 op_sel_hi:[0,0,0]
	v_mfma_scale_f32_16x16x128_f8f6f4 v[218:221], v[158:165], v[206:213], v[72:75], v154, v154 op_sel_hi:[0,0,0]
	v_mfma_scale_f32_16x16x128_f8f6f4 v[112:115], v[166:173], v[182:189], v[112:115], v154, v154 op_sel_hi:[0,0,0]
	v_mfma_scale_f32_16x16x128_f8f6f4 v[108:111], v[174:181], v[182:189], v[108:111], v154, v154 op_sel_hi:[0,0,0]
	v_mfma_scale_f32_16x16x128_f8f6f4 v[96:99], v[166:173], v[190:197], v[96:99], v154, v154 op_sel_hi:[0,0,0]
	v_mfma_scale_f32_16x16x128_f8f6f4 v[182:185], v[174:181], v[190:197], v[92:95], v154, v154 op_sel_hi:[0,0,0]
	v_mfma_scale_f32_16x16x128_f8f6f4 v[186:189], v[166:173], v[198:205], v[80:83], v154, v154 op_sel_hi:[0,0,0]
	v_mfma_scale_f32_16x16x128_f8f6f4 v[190:193], v[174:181], v[198:205], v[76:79], v154, v154 op_sel_hi:[0,0,0]
	v_mfma_scale_f32_16x16x128_f8f6f4 v[194:197], v[166:173], v[206:213], v[68:71], v154, v154 op_sel_hi:[0,0,0]
	v_mfma_scale_f32_16x16x128_f8f6f4 v[198:201], v[174:181], v[206:213], v[64:67], v154, v154 op_sel_hi:[0,0,0]
	s_setprio 0
	s_barrier
	s_nop 4
	ds_read_b128 v[64:67], v153 offset:16384
	ds_read_b128 v[68:71], v153 offset:17408
	ds_read_b128 v[72:75], v153 offset:18432
	ds_read_b128 v[76:79], v153 offset:19456
	ds_read_b128 v[80:83], v153 offset:20480
	ds_read_b128 v[84:87], v153 offset:21504
	ds_read_b128 v[88:91], v153 offset:22528
	ds_read_b128 v[92:95], v153 offset:23552
	s_mov_b32 m0, s55
	s_nop 0
	global_load_lds_dwordx4 v148, s[44:45]
	s_add_u32 s84, s44, 0x20000
	s_mov_b32 m0, s56
	s_nop 0
	global_load_lds_dwordx4 v150, s[44:45]
	s_addc_u32 s85, s45, 0
	s_mov_b32 m0, s57
	s_nop 0
	global_load_lds_dwordx4 v148, s[84:85]
	s_nop 0
	s_mov_b32 m0, s58
	s_nop 0
	global_load_lds_dwordx4 v150, s[84:85]
	s_nop 0
	s_mov_b32 m0, s54
	s_nop 0
	global_load_lds_dwordx4 v147, s[46:47]
	s_nop 0
	s_mov_b32 m0, s59
	s_nop 0
	global_load_lds_dwordx4 v149, s[46:47]
	s_waitcnt vmcnt(8)
	s_waitcnt lgkmcnt(0)
	s_barrier
	s_setprio 1
	v_mfma_scale_f32_16x16x128_f8f6f4 v[60:63], v[132:139], v[64:71], v[60:63], v154, v154 op_sel_hi:[0,0,0]
	v_mfma_scale_f32_16x16x128_f8f6f4 v[56:59], v[158:165], v[64:71], v[56:59], v154, v154 op_sel_hi:[0,0,0]
	v_mfma_scale_f32_16x16x128_f8f6f4 v[48:51], v[132:139], v[72:79], v[48:51], v154, v154 op_sel_hi:[0,0,0]
	v_mfma_scale_f32_16x16x128_f8f6f4 v[202:205], v[158:165], v[72:79], v[40:43], v154, v154 op_sel_hi:[0,0,0]
	v_mfma_scale_f32_16x16x128_f8f6f4 v[206:209], v[132:139], v[80:87], v[32:35], v154, v154 op_sel_hi:[0,0,0]
	v_mfma_scale_f32_16x16x128_f8f6f4 v[210:213], v[158:165], v[80:87], v[24:27], v154, v154 op_sel_hi:[0,0,0]
	v_mfma_scale_f32_16x16x128_f8f6f4 v[222:225], v[132:139], v[88:95], v[16:19], v154, v154 op_sel_hi:[0,0,0]
	v_mfma_scale_f32_16x16x128_f8f6f4 v[226:229], v[158:165], v[88:95], v[8:11], v154, v154 op_sel_hi:[0,0,0]
	v_mfma_scale_f32_16x16x128_f8f6f4 v[52:55], v[166:173], v[64:71], v[52:55], v154, v154 op_sel_hi:[0,0,0]
	v_mfma_scale_f32_16x16x128_f8f6f4 v[230:233], v[174:181], v[64:71], v[44:47], v154, v154 op_sel_hi:[0,0,0]
	v_mfma_scale_f32_16x16x128_f8f6f4 v[234:237], v[166:173], v[72:79], v[36:39], v154, v154 op_sel_hi:[0,0,0]
	v_mfma_scale_f32_16x16x128_f8f6f4 v[238:241], v[174:181], v[72:79], v[28:31], v154, v154 op_sel_hi:[0,0,0]
	v_mfma_scale_f32_16x16x128_f8f6f4 v[242:245], v[166:173], v[80:87], v[20:23], v154, v154 op_sel_hi:[0,0,0]
	v_mfma_scale_f32_16x16x128_f8f6f4 v[246:249], v[174:181], v[80:87], v[12:15], v154, v154 op_sel_hi:[0,0,0]
	v_mfma_scale_f32_16x16x128_f8f6f4 v[250:253], v[166:173], v[88:95], v[4:7], v154, v154 op_sel_hi:[0,0,0]
	v_mfma_scale_f32_16x16x128_f8f6f4 v[128:131], v[174:181], v[88:95], v[0:3], v154, v154 op_sel_hi:[0,0,0]
	s_setprio 0
	s_barrier
; #define PG8_WAIT_V(n) asm volatile("s_waitcnt vmcnt(" #n ")" ::: "memory")
; #define PG8_WAIT_L(n) asm volatile("s_waitcnt lgkmcnt(" #n ")" ::: "memory")
; #define PG8_BAR __builtin_amdgcn_s_barrier()
; #define PG8_SCHED __builtin_amdgcn_sched_barrier(0)
; #define PG8_STAGE_A(b, h, p) do { if constexpr (GATHER) { if ((h) == 0) PG8_STAGE(PG8_SA(b, h), p, vA0); else PG8_STAGE(PG8_SA(b, h), p, vA1); } else PG8_STAGE(PG8_SA(b, h), (p) + ((h) ? hstepA : (size_t)0), voffA); } while (0)
; template <class Epi, class Sched, bool ALIGN_EPI = true, bool SP2 = true, bool FP8 = false, bool GATHER = false>
; __device__ __forceinline__ void gemm_phase(LAS unsigned char* lds, const Dims g, const Sched& S, const Epi& E, const int wv) {
;     ...
;             PG8_LDB(B0, 1, 0); PG8_LDB(B1, 1, 1); PG8_SCHED; PG8_LDA(At, 1, 0); PG8_STAGE_A(0, 1, a2);
;             PG8_WAIT_V(8); PG8_WAIT_L(0); PG8_BAR; PG8_MMA(0, 0, At, B0); PG8_MMA(0, 1, At, B1); PG8_BAR; PG8_SCHED;
;             PG8_LDA(At, 1, 1); PG8_STAGE(PG8_SB(1, 0), b3, voffB); PG8_STAGE(PG8_SB(1, 1), b3 + hstepB, voffB); PG8_STAGE_A(1, 0, a3);
;             PG8_WAIT_V(8); PG8_WAIT_L(0); PG8_BAR; PG8_MMA(1, 0, At, B0); PG8_MMA(1, 1, At, B1); PG8_BAR; PG8_SCHED;
	s_nop 4
	ds_read_b128 v[0:3], v155
	ds_read_b128 v[4:7], v155 offset:1024
	ds_read_b128 v[8:11], v155 offset:2048
	ds_read_b128 v[12:15], v155 offset:3072
	ds_read_b128 v[132:135], v156
	ds_read_b128 v[136:139], v156 offset:1024
	ds_read_b128 v[158:161], v156 offset:2048
	ds_read_b128 v[162:165], v156 offset:3072
	ds_read_b128 v[16:19], v153 offset:32768
	ds_read_b128 v[20:23], v153 offset:33792
	ds_read_b128 v[24:27], v153 offset:34816
	ds_read_b128 v[28:31], v153 offset:35840
	ds_read_b128 v[32:35], v153 offset:36864
	ds_read_b128 v[36:39], v153 offset:37888
	ds_read_b128 v[40:43], v153 offset:38912
	ds_read_b128 v[44:47], v153 offset:39936
	s_add_u32 s46, s46, 0x20000
	s_addc_u32 s47, s47, 0
	s_mov_b32 m0, s60
	s_nop 0
	global_load_lds_dwordx4 v147, s[46:47]
	s_nop 0
	s_mov_b32 m0, s61
	s_nop 0
	global_load_lds_dwordx4 v149, s[46:47]
	s_waitcnt vmcnt(8)
	s_waitcnt lgkmcnt(0)
	s_barrier
	s_setprio 1
	v_mfma_scale_f32_16x16x128_f8f6f4 v[124:127], v[0:7], v[16:23], v[124:127], v154, v154 op_sel_hi:[0,0,0]
	v_mfma_scale_f32_16x16x128_f8f6f4 v[120:123], v[8:15], v[16:23], v[120:123], v154, v154 op_sel_hi:[0,0,0]
	v_mfma_scale_f32_16x16x128_f8f6f4 v[116:119], v[0:7], v[24:31], v[116:119], v154, v154 op_sel_hi:[0,0,0]
	v_mfma_scale_f32_16x16x128_f8f6f4 v[104:107], v[8:15], v[24:31], v[104:107], v154, v154 op_sel_hi:[0,0,0]
	v_mfma_scale_f32_16x16x128_f8f6f4 v[100:103], v[0:7], v[32:39], v[100:103], v154, v154 op_sel_hi:[0,0,0]
	v_mfma_scale_f32_16x16x128_f8f6f4 v[88:91], v[8:15], v[32:39], v[140:143], v154, v154 op_sel_hi:[0,0,0]
	v_mfma_scale_f32_16x16x128_f8f6f4 v[84:87], v[0:7], v[40:47], v[214:217], v154, v154 op_sel_hi:[0,0,0]
	v_mfma_scale_f32_16x16x128_f8f6f4 v[72:75], v[8:15], v[40:47], v[218:221], v154, v154 op_sel_hi:[0,0,0]
	v_mfma_scale_f32_16x16x128_f8f6f4 v[112:115], v[132:139], v[16:23], v[112:115], v154, v154 op_sel_hi:[0,0,0]
	v_mfma_scale_f32_16x16x128_f8f6f4 v[108:111], v[158:165], v[16:23], v[108:111], v154, v154 op_sel_hi:[0,0,0]
	v_mfma_scale_f32_16x16x128_f8f6f4 v[96:99], v[132:139], v[24:31], v[96:99], v154, v154 op_sel_hi:[0,0,0]
	v_mfma_scale_f32_16x16x128_f8f6f4 v[92:95], v[158:165], v[24:31], v[182:185], v154, v154 op_sel_hi:[0,0,0]
	v_mfma_scale_f32_16x16x128_f8f6f4 v[80:83], v[132:139], v[32:39], v[186:189], v154, v154 op_sel_hi:[0,0,0]
	v_mfma_scale_f32_16x16x128_f8f6f4 v[76:79], v[158:165], v[32:39], v[190:193], v154, v154 op_sel_hi:[0,0,0]
	v_mfma_scale_f32_16x16x128_f8f6f4 v[68:71], v[132:139], v[40:47], v[194:197], v154, v154 op_sel_hi:[0,0,0]
	v_mfma_scale_f32_16x16x128_f8f6f4 v[64:67], v[158:165], v[40:47], v[198:201], v154, v154 op_sel_hi:[0,0,0]
	s_setprio 0
	s_barrier
	ds_read_b128 v[166:169], v153 offset:49152
	ds_read_b128 v[170:173], v153 offset:50176
	ds_read_b128 v[174:177], v153 offset:51200
	ds_read_b128 v[178:181], v153 offset:52224
	ds_read_b128 v[182:185], v153 offset:53248
	ds_read_b128 v[186:189], v153 offset:54272
	ds_read_b128 v[190:193], v153 offset:55296
	ds_read_b128 v[194:197], v153 offset:56320
	s_add_u32 s46, s44, 0x80
	s_addc_u32 s47, s45, 0
	s_mov_b32 m0, s66
	s_nop 0
	global_load_lds_dwordx4 v148, s[46:47]
	s_add_u32 s44, s44, 0x20080
	s_mov_b32 m0, s67
	s_nop 0
	global_load_lds_dwordx4 v150, s[46:47]
	s_addc_u32 s45, s45, 0
	s_mov_b32 m0, s70
	s_nop 0
	global_load_lds_dwordx4 v148, s[44:45]
	s_nop 0
	s_mov_b32 m0, s71
	s_nop 0
	global_load_lds_dwordx4 v150, s[44:45]
	s_mov_b32 m0, s68
	s_nop 0
	global_load_lds_dwordx4 v147, s[42:43]
	s_nop 0
	s_mov_b32 m0, s69
	s_nop 0
	global_load_lds_dwordx4 v149, s[42:43]
	s_waitcnt vmcnt(8)
	s_waitcnt lgkmcnt(0)
	s_barrier
	s_setprio 1
	v_mfma_scale_f32_16x16x128_f8f6f4 v[60:63], v[0:7], v[166:173], v[60:63], v154, v154 op_sel_hi:[0,0,0]
	v_mfma_scale_f32_16x16x128_f8f6f4 v[56:59], v[8:15], v[166:173], v[56:59], v154, v154 op_sel_hi:[0,0,0]
	v_mfma_scale_f32_16x16x128_f8f6f4 v[48:51], v[0:7], v[174:181], v[48:51], v154, v154 op_sel_hi:[0,0,0]
	v_mfma_scale_f32_16x16x128_f8f6f4 v[40:43], v[8:15], v[174:181], v[202:205], v154, v154 op_sel_hi:[0,0,0]
	v_mfma_scale_f32_16x16x128_f8f6f4 v[32:35], v[0:7], v[182:189], v[206:209], v154, v154 op_sel_hi:[0,0,0]
	v_mfma_scale_f32_16x16x128_f8f6f4 v[24:27], v[8:15], v[182:189], v[210:213], v154, v154 op_sel_hi:[0,0,0]
	v_mfma_scale_f32_16x16x128_f8f6f4 v[16:19], v[0:7], v[190:197], v[222:225], v154, v154 op_sel_hi:[0,0,0]
	v_mfma_scale_f32_16x16x128_f8f6f4 v[8:11], v[8:15], v[190:197], v[226:229], v154, v154 op_sel_hi:[0,0,0]
	v_mfma_scale_f32_16x16x128_f8f6f4 v[52:55], v[132:139], v[166:173], v[52:55], v154, v154 op_sel_hi:[0,0,0]
	v_mfma_scale_f32_16x16x128_f8f6f4 v[44:47], v[158:165], v[166:173], v[230:233], v154, v154 op_sel_hi:[0,0,0]
	v_mfma_scale_f32_16x16x128_f8f6f4 v[36:39], v[132:139], v[174:181], v[234:237], v154, v154 op_sel_hi:[0,0,0]
	v_mfma_scale_f32_16x16x128_f8f6f4 v[28:31], v[158:165], v[174:181], v[238:241], v154, v154 op_sel_hi:[0,0,0]
	v_mfma_scale_f32_16x16x128_f8f6f4 v[20:23], v[132:139], v[182:189], v[242:245], v154, v154 op_sel_hi:[0,0,0]
	v_mfma_scale_f32_16x16x128_f8f6f4 v[12:15], v[158:165], v[182:189], v[246:249], v154, v154 op_sel_hi:[0,0,0]
	v_mfma_scale_f32_16x16x128_f8f6f4 v[4:7], v[132:139], v[190:197], v[250:253], v154, v154 op_sel_hi:[0,0,0]
	v_mfma_scale_f32_16x16x128_f8f6f4 v[0:3], v[158:165], v[190:197], v[128:131], v154, v154 op_sel_hi:[0,0,0]
	s_setprio 0
	s_barrier
	s_add_i32 s82, s82, 2
	s_add_u32 s23, s23, 0x100
	s_addc_u32 s25, s25, 0
	s_add_u32 s80, s80, 0x100
	s_addc_u32 s81, s81, 0
	s_add_u32 s40, s40, 0x100
	s_addc_u32 s41, s41, 0
	s_cmp_gt_u32 s82, 5
	s_cbranch_scc0 .LBB0_3284
	s_and_b64 vcc, exec, s[8:9]
	s_cbranch_vccz .LBB0_3287
	s_barrier
